# last two MFMA groups of each K-tile deferred past the end-of-tile barrier in the in-projection, GLU and out-projection K-loops (on top of the rotation)
# speedup vs baseline: 1.0041x; 1.0008x over previous
.Lrot_ip:
	v_mfma_f32_16x16x32_bf16 v[70:73], v[202:205], v[186:189], v[70:73]
	v_mfma_f32_16x16x32_bf16 v[82:85], v[206:209], v[186:189], v[82:85]
	v_mfma_f32_16x16x32_bf16 v[86:89], v[210:213], v[186:189], v[86:89]
	v_mfma_f32_16x16x32_bf16 v[74:77], v[178:181], v[186:189], v[74:77]
	v_mfma_f32_16x16x32_bf16 v[42:45], v[202:205], v[174:177], v[42:45]
	v_mfma_f32_16x16x32_bf16 v[54:57], v[206:209], v[174:177], v[54:57]
	v_mfma_f32_16x16x32_bf16 v[58:61], v[210:213], v[174:177], v[58:61]
	v_mfma_f32_16x16x32_bf16 v[50:53], v[178:181], v[174:177], v[50:53]
	v_add_u32_e32 v204, s9, v153
	v_add_u32_e32 v206, s8, v169
	v_add_u32_e32 v212, s9, v151
	v_add_u32_e32 v208, s9, v152
.Ldef_ip_body:
	ds_read_b64_tr_b16 v[174:175], v204
	ds_read_b64_tr_b16 v[176:177], v204 offset:2048
	ds_read_b64_tr_b16 v[178:179], v208
	ds_read_b64_tr_b16 v[180:181], v208 offset:2048
	ds_read_b128 v[182:185], v206
	ds_read_b128 v[186:189], v206 offset:2048
	ds_read_b64_tr_b16 v[190:191], v212
	ds_read_b64_tr_b16 v[192:193], v212 offset:2048
	v_add_u32_e32 v214, s9, v146
	ds_read_b64_tr_b16 v[194:195], v214
	ds_read_b64_tr_b16 v[196:197], v214 offset:2048
	ds_read_b128 v[198:201], v206 offset:4096
	s_waitcnt lgkmcnt(6)
	v_mfma_f32_16x16x32_bf16 v[62:65], v[174:177], v[182:185], v[62:65]
	v_add_u32_e32 v202, 0xfff40000, v173
	s_add_i32 s9, s2, s7
	s_mov_b32 s14, m0
	s_mov_b32 m0, s9
	s_nop 0
	global_load_lds_dwordx4 v202, s[16:17]
	s_mov_b32 m0, s14
	v_mfma_f32_16x16x32_bf16 v[46:49], v[178:181], v[182:185], v[46:49]
	s_waitcnt lgkmcnt(3)
	v_mfma_f32_16x16x32_bf16 v[38:41], v[190:193], v[182:185], v[38:41]
	s_waitcnt lgkmcnt(1)
	v_mfma_f32_16x16x32_bf16 v[34:37], v[194:197], v[182:185], v[34:37]
	v_mfma_f32_16x16x32_bf16 v[30:33], v[174:177], v[186:189], v[30:33]
	ds_read_b128 v[182:185], v206 offset:6144
	v_add_u32_e32 v202, 0xfff80000, v173
	s_add_i32 s14, s9, 0x2000
	v_mfma_f32_16x16x32_bf16 v[26:29], v[178:181], v[186:189], v[26:29]
	s_mov_b32 s30, m0
	s_mov_b32 m0, s14
	s_nop 0
	global_load_lds_dwordx4 v202, s[16:17]
	s_mov_b32 m0, s30
	v_mfma_f32_16x16x32_bf16 v[22:25], v[190:193], v[186:189], v[22:25]
	v_mfma_f32_16x16x32_bf16 v[18:21], v[194:197], v[186:189], v[18:21]
	s_waitcnt lgkmcnt(1)
	v_mfma_f32_16x16x32_bf16 v[66:69], v[174:177], v[198:201], v[66:69]
	ds_read_b128 v[186:189], v206 offset:8192
	v_add_u32_e32 v202, 0xfffc0000, v173
	s_add_i32 s14, s9, 0x4000
	v_mfma_f32_16x16x32_bf16 v[78:81], v[178:181], v[198:201], v[78:81]
	s_mov_b32 s30, m0
	s_mov_b32 m0, s14
	s_nop 0
	global_load_lds_dwordx4 v202, s[16:17]
	s_mov_b32 m0, s30
	v_mfma_f32_16x16x32_bf16 v[90:93], v[190:193], v[198:201], v[90:93]
	v_mfma_f32_16x16x32_bf16 v[94:97], v[194:197], v[198:201], v[94:97]
	s_waitcnt lgkmcnt(1)
	v_mfma_f32_16x16x32_bf16 v[114:117], v[174:177], v[182:185], v[114:117]
	ds_read_b128 v[198:201], v206 offset:10240
	s_addk_i32 s9, 0x6000
	s_mov_b32 s14, m0
	s_mov_b32 m0, s9
	s_nop 0
	global_load_lds_dwordx4 v173, s[16:17]
	s_mov_b32 m0, s14
	v_mfma_f32_16x16x32_bf16 v[122:125], v[178:181], v[182:185], v[122:125]
	v_mfma_f32_16x16x32_bf16 v[138:141], v[190:193], v[182:185], v[138:141]
	v_mfma_f32_16x16x32_bf16 v[142:145], v[194:197], v[182:185], v[142:145]
	ds_read_b128 v[182:185], v206 offset:12288
	ds_read_b64_tr_b16 v[202:203], v204 offset:16384
	ds_read_b64_tr_b16 v[204:205], v204 offset:18432
	s_waitcnt lgkmcnt(4)
	v_mfma_f32_16x16x32_bf16 v[118:121], v[174:177], v[186:189], v[118:121]
	v_mfma_f32_16x16x32_bf16 v[126:129], v[178:181], v[186:189], v[126:129]
	v_mfma_f32_16x16x32_bf16 v[134:137], v[190:193], v[186:189], v[134:137]
	v_mfma_f32_16x16x32_bf16 v[130:133], v[194:197], v[186:189], v[130:133]
	ds_read_b128 v[186:189], v206 offset:14336
	ds_read_b64_tr_b16 v[206:207], v208 offset:16384
	ds_read_b64_tr_b16 v[208:209], v208 offset:18432
	s_waitcnt lgkmcnt(6)
	v_mfma_f32_16x16x32_bf16 v[98:101], v[174:177], v[198:201], v[98:101]
	v_mfma_f32_16x16x32_bf16 v[102:105], v[178:181], v[198:201], v[102:105]
	v_mfma_f32_16x16x32_bf16 v[110:113], v[190:193], v[198:201], v[110:113]
	v_mfma_f32_16x16x32_bf16 v[106:109], v[194:197], v[198:201], v[106:109]
	v_add_u32_e32 v215, s8, v171
	ds_read_b128 v[198:201], v215
	ds_read_b64_tr_b16 v[210:211], v212 offset:16384
	ds_read_b64_tr_b16 v[212:213], v212 offset:18432
	s_waitcnt lgkmcnt(8)
	v_mfma_f32_16x16x32_bf16 v[70:73], v[174:177], v[182:185], v[70:73]
	v_mfma_f32_16x16x32_bf16 v[82:85], v[178:181], v[182:185], v[82:85]
	v_mfma_f32_16x16x32_bf16 v[86:89], v[190:193], v[182:185], v[86:89]
	v_mfma_f32_16x16x32_bf16 v[74:77], v[194:197], v[182:185], v[74:77]
	s_waitcnt lgkmcnt(5)
	v_mfma_f32_16x16x32_bf16 v[42:45], v[174:177], v[186:189], v[42:45]
	ds_read_b128 v[174:177], v215 offset:2048
	s_and_b32 s8, s6, 0x8000
	v_mfma_f32_16x16x32_bf16 v[54:57], v[178:181], v[186:189], v[54:57]
	ds_read_b64_tr_b16 v[178:179], v214 offset:16384
	ds_read_b64_tr_b16 v[180:181], v214 offset:18432
	v_mfma_f32_16x16x32_bf16 v[58:61], v[190:193], v[186:189], v[58:61]
	v_mfma_f32_16x16x32_bf16 v[50:53], v[194:197], v[186:189], v[50:53]
	s_waitcnt lgkmcnt(5)
	v_mfma_f32_16x16x32_bf16 v[62:65], v[202:205], v[198:201], v[62:65]
	ds_read_b128 v[182:185], v215 offset:4096
	s_add_u32 s14, s3, s0
	s_addc_u32 s30, s4, s1
	v_mfma_f32_16x16x32_bf16 v[46:49], v[206:209], v[198:201], v[46:49]
	s_waitcnt vmcnt(7)
	v_add_u32_e32 v190, s8, v172
	s_add_u32 s8, s14, 0x100000
	s_waitcnt lgkmcnt(4)
	v_mfma_f32_16x16x32_bf16 v[38:41], v[210:213], v[198:201], v[38:41]
	ds_write_b128 v190, v[14:17]
	s_addc_u32 s9, s30, 0
	global_load_dwordx4 v[14:17], v162, s[8:9]
	s_waitcnt lgkmcnt(2)
	v_mfma_f32_16x16x32_bf16 v[34:37], v[178:181], v[198:201], v[34:37]
	v_mfma_f32_16x16x32_bf16 v[30:33], v[202:205], v[174:177], v[30:33]
	ds_read_b128 v[186:189], v215 offset:6144
	s_waitcnt vmcnt(7)
	s_add_u32 s8, s14, 0x120000
	v_mfma_f32_16x16x32_bf16 v[26:29], v[206:209], v[174:177], v[26:29]
	ds_write_b128 v190, v[10:13] offset:8192
	s_addc_u32 s9, s30, 0
	global_load_dwordx4 v[10:13], v162, s[8:9]
	v_mfma_f32_16x16x32_bf16 v[22:25], v[210:213], v[174:177], v[22:25]
	v_mfma_f32_16x16x32_bf16 v[18:21], v[178:181], v[174:177], v[18:21]
	s_waitcnt lgkmcnt(3)
	v_mfma_f32_16x16x32_bf16 v[66:69], v[202:205], v[182:185], v[66:69]
	ds_read_b128 v[174:177], v215 offset:8192
	s_waitcnt vmcnt(7)
	s_add_u32 s8, s14, 0x140000
	v_mfma_f32_16x16x32_bf16 v[78:81], v[206:209], v[182:185], v[78:81]
	ds_write_b128 v190, v[6:9] offset:16384
	s_addc_u32 s9, s30, 0
	global_load_dwordx4 v[6:9], v162, s[8:9]
	v_mfma_f32_16x16x32_bf16 v[90:93], v[210:213], v[182:185], v[90:93]
	v_mfma_f32_16x16x32_bf16 v[94:97], v[178:181], v[182:185], v[94:97]
	s_waitcnt lgkmcnt(3)
	v_mfma_f32_16x16x32_bf16 v[114:117], v[202:205], v[186:189], v[114:117]
	ds_read_b128 v[182:185], v215 offset:10240
	s_waitcnt vmcnt(7)
	s_add_u32 s8, s14, 0x160000
	v_mfma_f32_16x16x32_bf16 v[122:125], v[206:209], v[186:189], v[122:125]
	ds_write_b128 v190, v[2:5] offset:24576
	s_addc_u32 s9, s30, 0
	global_load_dwordx4 v[2:5], v162, s[8:9]
	v_mfma_f32_16x16x32_bf16 v[138:141], v[210:213], v[186:189], v[138:141]
	v_mfma_f32_16x16x32_bf16 v[142:145], v[178:181], v[186:189], v[142:145]
	s_waitcnt lgkmcnt(3)
	v_mfma_f32_16x16x32_bf16 v[118:121], v[202:205], v[174:177], v[118:121]
	ds_read_b128 v[186:189], v215 offset:12288
	v_mfma_f32_16x16x32_bf16 v[126:129], v[206:209], v[174:177], v[126:129]
	v_mfma_f32_16x16x32_bf16 v[134:137], v[210:213], v[174:177], v[134:137]
	v_mfma_f32_16x16x32_bf16 v[130:133], v[178:181], v[174:177], v[130:133]
	s_waitcnt lgkmcnt(2)
	v_mfma_f32_16x16x32_bf16 v[98:101], v[202:205], v[182:185], v[98:101]
	ds_read_b128 v[174:177], v215 offset:14336
	v_mfma_f32_16x16x32_bf16 v[102:105], v[206:209], v[182:185], v[102:105]
	v_mfma_f32_16x16x32_bf16 v[110:113], v[210:213], v[182:185], v[110:113]
	v_mfma_f32_16x16x32_bf16 v[106:109], v[178:181], v[182:185], v[106:109]
	s_waitcnt lgkmcnt(1)
	s_waitcnt lgkmcnt(0)
	s_add_i32 s8, s5, 0x8000
	s_cmp_lg_u32 s5, 0x10000
	s_cselect_b32 s5, s8, 0
	s_add_i32 s8, s7, 0x8000
	s_cmp_lg_u32 s7, 0x10000
	s_cselect_b32 s7, s8, 0
	s_add_u32 s0, s0, 0x80000
	s_addc_u32 s1, s1, 0
	s_add_i32 s6, s6, 0x8000
	v_add_u32_e32 v173, 0x80, v173
	s_add_i32 s9, s6, 0xffff8000
	s_and_b32 s9, s9, 0x8000
	s_add_i32 s9, s9, 0
	s_add_i32 s8, s5, 0
	s_add_i32 s9, s9, 0x18000
	s_waitcnt lgkmcnt(0)
	s_barrier
	s_cmp_lg_u32 s0, 0xf00000
	s_cbranch_scc1 .Lrot_ip
	v_mfma_f32_16x16x32_bf16 v[70:73], v[202:205], v[186:189], v[70:73]
	v_mfma_f32_16x16x32_bf16 v[82:85], v[206:209], v[186:189], v[82:85]
	v_mfma_f32_16x16x32_bf16 v[86:89], v[210:213], v[186:189], v[86:89]
	v_mfma_f32_16x16x32_bf16 v[74:77], v[178:181], v[186:189], v[74:77]
	v_mfma_f32_16x16x32_bf16 v[42:45], v[202:205], v[174:177], v[42:45]
	v_mfma_f32_16x16x32_bf16 v[54:57], v[206:209], v[174:177], v[54:57]
	v_mfma_f32_16x16x32_bf16 v[58:61], v[210:213], v[174:177], v[58:61]
	v_mfma_f32_16x16x32_bf16 v[50:53], v[178:181], v[174:177], v[50:53]
	s_add_i32 s0, 0, 0x18000
	v_add_u32_e32 v202, s0, v153
	v_add_u32_e32 v169, 0, v169
	v_add_u32_e32 v210, s0, v151
	v_add_u32_e32 v212, s0, v146
	ds_read_b64_tr_b16 v[172:173], v202
	ds_read_b64_tr_b16 v[174:175], v202 offset:2048
	v_add_u32_e32 v206, s0, v152
	ds_read_b128 v[176:179], v169
	ds_read_b64_tr_b16 v[180:181], v206
	ds_read_b64_tr_b16 v[182:183], v206 offset:2048
	ds_read_b128 v[184:187], v169 offset:2048
	ds_read_b64_tr_b16 v[188:189], v210
	ds_read_b64_tr_b16 v[190:191], v210 offset:2048
	ds_read_b64_tr_b16 v[192:193], v212
	ds_read_b64_tr_b16 v[194:195], v212 offset:2048
	s_waitcnt lgkmcnt(7)
	v_mfma_f32_16x16x32_bf16 v[62:65], v[172:175], v[176:179], v[62:65]
	ds_read_b128 v[196:199], v169 offset:4096
	s_waitcnt lgkmcnt(6)
	v_mfma_f32_16x16x32_bf16 v[46:49], v[180:183], v[176:179], v[46:49]
	s_waitcnt lgkmcnt(3)
	v_mfma_f32_16x16x32_bf16 v[38:41], v[188:191], v[176:179], v[38:41]
	s_waitcnt lgkmcnt(1)
	v_mfma_f32_16x16x32_bf16 v[34:37], v[192:195], v[176:179], v[34:37]
	v_mfma_f32_16x16x32_bf16 v[30:33], v[172:175], v[184:187], v[30:33]
	ds_read_b128 v[176:179], v169 offset:6144
	v_mfma_f32_16x16x32_bf16 v[26:29], v[180:183], v[184:187], v[26:29]
	v_mfma_f32_16x16x32_bf16 v[22:25], v[188:191], v[184:187], v[22:25]
	v_mfma_f32_16x16x32_bf16 v[18:21], v[192:195], v[184:187], v[18:21]
	s_waitcnt lgkmcnt(1)
	v_mfma_f32_16x16x32_bf16 v[66:69], v[172:175], v[196:199], v[66:69]
	ds_read_b128 v[184:187], v169 offset:8192
	v_mfma_f32_16x16x32_bf16 v[78:81], v[180:183], v[196:199], v[78:81]
	v_mfma_f32_16x16x32_bf16 v[90:93], v[188:191], v[196:199], v[90:93]
	v_mfma_f32_16x16x32_bf16 v[94:97], v[192:195], v[196:199], v[94:97]
	s_waitcnt lgkmcnt(1)
	v_mfma_f32_16x16x32_bf16 v[114:117], v[172:175], v[176:179], v[114:117]
	ds_read_b128 v[196:199], v169 offset:10240
	v_mfma_f32_16x16x32_bf16 v[122:125], v[180:183], v[176:179], v[122:125]
	v_mfma_f32_16x16x32_bf16 v[138:141], v[188:191], v[176:179], v[138:141]
	v_mfma_f32_16x16x32_bf16 v[142:145], v[192:195], v[176:179], v[142:145]
	ds_read_b128 v[176:179], v169 offset:12288
	ds_read_b64_tr_b16 v[200:201], v202 offset:16384
	ds_read_b64_tr_b16 v[202:203], v202 offset:18432
	s_waitcnt lgkmcnt(4)
	v_mfma_f32_16x16x32_bf16 v[118:121], v[172:175], v[184:187], v[118:121]
	v_mfma_f32_16x16x32_bf16 v[126:129], v[180:183], v[184:187], v[126:129]
	v_mfma_f32_16x16x32_bf16 v[134:137], v[188:191], v[184:187], v[134:137]
	v_mfma_f32_16x16x32_bf16 v[130:133], v[192:195], v[184:187], v[130:133]
	ds_read_b128 v[184:187], v169 offset:14336
	ds_read_b64_tr_b16 v[204:205], v206 offset:16384
	ds_read_b64_tr_b16 v[206:207], v206 offset:18432
	s_waitcnt lgkmcnt(6)
	v_mfma_f32_16x16x32_bf16 v[98:101], v[172:175], v[196:199], v[98:101]
	v_mfma_f32_16x16x32_bf16 v[102:105], v[180:183], v[196:199], v[102:105]
	v_mfma_f32_16x16x32_bf16 v[110:113], v[188:191], v[196:199], v[110:113]
	v_mfma_f32_16x16x32_bf16 v[106:109], v[192:195], v[196:199], v[106:109]
	v_add_u32_e32 v171, 0, v171
	ds_read_b128 v[196:199], v171
	ds_read_b64_tr_b16 v[208:209], v210 offset:16384
	ds_read_b64_tr_b16 v[210:211], v210 offset:18432
	s_waitcnt lgkmcnt(8)
	v_mfma_f32_16x16x32_bf16 v[70:73], v[172:175], v[176:179], v[70:73]
	v_mfma_f32_16x16x32_bf16 v[82:85], v[180:183], v[176:179], v[82:85]
	v_mfma_f32_16x16x32_bf16 v[86:89], v[188:191], v[176:179], v[86:89]
	v_mfma_f32_16x16x32_bf16 v[74:77], v[192:195], v[176:179], v[74:77]
	s_waitcnt lgkmcnt(5)
	v_mfma_f32_16x16x32_bf16 v[42:45], v[172:175], v[184:187], v[42:45]
	ds_read_b128 v[172:175], v171 offset:2048
	ds_read_b64_tr_b16 v[176:177], v212 offset:16384
	ds_read_b64_tr_b16 v[178:179], v212 offset:18432
	v_mfma_f32_16x16x32_bf16 v[54:57], v[180:183], v[184:187], v[54:57]
	v_mfma_f32_16x16x32_bf16 v[58:61], v[188:191], v[184:187], v[58:61]
	v_mfma_f32_16x16x32_bf16 v[50:53], v[192:195], v[184:187], v[50:53]
	ds_read_b128 v[180:183], v171 offset:4096
	s_waitcnt vmcnt(3)
	v_add_u32_e32 v168, s38, v168
	s_waitcnt lgkmcnt(6)
	v_mfma_f32_16x16x32_bf16 v[62:65], v[200:203], v[196:199], v[62:65]
	ds_write_b128 v168, v[14:17]
	v_mfma_f32_16x16x32_bf16 v[46:49], v[204:207], v[196:199], v[46:49]
	s_waitcnt lgkmcnt(5)
	v_mfma_f32_16x16x32_bf16 v[38:41], v[208:211], v[196:199], v[38:41]
	s_waitcnt lgkmcnt(2)
	v_mfma_f32_16x16x32_bf16 v[14:17], v[176:179], v[196:199], v[34:37]
	s_nop 2
	ds_read_b128 v[34:37], v171 offset:6144
	s_waitcnt vmcnt(2)
	v_mfma_f32_16x16x32_bf16 v[30:33], v[200:203], v[172:175], v[30:33]
	ds_write_b128 v168, v[10:13] offset:8192
	v_mfma_f32_16x16x32_bf16 v[26:29], v[204:207], v[172:175], v[26:29]
	v_mfma_f32_16x16x32_bf16 v[22:25], v[208:211], v[172:175], v[22:25]
	v_mfma_f32_16x16x32_bf16 v[10:13], v[176:179], v[172:175], v[18:21]
	s_waitcnt lgkmcnt(3)
	v_mfma_f32_16x16x32_bf16 v[18:21], v[200:203], v[180:183], v[66:69]
	v_mfma_f32_16x16x32_bf16 v[66:69], v[204:207], v[180:183], v[78:81]
	v_mfma_f32_16x16x32_bf16 v[78:81], v[208:211], v[180:183], v[90:93]
	s_nop 2
	ds_read_b128 v[90:93], v171 offset:8192
	s_waitcnt vmcnt(1)
	ds_write_b128 v168, v[6:9] offset:16384
	v_mfma_f32_16x16x32_bf16 v[6:9], v[176:179], v[180:183], v[94:97]
	s_waitcnt lgkmcnt(3)
	v_mfma_f32_16x16x32_bf16 v[94:97], v[200:203], v[34:37], v[114:117]
	v_mfma_f32_16x16x32_bf16 v[114:117], v[204:207], v[34:37], v[122:125]
	v_mfma_f32_16x16x32_bf16 v[122:125], v[208:211], v[34:37], v[138:141]
	s_nop 2
	ds_read_b128 v[138:141], v171 offset:10240
	s_waitcnt vmcnt(0)
	ds_write_b128 v168, v[2:5] offset:24576
	v_mfma_f32_16x16x32_bf16 v[2:5], v[176:179], v[34:37], v[142:145]
	s_waitcnt lgkmcnt(3)
	v_mfma_f32_16x16x32_bf16 v[34:37], v[200:203], v[90:93], v[118:121]
	v_mfma_f32_16x16x32_bf16 v[118:121], v[204:207], v[90:93], v[126:129]
	v_mfma_f32_16x16x32_bf16 v[126:129], v[208:211], v[90:93], v[134:137]
	s_nop 2
	ds_read_b128 v[134:137], v171 offset:12288
	v_mfma_f32_16x16x32_bf16 v[90:93], v[176:179], v[90:93], v[130:133]
	s_waitcnt lgkmcnt(2)
	v_mfma_f32_16x16x32_bf16 v[98:101], v[200:203], v[138:141], v[98:101]
	s_nop 0
	ds_read_b128 v[130:133], v171 offset:14336
	v_mfma_f32_16x16x32_bf16 v[102:105], v[204:207], v[138:141], v[102:105]
	v_mfma_f32_16x16x32_bf16 v[110:113], v[208:211], v[138:141], v[110:113]
	v_mfma_f32_16x16x32_bf16 v[106:109], v[176:179], v[138:141], v[106:109]
	s_waitcnt lgkmcnt(1)
	v_mfma_f32_16x16x32_bf16 v[70:73], v[200:203], v[134:137], v[70:73]
	v_mfma_f32_16x16x32_bf16 v[82:85], v[204:207], v[134:137], v[82:85]
	v_mfma_f32_16x16x32_bf16 v[86:89], v[208:211], v[134:137], v[86:89]
	v_mfma_f32_16x16x32_bf16 v[74:77], v[176:179], v[134:137], v[74:77]
	s_waitcnt lgkmcnt(0)
	v_mfma_f32_16x16x32_bf16 v[42:45], v[200:203], v[130:133], v[42:45]
	v_mfma_f32_16x16x32_bf16 v[54:57], v[204:207], v[130:133], v[54:57]
	v_mfma_f32_16x16x32_bf16 v[58:61], v[208:211], v[130:133], v[58:61]
	v_mfma_f32_16x16x32_bf16 v[50:53], v[176:179], v[130:133], v[50:53]
	s_waitcnt lgkmcnt(0)
	s_barrier
	v_add_u32_e32 v153, s38, v153
	v_add_u32_e32 v152, s38, v152
	v_add_u32_e32 v151, s38, v151
	ds_read_b64_tr_b16 v[130:131], v153
	ds_read_b64_tr_b16 v[132:133], v153 offset:2048
	ds_read_b64_tr_b16 v[134:135], v152
	ds_read_b64_tr_b16 v[136:137], v152 offset:2048
	ds_read_b128 v[138:141], v169 offset:32768
	ds_read_b64_tr_b16 v[142:143], v151
	ds_read_b128 v[172:175], v169 offset:34816
	ds_read_b128 v[176:179], v169 offset:36864
	ds_read_b64_tr_b16 v[144:145], v151 offset:2048
	v_add_u32_e32 v146, s38, v146
	ds_read_b64_tr_b16 v[180:181], v146
	ds_read_b64_tr_b16 v[182:183], v146 offset:2048
	s_waitcnt lgkmcnt(6)
	v_mfma_f32_16x16x32_bf16 v[62:65], v[130:133], v[138:141], v[62:65]
	v_mfma_f32_16x16x32_bf16 v[46:49], v[134:137], v[138:141], v[46:49]
	s_waitcnt lgkmcnt(2)
	v_mfma_f32_16x16x32_bf16 v[38:41], v[142:145], v[138:141], v[38:41]
	s_waitcnt lgkmcnt(0)
	v_mfma_f32_16x16x32_bf16 v[14:17], v[180:183], v[138:141], v[14:17]
	v_mfma_f32_16x16x32_bf16 v[30:33], v[130:133], v[172:175], v[30:33]
	ds_read_b128 v[138:141], v169 offset:38912
	v_mfma_f32_16x16x32_bf16 v[26:29], v[134:137], v[172:175], v[26:29]
	v_mfma_f32_16x16x32_bf16 v[22:25], v[142:145], v[172:175], v[22:25]
	v_mfma_f32_16x16x32_bf16 v[10:13], v[180:183], v[172:175], v[10:13]
	v_mfma_f32_16x16x32_bf16 v[18:21], v[130:133], v[176:179], v[18:21]
	ds_read_b128 v[172:175], v169 offset:40960
	v_mfma_f32_16x16x32_bf16 v[66:69], v[134:137], v[176:179], v[66:69]
	v_mfma_f32_16x16x32_bf16 v[78:81], v[142:145], v[176:179], v[78:81]
	v_mfma_f32_16x16x32_bf16 v[6:9], v[180:183], v[176:179], v[6:9]
	s_waitcnt lgkmcnt(1)
	v_mfma_f32_16x16x32_bf16 v[176:179], v[130:133], v[138:141], v[94:97]
	s_nop 2
	ds_read_b128 v[94:97], v169 offset:43008
	v_mfma_f32_16x16x32_bf16 v[2:5], v[180:183], v[138:141], v[2:5]
	v_mfma_f32_16x16x32_bf16 v[184:187], v[134:137], v[138:141], v[114:117]
	v_mfma_f32_16x16x32_bf16 v[188:191], v[142:145], v[138:141], v[122:125]
	s_nop 1
	ds_read_b128 v[114:117], v169 offset:45056
	ds_read_b64_tr_b16 v[196:197], v153 offset:16384
	ds_read_b64_tr_b16 v[198:199], v153 offset:18432
	s_waitcnt lgkmcnt(4)
	v_mfma_f32_16x16x32_bf16 v[34:37], v[130:133], v[172:175], v[34:37]
	v_mfma_f32_16x16x32_bf16 v[138:141], v[134:137], v[172:175], v[118:121]
	v_mfma_f32_16x16x32_bf16 v[192:195], v[142:145], v[172:175], v[126:129]
	v_mfma_f32_16x16x32_bf16 v[172:175], v[180:183], v[172:175], v[90:93]
	s_nop 2
	ds_read_b128 v[90:93], v169 offset:47104
	ds_read_b64_tr_b16 v[212:213], v152 offset:16384
	ds_read_b64_tr_b16 v[214:215], v152 offset:18432
	s_waitcnt lgkmcnt(6)
	v_mfma_f32_16x16x32_bf16 v[200:203], v[130:133], v[94:97], v[98:101]
	v_mfma_f32_16x16x32_bf16 v[204:207], v[134:137], v[94:97], v[102:105]
	v_mfma_f32_16x16x32_bf16 v[208:211], v[142:145], v[94:97], v[110:113]
	v_mfma_f32_16x16x32_bf16 v[216:219], v[180:183], v[94:97], v[106:109]
	s_waitcnt lgkmcnt(5)
	v_mfma_f32_16x16x32_bf16 v[220:223], v[130:133], v[114:117], v[70:73]
	s_nop 2
	ds_read_b128 v[70:73], v171 offset:32768
	ds_read_b64_tr_b16 v[232:233], v151 offset:16384
	ds_read_b64_tr_b16 v[234:235], v151 offset:18432
	v_mfma_f32_16x16x32_bf16 v[224:227], v[134:137], v[114:117], v[82:85]
	v_mfma_f32_16x16x32_bf16 v[228:231], v[142:145], v[114:117], v[86:89]
	v_mfma_f32_16x16x32_bf16 v[236:239], v[180:183], v[114:117], v[74:77]
	s_waitcnt lgkmcnt(5)
	v_mfma_f32_16x16x32_bf16 v[130:133], v[130:133], v[90:93], v[42:45]
	s_nop 2
	ds_read_b128 v[42:45], v171 offset:34816
	ds_read_b64_tr_b16 v[240:241], v146 offset:16384
	ds_read_b64_tr_b16 v[242:243], v146 offset:18432
	v_mfma_f32_16x16x32_bf16 v[134:137], v[134:137], v[90:93], v[54:57]
	v_mfma_f32_16x16x32_bf16 v[142:145], v[142:145], v[90:93], v[58:61]
	v_mfma_f32_16x16x32_bf16 v[180:183], v[180:183], v[90:93], v[50:53]
	s_waitcnt lgkmcnt(3)
	v_mfma_f32_16x16x32_bf16 v[118:121], v[232:235], v[70:73], v[38:41]
	s_nop 2
	ds_read_b128 v[38:41], v171 offset:36864
	v_mfma_f32_16x16x32_bf16 v[126:129], v[196:199], v[70:73], v[62:65]
	v_mfma_f32_16x16x32_bf16 v[122:125], v[212:215], v[70:73], v[46:49]
	s_waitcnt lgkmcnt(1)
	v_mfma_f32_16x16x32_bf16 v[114:117], v[240:243], v[70:73], v[14:17]
	s_nop 2
	ds_read_b128 v[14:17], v171 offset:38912
	v_mfma_f32_16x16x32_bf16 v[110:113], v[196:199], v[42:45], v[30:33]
	v_mfma_f32_16x16x32_bf16 v[106:109], v[212:215], v[42:45], v[26:29]
	v_mfma_f32_16x16x32_bf16 v[102:105], v[232:235], v[42:45], v[22:25]
	v_mfma_f32_16x16x32_bf16 v[98:101], v[240:243], v[42:45], v[10:13]
	s_nop 2
	ds_read_b128 v[10:13], v171 offset:40960
	s_waitcnt lgkmcnt(2)
	v_mfma_f32_16x16x32_bf16 v[94:97], v[196:199], v[38:41], v[18:21]
	v_mfma_f32_16x16x32_bf16 v[90:93], v[212:215], v[38:41], v[66:69]
	v_mfma_f32_16x16x32_bf16 v[86:89], v[232:235], v[38:41], v[78:81]
	v_mfma_f32_16x16x32_bf16 v[82:85], v[240:243], v[38:41], v[6:9]
	s_nop 2
	ds_read_b128 v[6:9], v171 offset:43008
	s_waitcnt lgkmcnt(2)
	v_mfma_f32_16x16x32_bf16 v[78:81], v[196:199], v[14:17], v[176:179]
	v_mfma_f32_16x16x32_bf16 v[74:77], v[212:215], v[14:17], v[184:187]
	v_mfma_f32_16x16x32_bf16 v[70:73], v[232:235], v[14:17], v[188:191]
	v_mfma_f32_16x16x32_bf16 v[66:69], v[240:243], v[14:17], v[2:5]
	s_nop 2
	ds_read_b128 v[2:5], v171 offset:45056
	s_waitcnt lgkmcnt(2)
	v_mfma_f32_16x16x32_bf16 v[62:65], v[196:199], v[10:13], v[34:37]
	v_mfma_f32_16x16x32_bf16 v[58:61], v[212:215], v[10:13], v[138:141]
	v_mfma_f32_16x16x32_bf16 v[54:57], v[232:235], v[10:13], v[192:195]
	v_mfma_f32_16x16x32_bf16 v[50:53], v[240:243], v[10:13], v[172:175]
	s_waitcnt lgkmcnt(1)
	v_mfma_f32_16x16x32_bf16 v[46:49], v[196:199], v[6:9], v[200:203]
	ds_read_b128 v[138:141], v171 offset:47104
	v_mfma_f32_16x16x32_bf16 v[42:45], v[212:215], v[6:9], v[204:207]
	v_mfma_f32_16x16x32_bf16 v[38:41], v[232:235], v[6:9], v[208:211]
	v_mfma_f32_16x16x32_bf16 v[34:37], v[240:243], v[6:9], v[216:219]
	s_waitcnt lgkmcnt(1)
	v_mfma_f32_16x16x32_bf16 v[30:33], v[196:199], v[2:5], v[220:223]
	v_mfma_f32_16x16x32_bf16 v[26:29], v[212:215], v[2:5], v[224:227]
	v_mfma_f32_16x16x32_bf16 v[22:25], v[232:235], v[2:5], v[228:231]
	v_mfma_f32_16x16x32_bf16 v[18:21], v[240:243], v[2:5], v[236:239]
	s_waitcnt lgkmcnt(0)
	v_mfma_f32_16x16x32_bf16 v[14:17], v[196:199], v[138:141], v[130:133]
	v_mfma_f32_16x16x32_bf16 v[10:13], v[212:215], v[138:141], v[134:137]
	v_mfma_f32_16x16x32_bf16 v[6:9], v[232:235], v[138:141], v[142:145]
	v_mfma_f32_16x16x32_bf16 v[2:5], v[240:243], v[138:141], v[180:183]
	s_waitcnt lgkmcnt(0)
	s_barrier
	v_mov_b32_e32 v151, v155
	v_mov_b32_e32 v168, v1
	s_cmpk_gt_i32 s28, 0x3ff
	s_mov_b64 s[0:1], -1
	s_cbranch_scc1 .LBB0_607
	s_add_i32 s0, s52, s50
	v_add_u32_e32 v140, s0, v168
	s_lshl_b32 s0, s51, 6
	s_or_b32 s0, s0, s28
	v_lshlrev_b32_e32 v132, 2, v151
	v_add_u32_e32 v146, s0, v132
	v_ashrrev_i32_e32 v141, 31, v140
	v_lshlrev_b64 v[142:143], 11, v[140:141]
	v_cmp_lt_i32_e64 s[4:5], s39, v146
	s_and_saveexec_b64 s[0:1], s[4:5]
	s_xor_b64 s[0:1], exec, s[0:1]
	s_cbranch_execz .LBB0_442
	v_cmp_lt_u32_e32 vcc, s41, v146
	s_and_saveexec_b64 s[2:3], vcc
	s_xor_b64 s[2:3], exec, s[2:3]
	s_cbranch_execz .LBB0_439
	v_cmp_lt_u32_e32 vcc, s42, v146
	v_cvt_pk_bf16_f32 v130, v126, v127
	v_cvt_pk_bf16_f32 v131, v128, v129
	s_and_saveexec_b64 s[6:7], vcc
	s_xor_b64 s[6:7], exec, s[6:7]
	s_cbranch_execz .LBB0_436
	v_lshl_add_u64 v[134:135], s[24:25], 0, v[142:143]
	v_lshl_add_u64 v[134:135], v[146:147], 1, v[134:135]
	v_add_co_u32_e32 v134, vcc, 0xfffff000, v134
	s_nop 1
	v_addc_co_u32_e32 v135, vcc, -1, v135, vcc
	global_store_dwordx2 v[134:135], v[130:131], off offset:-2048

.Lrot_gl:
	v_mfma_f32_16x16x32_bf16 v[70:73], v[192:195], v[176:179], v[70:73]
	v_mfma_f32_16x16x32_bf16 v[82:85], v[196:199], v[176:179], v[82:85]
	v_mfma_f32_16x16x32_bf16 v[86:89], v[216:219], v[176:179], v[86:89]
	v_mfma_f32_16x16x32_bf16 v[74:77], v[164:167], v[176:179], v[74:77]
	v_mfma_f32_16x16x32_bf16 v[46:49], v[192:195], v[160:163], v[46:49]
	v_mfma_f32_16x16x32_bf16 v[58:61], v[196:199], v[160:163], v[58:61]
	v_mfma_f32_16x16x32_bf16 v[62:65], v[216:219], v[160:163], v[62:65]
	v_mfma_f32_16x16x32_bf16 v[50:53], v[164:167], v[160:163], v[50:53]
.Ldef_gl_body:
	ds_read_b64_tr_b16 v[160:161], v157
	ds_read_b64_tr_b16 v[162:163], v157 offset:2048
	ds_read_b64_tr_b16 v[164:165], v168
	ds_read_b64_tr_b16 v[166:167], v168 offset:2048
	ds_read_b128 v[172:175], v169
	ds_read_b128 v[176:179], v169 offset:2048
	ds_read_b64_tr_b16 v[180:181], v200
	ds_read_b64_tr_b16 v[182:183], v200 offset:2048
	v_add_u32_e32 v201, s34, v148
	ds_read_b64_tr_b16 v[184:185], v201
	ds_read_b64_tr_b16 v[186:187], v201 offset:2048
	ds_read_b128 v[188:191], v169 offset:4096
	s_waitcnt lgkmcnt(6)
	v_mfma_f32_16x16x32_bf16 v[18:21], v[160:163], v[172:175], v[18:21]
	v_add_u32_e32 v192, 0xfffa0000, v156
	s_add_i32 s34, s27, s31
	s_mov_b32 s35, m0
	s_mov_b32 m0, s34
	s_nop 0
	global_load_lds_dwordx4 v192, s[6:7]
	s_mov_b32 m0, s35
	v_mfma_f32_16x16x32_bf16 v[22:25], v[164:167], v[172:175], v[22:25]
	s_waitcnt lgkmcnt(3)
	v_mfma_f32_16x16x32_bf16 v[26:29], v[180:183], v[172:175], v[26:29]
	s_waitcnt lgkmcnt(1)
	v_mfma_f32_16x16x32_bf16 v[30:33], v[184:187], v[172:175], v[30:33]
	v_mfma_f32_16x16x32_bf16 v[34:37], v[160:163], v[176:179], v[34:37]
	ds_read_b128 v[172:175], v169 offset:6144
	v_add_u32_e32 v192, 0xfffc0000, v156
	s_add_i32 s35, s34, 0x2000
	v_mfma_f32_16x16x32_bf16 v[38:41], v[164:167], v[176:179], v[38:41]
	s_mov_b32 s36, m0
	s_mov_b32 m0, s35
	s_nop 0
	global_load_lds_dwordx4 v192, s[6:7]
	s_mov_b32 m0, s36
	v_mfma_f32_16x16x32_bf16 v[42:45], v[180:183], v[176:179], v[42:45]
	v_mfma_f32_16x16x32_bf16 v[54:57], v[184:187], v[176:179], v[54:57]
	s_waitcnt lgkmcnt(1)
	v_mfma_f32_16x16x32_bf16 v[66:69], v[160:163], v[188:191], v[66:69]
	ds_read_b128 v[176:179], v169 offset:8192
	v_add_u32_e32 v192, 0xfffe0000, v156
	s_add_i32 s35, s34, 0x4000
	v_mfma_f32_16x16x32_bf16 v[78:81], v[164:167], v[188:191], v[78:81]
	s_mov_b32 s36, m0
	s_mov_b32 m0, s35
	s_nop 0
	global_load_lds_dwordx4 v192, s[6:7]
	s_mov_b32 m0, s36
	v_mfma_f32_16x16x32_bf16 v[90:93], v[180:183], v[188:191], v[90:93]
	v_mfma_f32_16x16x32_bf16 v[94:97], v[184:187], v[188:191], v[94:97]
	s_waitcnt lgkmcnt(1)
	v_mfma_f32_16x16x32_bf16 v[114:117], v[160:163], v[172:175], v[114:117]
	ds_read_b128 v[188:191], v169 offset:10240
	s_addk_i32 s34, 0x6000
	s_mov_b32 s35, m0
	s_mov_b32 m0, s34
	s_nop 0
	global_load_lds_dwordx4 v156, s[6:7]
	s_mov_b32 m0, s35
	v_mfma_f32_16x16x32_bf16 v[122:125], v[164:167], v[172:175], v[122:125]
	v_mfma_f32_16x16x32_bf16 v[138:141], v[180:183], v[172:175], v[138:141]
	v_mfma_f32_16x16x32_bf16 v[142:145], v[184:187], v[172:175], v[142:145]
	ds_read_b128 v[172:175], v169 offset:12288
	ds_read_b64_tr_b16 v[192:193], v157 offset:16384
	ds_read_b64_tr_b16 v[194:195], v157 offset:18432
	s_waitcnt lgkmcnt(4)
	v_mfma_f32_16x16x32_bf16 v[118:121], v[160:163], v[176:179], v[118:121]
	v_mfma_f32_16x16x32_bf16 v[126:129], v[164:167], v[176:179], v[126:129]
	v_mfma_f32_16x16x32_bf16 v[134:137], v[180:183], v[176:179], v[134:137]
	v_mfma_f32_16x16x32_bf16 v[130:133], v[184:187], v[176:179], v[130:133]
	ds_read_b128 v[176:179], v169 offset:14336
	ds_read_b64_tr_b16 v[196:197], v168 offset:16384
	ds_read_b64_tr_b16 v[198:199], v168 offset:18432
	s_waitcnt lgkmcnt(6)
	v_mfma_f32_16x16x32_bf16 v[98:101], v[160:163], v[188:191], v[98:101]
	v_mfma_f32_16x16x32_bf16 v[102:105], v[164:167], v[188:191], v[102:105]
	v_mfma_f32_16x16x32_bf16 v[110:113], v[180:183], v[188:191], v[110:113]
	v_mfma_f32_16x16x32_bf16 v[106:109], v[184:187], v[188:191], v[106:109]
	v_add_u32_e32 v157, s33, v153
	ds_read_b128 v[188:191], v157
	ds_read_b64_tr_b16 v[216:217], v200 offset:16384
	ds_read_b64_tr_b16 v[218:219], v200 offset:18432
	s_waitcnt lgkmcnt(8)
	v_mfma_f32_16x16x32_bf16 v[70:73], v[160:163], v[172:175], v[70:73]
	v_mfma_f32_16x16x32_bf16 v[82:85], v[164:167], v[172:175], v[82:85]
	v_mfma_f32_16x16x32_bf16 v[86:89], v[180:183], v[172:175], v[86:89]
	v_mfma_f32_16x16x32_bf16 v[74:77], v[184:187], v[172:175], v[74:77]
	s_waitcnt lgkmcnt(5)
	v_mfma_f32_16x16x32_bf16 v[46:49], v[160:163], v[176:179], v[46:49]
	ds_read_b128 v[160:163], v157 offset:2048
	s_and_b32 s33, s29, 0x8000
	v_mfma_f32_16x16x32_bf16 v[58:61], v[164:167], v[176:179], v[58:61]
	ds_read_b64_tr_b16 v[164:165], v201 offset:16384
	ds_read_b64_tr_b16 v[166:167], v201 offset:18432
	v_mfma_f32_16x16x32_bf16 v[62:65], v[180:183], v[176:179], v[62:65]
	v_mfma_f32_16x16x32_bf16 v[50:53], v[184:187], v[176:179], v[50:53]
	s_waitcnt lgkmcnt(5)
	v_mfma_f32_16x16x32_bf16 v[18:21], v[192:195], v[188:191], v[18:21]
	ds_read_b128 v[172:175], v157 offset:4096
	v_add_u32_e32 v168, s33, v155
	s_add_u32 s33, s2, s0
	v_mfma_f32_16x16x32_bf16 v[22:25], v[196:199], v[188:191], v[22:25]
	s_addc_u32 s36, s28, s1
	s_waitcnt vmcnt(7)
	s_add_u32 s34, s33, 0x40000
	s_waitcnt lgkmcnt(4)
	v_mfma_f32_16x16x32_bf16 v[26:29], v[216:219], v[188:191], v[26:29]
	ds_write_b128 v168, v[14:17]
	s_addc_u32 s35, s36, 0
	global_load_dwordx4 v[14:17], v208, s[34:35]
	s_waitcnt lgkmcnt(2)
	v_mfma_f32_16x16x32_bf16 v[30:33], v[164:167], v[188:191], v[30:33]
	v_mfma_f32_16x16x32_bf16 v[34:37], v[192:195], v[160:163], v[34:37]
	ds_read_b128 v[176:179], v157 offset:6144
	s_waitcnt vmcnt(7)
	s_add_u32 s34, s33, 0x48000
	v_mfma_f32_16x16x32_bf16 v[38:41], v[196:199], v[160:163], v[38:41]
	ds_write_b128 v168, v[10:13] offset:8192
	s_addc_u32 s35, s36, 0
	global_load_dwordx4 v[10:13], v208, s[34:35]
	v_mfma_f32_16x16x32_bf16 v[42:45], v[216:219], v[160:163], v[42:45]
	v_mfma_f32_16x16x32_bf16 v[54:57], v[164:167], v[160:163], v[54:57]
	s_waitcnt lgkmcnt(3)
	v_mfma_f32_16x16x32_bf16 v[66:69], v[192:195], v[172:175], v[66:69]
	ds_read_b128 v[160:163], v157 offset:8192
	s_waitcnt vmcnt(7)
	s_add_u32 s34, s33, 0x50000
	v_mfma_f32_16x16x32_bf16 v[78:81], v[196:199], v[172:175], v[78:81]
	ds_write_b128 v168, v[6:9] offset:16384
	s_addc_u32 s35, s36, 0
	global_load_dwordx4 v[6:9], v208, s[34:35]
	v_mfma_f32_16x16x32_bf16 v[90:93], v[216:219], v[172:175], v[90:93]
	v_mfma_f32_16x16x32_bf16 v[94:97], v[164:167], v[172:175], v[94:97]
	s_waitcnt lgkmcnt(3)
	v_mfma_f32_16x16x32_bf16 v[114:117], v[192:195], v[176:179], v[114:117]
	ds_read_b128 v[172:175], v157 offset:10240
	s_waitcnt vmcnt(7)
	s_add_u32 s34, s33, 0x58000
	v_mfma_f32_16x16x32_bf16 v[122:125], v[196:199], v[176:179], v[122:125]
	ds_write_b128 v168, v[2:5] offset:24576
	s_addc_u32 s35, s36, 0
	global_load_dwordx4 v[2:5], v208, s[34:35]
	v_mfma_f32_16x16x32_bf16 v[138:141], v[216:219], v[176:179], v[138:141]
	v_mfma_f32_16x16x32_bf16 v[142:145], v[164:167], v[176:179], v[142:145]
	s_waitcnt lgkmcnt(3)
	v_mfma_f32_16x16x32_bf16 v[118:121], v[192:195], v[160:163], v[118:121]
	ds_read_b128 v[176:179], v157 offset:12288
	v_mfma_f32_16x16x32_bf16 v[126:129], v[196:199], v[160:163], v[126:129]
	v_mfma_f32_16x16x32_bf16 v[134:137], v[216:219], v[160:163], v[134:137]
	v_mfma_f32_16x16x32_bf16 v[130:133], v[164:167], v[160:163], v[130:133]
	s_waitcnt lgkmcnt(2)
	v_mfma_f32_16x16x32_bf16 v[98:101], v[192:195], v[172:175], v[98:101]
	ds_read_b128 v[160:163], v157 offset:14336
	v_mfma_f32_16x16x32_bf16 v[102:105], v[196:199], v[172:175], v[102:105]
	v_mfma_f32_16x16x32_bf16 v[110:113], v[216:219], v[172:175], v[110:113]
	v_mfma_f32_16x16x32_bf16 v[106:109], v[164:167], v[172:175], v[106:109]
	s_waitcnt lgkmcnt(1)
	s_waitcnt lgkmcnt(0)
	s_add_i32 s33, s30, 0x8000
	s_cmp_lg_u32 s30, 0x10000
	s_cselect_b32 s30, s33, 0
	s_add_i32 s33, s31, 0x8000
	s_cmp_lg_u32 s31, 0x10000
	s_cselect_b32 s31, s33, 0
	s_add_u32 s0, s0, 0x20000
	s_addc_u32 s1, s1, 0
	s_add_i32 s29, s29, 0x8000
	v_add_u32_e32 v156, 0x80, v156
	s_add_i32 s34, s29, 0xffff8000
	s_and_b32 s34, s34, 0x8000
	s_add_i32 s34, s34, 0
	s_add_i32 s33, s30, 0
	s_add_i32 s34, s34, 0x18000
	v_add_u32_e32 v157, s34, v152
	v_add_u32_e32 v169, s33, v150
	v_add_u32_e32 v200, s34, v149
	v_add_u32_e32 v168, s34, v151
	s_waitcnt lgkmcnt(0)
	s_barrier
	s_cmp_lg_u32 s0, 0x1c0000
	s_cbranch_scc1 .Lrot_gl
	v_mfma_f32_16x16x32_bf16 v[70:73], v[192:195], v[176:179], v[70:73]
	v_mfma_f32_16x16x32_bf16 v[82:85], v[196:199], v[176:179], v[82:85]
	v_mfma_f32_16x16x32_bf16 v[86:89], v[216:219], v[176:179], v[86:89]
	v_mfma_f32_16x16x32_bf16 v[74:77], v[164:167], v[176:179], v[74:77]
	v_mfma_f32_16x16x32_bf16 v[46:49], v[192:195], v[160:163], v[46:49]
	v_mfma_f32_16x16x32_bf16 v[58:61], v[196:199], v[160:163], v[58:61]
	v_mfma_f32_16x16x32_bf16 v[62:65], v[216:219], v[160:163], v[62:65]
	v_mfma_f32_16x16x32_bf16 v[50:53], v[164:167], v[160:163], v[50:53]
	s_add_i32 s0, 0, 0x18000
	s_add_i32 s1, 0, 0x10000
	v_add_u32_e32 v155, s0, v152
	v_add_u32_e32 v157, s1, v150
	v_add_u32_e32 v168, s0, v149
	v_add_u32_e32 v169, s0, v148
	v_add_u32_e32 v156, s0, v151
	ds_read_b64_tr_b16 v[160:161], v155
	ds_read_b64_tr_b16 v[162:163], v155 offset:2048
	ds_read_b64_tr_b16 v[164:165], v156
	ds_read_b64_tr_b16 v[166:167], v156 offset:2048
	ds_read_b128 v[172:175], v157
	ds_read_b128 v[176:179], v157 offset:2048
	ds_read_b64_tr_b16 v[180:181], v168
	ds_read_b64_tr_b16 v[182:183], v168 offset:2048
	ds_read_b64_tr_b16 v[184:185], v169
	ds_read_b64_tr_b16 v[186:187], v169 offset:2048
	ds_read_b128 v[188:191], v157 offset:4096
	s_waitcnt lgkmcnt(6)
	v_mfma_f32_16x16x32_bf16 v[18:21], v[160:163], v[172:175], v[18:21]
	v_mfma_f32_16x16x32_bf16 v[22:25], v[164:167], v[172:175], v[22:25]
	s_waitcnt lgkmcnt(3)
	v_mfma_f32_16x16x32_bf16 v[26:29], v[180:183], v[172:175], v[26:29]
	s_waitcnt lgkmcnt(1)
	v_mfma_f32_16x16x32_bf16 v[30:33], v[184:187], v[172:175], v[30:33]
	ds_read_b128 v[172:175], v157 offset:6144
	v_mfma_f32_16x16x32_bf16 v[34:37], v[160:163], v[176:179], v[34:37]
	v_mfma_f32_16x16x32_bf16 v[38:41], v[164:167], v[176:179], v[38:41]
	v_mfma_f32_16x16x32_bf16 v[42:45], v[180:183], v[176:179], v[42:45]
	v_mfma_f32_16x16x32_bf16 v[54:57], v[184:187], v[176:179], v[54:57]
	ds_read_b128 v[176:179], v157 offset:8192
	s_waitcnt lgkmcnt(2)
	v_mfma_f32_16x16x32_bf16 v[66:69], v[160:163], v[188:191], v[66:69]
	v_mfma_f32_16x16x32_bf16 v[78:81], v[164:167], v[188:191], v[78:81]
	v_mfma_f32_16x16x32_bf16 v[90:93], v[180:183], v[188:191], v[90:93]
	v_mfma_f32_16x16x32_bf16 v[94:97], v[184:187], v[188:191], v[94:97]
	ds_read_b128 v[188:191], v157 offset:10240
	s_waitcnt lgkmcnt(2)
	v_mfma_f32_16x16x32_bf16 v[114:117], v[160:163], v[172:175], v[114:117]
	v_mfma_f32_16x16x32_bf16 v[122:125], v[164:167], v[172:175], v[122:125]
	v_mfma_f32_16x16x32_bf16 v[138:141], v[180:183], v[172:175], v[138:141]
	v_mfma_f32_16x16x32_bf16 v[142:145], v[184:187], v[172:175], v[142:145]
	ds_read_b128 v[172:175], v157 offset:12288
	ds_read_b64_tr_b16 v[192:193], v155 offset:16384
	ds_read_b64_tr_b16 v[194:195], v155 offset:18432
	s_waitcnt lgkmcnt(4)
	v_mfma_f32_16x16x32_bf16 v[118:121], v[160:163], v[176:179], v[118:121]
	v_mfma_f32_16x16x32_bf16 v[126:129], v[164:167], v[176:179], v[126:129]
	v_mfma_f32_16x16x32_bf16 v[134:137], v[180:183], v[176:179], v[134:137]
	v_mfma_f32_16x16x32_bf16 v[130:133], v[184:187], v[176:179], v[130:133]
	ds_read_b128 v[176:179], v157 offset:14336
	ds_read_b64_tr_b16 v[196:197], v156 offset:16384
	ds_read_b64_tr_b16 v[198:199], v156 offset:18432
	s_waitcnt lgkmcnt(6)
	v_mfma_f32_16x16x32_bf16 v[98:101], v[160:163], v[188:191], v[98:101]
	v_mfma_f32_16x16x32_bf16 v[102:105], v[164:167], v[188:191], v[102:105]
	v_mfma_f32_16x16x32_bf16 v[110:113], v[180:183], v[188:191], v[110:113]
	v_mfma_f32_16x16x32_bf16 v[106:109], v[184:187], v[188:191], v[106:109]
	v_add_u32_e32 v155, s1, v153
	ds_read_b128 v[188:191], v155
	ds_read_b64_tr_b16 v[216:217], v168 offset:16384
	ds_read_b64_tr_b16 v[218:219], v168 offset:18432
	s_waitcnt lgkmcnt(8)
	v_mfma_f32_16x16x32_bf16 v[70:73], v[160:163], v[172:175], v[70:73]
	v_mfma_f32_16x16x32_bf16 v[82:85], v[164:167], v[172:175], v[82:85]
	v_mfma_f32_16x16x32_bf16 v[86:89], v[180:183], v[172:175], v[86:89]
	v_mfma_f32_16x16x32_bf16 v[74:77], v[184:187], v[172:175], v[74:77]
	s_waitcnt lgkmcnt(5)
	v_mfma_f32_16x16x32_bf16 v[46:49], v[160:163], v[176:179], v[46:49]
	v_mfma_f32_16x16x32_bf16 v[58:61], v[164:167], v[176:179], v[58:61]
	ds_read_b128 v[160:163], v155 offset:2048
	ds_read_b64_tr_b16 v[164:165], v169 offset:16384
	ds_read_b64_tr_b16 v[166:167], v169 offset:18432
	v_mfma_f32_16x16x32_bf16 v[62:65], v[180:183], v[176:179], v[62:65]
	v_mfma_f32_16x16x32_bf16 v[50:53], v[184:187], v[176:179], v[50:53]
	ds_read_b128 v[172:175], v155 offset:4096
	s_add_i32 s0, 0, 0x20000
	s_waitcnt vmcnt(3)
	v_add_u32_e32 v154, s0, v154
	s_waitcnt lgkmcnt(6)
	v_mfma_f32_16x16x32_bf16 v[18:21], v[192:195], v[188:191], v[18:21]
	ds_write_b128 v154, v[14:17]
	v_mfma_f32_16x16x32_bf16 v[22:25], v[196:199], v[188:191], v[22:25]
	s_waitcnt lgkmcnt(5)
	v_mfma_f32_16x16x32_bf16 v[26:29], v[216:219], v[188:191], v[26:29]
	s_waitcnt lgkmcnt(2)
	v_mfma_f32_16x16x32_bf16 v[14:17], v[164:167], v[188:191], v[30:33]
	v_mfma_f32_16x16x32_bf16 v[30:33], v[192:195], v[160:163], v[34:37]
	v_mfma_f32_16x16x32_bf16 v[34:37], v[196:199], v[160:163], v[38:41]
	v_mfma_f32_16x16x32_bf16 v[38:41], v[216:219], v[160:163], v[42:45]
	s_nop 2
	ds_read_b128 v[42:45], v155 offset:6144
	s_waitcnt vmcnt(2)
	ds_write_b128 v154, v[10:13] offset:8192
	v_mfma_f32_16x16x32_bf16 v[10:13], v[164:167], v[160:163], v[54:57]
	s_waitcnt lgkmcnt(3)
	v_mfma_f32_16x16x32_bf16 v[54:57], v[192:195], v[172:175], v[66:69]
	v_mfma_f32_16x16x32_bf16 v[66:69], v[196:199], v[172:175], v[78:81]
	v_mfma_f32_16x16x32_bf16 v[78:81], v[216:219], v[172:175], v[90:93]
	s_nop 2
	ds_read_b128 v[90:93], v155 offset:8192
	s_waitcnt vmcnt(1)
	ds_write_b128 v154, v[6:9] offset:16384
	v_mfma_f32_16x16x32_bf16 v[6:9], v[164:167], v[172:175], v[94:97]
	s_waitcnt lgkmcnt(3)
	v_mfma_f32_16x16x32_bf16 v[94:97], v[192:195], v[42:45], v[114:117]
	v_mfma_f32_16x16x32_bf16 v[114:117], v[196:199], v[42:45], v[122:125]
	v_mfma_f32_16x16x32_bf16 v[122:125], v[216:219], v[42:45], v[138:141]
	s_nop 2
	ds_read_b128 v[138:141], v155 offset:10240
	s_waitcnt vmcnt(0)
	ds_write_b128 v154, v[2:5] offset:24576
	v_mfma_f32_16x16x32_bf16 v[2:5], v[164:167], v[42:45], v[142:145]
	s_waitcnt lgkmcnt(3)
	v_mfma_f32_16x16x32_bf16 v[42:45], v[192:195], v[90:93], v[118:121]
	v_mfma_f32_16x16x32_bf16 v[118:121], v[196:199], v[90:93], v[126:129]
	v_mfma_f32_16x16x32_bf16 v[126:129], v[216:219], v[90:93], v[134:137]
	s_nop 2
	ds_read_b128 v[134:137], v155 offset:12288
	v_mfma_f32_16x16x32_bf16 v[90:93], v[164:167], v[90:93], v[130:133]
	s_nop 2
	ds_read_b128 v[130:133], v155 offset:14336
	s_waitcnt lgkmcnt(3)
	v_mfma_f32_16x16x32_bf16 v[98:101], v[192:195], v[138:141], v[98:101]
	v_mfma_f32_16x16x32_bf16 v[102:105], v[196:199], v[138:141], v[102:105]
	v_mfma_f32_16x16x32_bf16 v[110:113], v[216:219], v[138:141], v[110:113]
	v_mfma_f32_16x16x32_bf16 v[106:109], v[164:167], v[138:141], v[106:109]
	s_waitcnt lgkmcnt(1)
	v_mfma_f32_16x16x32_bf16 v[70:73], v[192:195], v[134:137], v[70:73]
	v_mfma_f32_16x16x32_bf16 v[82:85], v[196:199], v[134:137], v[82:85]
	v_mfma_f32_16x16x32_bf16 v[86:89], v[216:219], v[134:137], v[86:89]
	v_mfma_f32_16x16x32_bf16 v[74:77], v[164:167], v[134:137], v[74:77]
	s_waitcnt lgkmcnt(0)
	v_mfma_f32_16x16x32_bf16 v[46:49], v[192:195], v[130:133], v[46:49]
	v_mfma_f32_16x16x32_bf16 v[58:61], v[196:199], v[130:133], v[58:61]
	v_mfma_f32_16x16x32_bf16 v[62:65], v[216:219], v[130:133], v[62:65]
	v_mfma_f32_16x16x32_bf16 v[50:53], v[164:167], v[130:133], v[50:53]
	s_waitcnt lgkmcnt(0)
	s_barrier
	v_add_u32_e32 v152, s0, v152
	v_add_u32_e32 v169, 0, v150
	v_add_u32_e32 v200, s0, v149
	v_add_u32_e32 v201, s0, v148
	v_add_u32_e32 v168, s0, v151
	ds_read_b64_tr_b16 v[130:131], v152
	ds_read_b64_tr_b16 v[132:133], v152 offset:2048
	ds_read_b64_tr_b16 v[134:135], v168
	ds_read_b64_tr_b16 v[136:137], v168 offset:2048
	ds_read_b128 v[138:141], v169
	ds_read_b128 v[142:145], v169 offset:2048
	ds_read_b64_tr_b16 v[154:155], v200
	ds_read_b64_tr_b16 v[156:157], v200 offset:2048
	ds_read_b64_tr_b16 v[148:149], v201
	ds_read_b64_tr_b16 v[150:151], v201 offset:2048
	ds_read_b128 v[160:163], v169 offset:4096
	s_waitcnt lgkmcnt(6)
	v_mfma_f32_16x16x32_bf16 v[18:21], v[130:133], v[138:141], v[18:21]
	v_mfma_f32_16x16x32_bf16 v[22:25], v[134:137], v[138:141], v[22:25]
	s_waitcnt lgkmcnt(3)
	v_mfma_f32_16x16x32_bf16 v[26:29], v[154:157], v[138:141], v[26:29]
	s_waitcnt lgkmcnt(1)
	v_mfma_f32_16x16x32_bf16 v[14:17], v[148:151], v[138:141], v[14:17]
	ds_read_b128 v[138:141], v169 offset:6144
	v_mfma_f32_16x16x32_bf16 v[10:13], v[148:151], v[142:145], v[10:13]
	v_mfma_f32_16x16x32_bf16 v[30:33], v[130:133], v[142:145], v[30:33]
	v_mfma_f32_16x16x32_bf16 v[34:37], v[134:137], v[142:145], v[34:37]
	v_mfma_f32_16x16x32_bf16 v[38:41], v[154:157], v[142:145], v[38:41]
	ds_read_b128 v[142:145], v169 offset:8192
	s_waitcnt lgkmcnt(2)
	v_mfma_f32_16x16x32_bf16 v[6:9], v[148:151], v[160:163], v[6:9]
	v_mfma_f32_16x16x32_bf16 v[54:57], v[130:133], v[160:163], v[54:57]
	v_mfma_f32_16x16x32_bf16 v[66:69], v[134:137], v[160:163], v[66:69]
	v_mfma_f32_16x16x32_bf16 v[78:81], v[154:157], v[160:163], v[78:81]
	s_waitcnt lgkmcnt(1)
	v_mfma_f32_16x16x32_bf16 v[160:163], v[134:137], v[138:141], v[114:117]
	s_nop 2
	ds_read_b128 v[114:117], v169 offset:10240
	v_mfma_f32_16x16x32_bf16 v[2:5], v[148:151], v[138:141], v[2:5]
	v_mfma_f32_16x16x32_bf16 v[94:97], v[130:133], v[138:141], v[94:97]
	v_mfma_f32_16x16x32_bf16 v[164:167], v[154:157], v[138:141], v[122:125]
	s_waitcnt lgkmcnt(1)
	v_mfma_f32_16x16x32_bf16 v[138:141], v[134:137], v[142:145], v[118:121]
	s_nop 2
	ds_read_b128 v[118:121], v169 offset:12288
	ds_read_b64_tr_b16 v[176:177], v152 offset:16384
	ds_read_b64_tr_b16 v[178:179], v152 offset:18432
	v_mfma_f32_16x16x32_bf16 v[42:45], v[130:133], v[142:145], v[42:45]
	v_mfma_f32_16x16x32_bf16 v[172:175], v[154:157], v[142:145], v[126:129]
	v_mfma_f32_16x16x32_bf16 v[142:145], v[148:151], v[142:145], v[90:93]
	s_nop 2
	ds_read_b128 v[90:93], v169 offset:14336
	ds_read_b64_tr_b16 v[192:193], v168 offset:16384
	ds_read_b64_tr_b16 v[194:195], v168 offset:18432
	s_waitcnt lgkmcnt(6)
	v_mfma_f32_16x16x32_bf16 v[180:183], v[130:133], v[114:117], v[98:101]
	v_mfma_f32_16x16x32_bf16 v[184:187], v[134:137], v[114:117], v[102:105]
	v_mfma_f32_16x16x32_bf16 v[188:191], v[154:157], v[114:117], v[110:113]
	v_mfma_f32_16x16x32_bf16 v[196:199], v[148:151], v[114:117], v[106:109]
	v_add_u32_e32 v168, 0, v153
	s_waitcnt lgkmcnt(5)
	v_mfma_f32_16x16x32_bf16 v[216:219], v[130:133], v[118:121], v[70:73]
	s_nop 2
	ds_read_b128 v[70:73], v168
	ds_read_b64_tr_b16 v[228:229], v200 offset:16384
	ds_read_b64_tr_b16 v[230:231], v200 offset:18432
	v_mfma_f32_16x16x32_bf16 v[220:223], v[134:137], v[118:121], v[82:85]
	v_mfma_f32_16x16x32_bf16 v[224:227], v[154:157], v[118:121], v[86:89]
	v_mfma_f32_16x16x32_bf16 v[232:235], v[148:151], v[118:121], v[74:77]
	s_waitcnt lgkmcnt(5)
	v_mfma_f32_16x16x32_bf16 v[236:239], v[130:133], v[90:93], v[46:49]
	s_nop 2
	ds_read_b128 v[46:49], v168 offset:2048
	ds_read_b64_tr_b16 v[244:245], v201 offset:16384
	ds_read_b64_tr_b16 v[246:247], v201 offset:18432
	v_mfma_f32_16x16x32_bf16 v[240:243], v[134:137], v[90:93], v[58:61]
	v_mfma_f32_16x16x32_bf16 v[152:155], v[154:157], v[90:93], v[62:65]
	v_mfma_f32_16x16x32_bf16 v[148:151], v[148:151], v[90:93], v[50:53]
	s_waitcnt lgkmcnt(5)
	v_mfma_f32_16x16x32_bf16 v[248:251], v[176:179], v[70:73], v[18:21]
	s_nop 2
	ds_read_b128 v[18:21], v168 offset:4096
	v_mfma_f32_16x16x32_bf16 v[202:205], v[192:195], v[70:73], v[22:25]
	s_waitcnt lgkmcnt(4)
	v_mfma_f32_16x16x32_bf16 v[134:137], v[228:231], v[70:73], v[26:29]
	s_waitcnt lgkmcnt(1)
	v_mfma_f32_16x16x32_bf16 v[130:133], v[244:247], v[70:73], v[14:17]
	s_nop 2
	ds_read_b128 v[14:17], v168 offset:6144
	v_mfma_f32_16x16x32_bf16 v[126:129], v[176:179], v[46:49], v[30:33]
	v_mfma_f32_16x16x32_bf16 v[122:125], v[192:195], v[46:49], v[34:37]
	v_mfma_f32_16x16x32_bf16 v[118:121], v[228:231], v[46:49], v[38:41]
	v_mfma_f32_16x16x32_bf16 v[114:117], v[244:247], v[46:49], v[10:13]
	s_nop 2
	ds_read_b128 v[10:13], v168 offset:8192
	s_waitcnt lgkmcnt(2)
	v_mfma_f32_16x16x32_bf16 v[110:113], v[176:179], v[18:21], v[54:57]
	v_mfma_f32_16x16x32_bf16 v[106:109], v[192:195], v[18:21], v[66:69]
	v_mfma_f32_16x16x32_bf16 v[102:105], v[228:231], v[18:21], v[78:81]
	v_mfma_f32_16x16x32_bf16 v[98:101], v[244:247], v[18:21], v[6:9]
	s_nop 2
	ds_read_b128 v[6:9], v168 offset:10240
	s_waitcnt lgkmcnt(2)
	v_mfma_f32_16x16x32_bf16 v[94:97], v[176:179], v[14:17], v[94:97]
	v_mfma_f32_16x16x32_bf16 v[90:93], v[192:195], v[14:17], v[160:163]
	v_mfma_f32_16x16x32_bf16 v[86:89], v[228:231], v[14:17], v[164:167]
	v_mfma_f32_16x16x32_bf16 v[82:85], v[244:247], v[14:17], v[2:5]
	s_nop 2
	ds_read_b128 v[2:5], v168 offset:12288
	s_waitcnt lgkmcnt(2)
	v_mfma_f32_16x16x32_bf16 v[78:81], v[176:179], v[10:13], v[42:45]
	v_mfma_f32_16x16x32_bf16 v[74:77], v[192:195], v[10:13], v[138:141]
	v_mfma_f32_16x16x32_bf16 v[70:73], v[228:231], v[10:13], v[172:175]
	v_mfma_f32_16x16x32_bf16 v[66:69], v[244:247], v[10:13], v[142:145]
	ds_read_b128 v[14:17], v168 offset:14336
	s_waitcnt lgkmcnt(2)
	v_mfma_f32_16x16x32_bf16 v[62:65], v[176:179], v[6:9], v[180:183]
	v_mfma_f32_16x16x32_bf16 v[58:61], v[192:195], v[6:9], v[184:187]
	v_mfma_f32_16x16x32_bf16 v[54:57], v[228:231], v[6:9], v[188:191]
	v_mfma_f32_16x16x32_bf16 v[50:53], v[244:247], v[6:9], v[196:199]
	s_waitcnt lgkmcnt(1)
	v_mfma_f32_16x16x32_bf16 v[46:49], v[176:179], v[2:5], v[216:219]
	v_mfma_f32_16x16x32_bf16 v[42:45], v[192:195], v[2:5], v[220:223]
	v_mfma_f32_16x16x32_bf16 v[38:41], v[228:231], v[2:5], v[224:227]
	v_mfma_f32_16x16x32_bf16 v[34:37], v[244:247], v[2:5], v[232:235]
	s_waitcnt lgkmcnt(0)
	v_mfma_f32_16x16x32_bf16 v[10:13], v[228:231], v[14:17], v[152:155]
	v_mfma_f32_16x16x32_bf16 v[2:5], v[244:247], v[14:17], v[148:151]
	v_mfma_f32_16x16x32_bf16 v[26:29], v[176:179], v[14:17], v[236:239]
	v_mfma_f32_16x16x32_bf16 v[18:21], v[192:195], v[14:17], v[240:243]
	s_lshl_b32 s0, s26, 6
	v_mov_b32_e32 v144, v1
	v_mov_b32_e32 v145, v252
	s_or_b32 s0, s0, s22
	s_waitcnt lgkmcnt(0)
	s_barrier
	s_add_i32 s24, s24, 0
	v_lshl_add_u32 v6, v145, 2, s0
	s_add_i32 s0, s25, s21
	v_add_u32_e32 v138, s0, v144
	v_ashrrev_i32_e32 v139, 31, v138
	v_ashrrev_i32_e32 v7, 31, v6
	v_lshlrev_b64 v[8:9], 11, v[138:139]
	v_lshl_add_u64 v[8:9], s[6:7], 0, v[8:9]
	v_lshlrev_b64 v[140:141], 1, v[6:7]
	v_lshl_add_u64 v[142:143], v[8:9], 0, v[140:141]
	v_lshl_add_u64 v[6:7], v[6:7], 2, s[94:95]
	global_load_dwordx2 v[216:217], v[142:143], off
	global_load_dwordx4 v[30:33], v[6:7], off
	global_load_dwordx4 v[22:25], v[6:7], off offset:64
	global_load_dwordx4 v[14:17], v[6:7], off offset:128
	s_nop 0
	global_load_dwordx4 v[6:9], v[6:7], off offset:192
	s_nop 0
	global_load_dwordx2 v[218:219], v[142:143], off offset:32
	global_load_dwordx2 v[220:221], v[142:143], off offset:64
	global_load_dwordx2 v[200:201], v[142:143], off offset:96
	v_add_u32_e32 v142, 16, v138
	v_ashrrev_i32_e32 v143, 31, v142
	v_lshlrev_b64 v[142:143], 11, v[142:143]
	v_lshl_add_u64 v[142:143], s[6:7], 0, v[142:143]
	v_lshl_add_u64 v[142:143], v[142:143], 0, v[140:141]
	global_load_dwordx2 v[198:199], v[142:143], off
	global_load_dwordx2 v[196:197], v[142:143], off offset:32
	global_load_dwordx2 v[194:195], v[142:143], off offset:64
	global_load_dwordx2 v[192:193], v[142:143], off offset:96
	v_add_u32_e32 v142, 32, v138
	v_ashrrev_i32_e32 v143, 31, v142
	v_lshlrev_b64 v[142:143], 11, v[142:143]
	v_lshl_add_u64 v[142:143], s[6:7], 0, v[142:143]
	v_lshl_add_u64 v[142:143], v[142:143], 0, v[140:141]
	global_load_dwordx2 v[190:191], v[142:143], off
	global_load_dwordx2 v[188:189], v[142:143], off offset:32
	global_load_dwordx2 v[186:187], v[142:143], off offset:64
	global_load_dwordx2 v[184:185], v[142:143], off offset:96
	v_add_u32_e32 v142, 48, v138
	v_ashrrev_i32_e32 v143, 31, v142
	v_lshlrev_b64 v[142:143], 11, v[142:143]
	v_lshl_add_u64 v[142:143], s[6:7], 0, v[142:143]
	v_lshl_add_u64 v[142:143], v[142:143], 0, v[140:141]
	global_load_dwordx2 v[182:183], v[142:143], off
	global_load_dwordx2 v[180:181], v[142:143], off offset:32
	global_load_dwordx2 v[178:179], v[142:143], off offset:64
	global_load_dwordx2 v[176:177], v[142:143], off offset:96
	v_add_u32_e32 v142, 64, v138
	v_ashrrev_i32_e32 v143, 31, v142
	v_lshlrev_b64 v[142:143], 11, v[142:143]
	v_lshl_add_u64 v[142:143], s[6:7], 0, v[142:143]
	v_lshl_add_u64 v[142:143], v[142:143], 0, v[140:141]
	global_load_dwordx2 v[174:175], v[142:143], off
	global_load_dwordx2 v[172:173], v[142:143], off offset:32
	global_load_dwordx2 v[168:169], v[142:143], off offset:64
	global_load_dwordx2 v[166:167], v[142:143], off offset:96
	v_add_u32_e32 v142, 0x50, v138
	v_ashrrev_i32_e32 v143, 31, v142
	v_lshlrev_b64 v[142:143], 11, v[142:143]
	v_lshl_add_u64 v[142:143], s[6:7], 0, v[142:143]
	v_lshl_add_u64 v[142:143], v[142:143], 0, v[140:141]
	global_load_dwordx2 v[164:165], v[142:143], off
	global_load_dwordx2 v[162:163], v[142:143], off offset:32
	global_load_dwordx2 v[160:161], v[142:143], off offset:64
	global_load_dwordx2 v[156:157], v[142:143], off offset:96
	v_add_u32_e32 v215, s25, v144
	v_lshlrev_b32_e32 v222, 3, v145
	v_mul_lo_u32 v215, v215, s18
	v_add3_u32 v215, s24, v222, v215
	v_add_u32_e32 v142, 0x60, v138
	v_add_u32_e32 v138, 0x70, v138
	v_ashrrev_i32_e32 v143, 31, v142
	v_ashrrev_i32_e32 v139, 31, v138
	v_lshlrev_b64 v[142:143], 11, v[142:143]
	v_lshlrev_b64 v[138:139], 11, v[138:139]
	v_lshl_add_u64 v[142:143], s[6:7], 0, v[142:143]
	v_lshl_add_u64 v[138:139], s[6:7], 0, v[138:139]
	v_lshl_add_u64 v[142:143], v[142:143], 0, v[140:141]
	v_lshl_add_u64 v[138:139], v[138:139], 0, v[140:141]
	global_load_dwordx2 v[154:155], v[142:143], off
	global_load_dwordx2 v[152:153], v[142:143], off offset:32
	global_load_dwordx2 v[150:151], v[142:143], off offset:64
	global_load_dwordx2 v[148:149], v[142:143], off offset:96
	global_load_dwordx2 v[144:145], v[138:139], off
	s_nop 0
	global_load_dwordx2 v[142:143], v[138:139], off offset:32
	global_load_dwordx2 v[140:141], v[138:139], off offset:64
	s_nop 0
	global_load_dwordx2 v[138:139], v[138:139], off offset:96
	s_lshl_b32 s2, s22, 1
	s_waitcnt vmcnt(34)
	v_pk_add_f32 v[224:225], v[250:251], v[32:33]
	v_pk_add_f32 v[226:227], v[248:249], v[30:31]
	v_pk_mul_f32 v[224:225], v[224:225], s[14:15] op_sel_hi:[1,0]
	v_pk_mul_f32 v[226:227], v[226:227], s[14:15] op_sel_hi:[1,0]
	v_exp_f32_e32 v224, v224
	v_exp_f32_e32 v226, v226
	v_exp_f32_e32 v227, v227
	v_exp_f32_e32 v225, v225
	s_waitcnt vmcnt(33)
	v_pk_add_f32 v[202:203], v[202:203], v[22:23]
	v_pk_add_f32 v[204:205], v[204:205], v[24:25]
	v_pk_mul_f32 v[202:203], v[202:203], s[14:15] op_sel_hi:[1,0]
	v_pk_mul_f32 v[204:205], v[204:205], s[14:15] op_sel_hi:[1,0]
	v_exp_f32_e32 v202, v202
	v_exp_f32_e32 v203, v203
	v_exp_f32_e32 v204, v204
	v_exp_f32_e32 v205, v205
	v_pk_add_f32 v[226:227], v[226:227], 1.0 op_sel_hi:[1,0]
	v_pk_add_f32 v[224:225], v[224:225], 1.0 op_sel_hi:[1,0]
	s_waitcnt vmcnt(32)
	v_pk_add_f32 v[134:135], v[134:135], v[14:15]
	v_rcp_f32_e32 v226, v226
	v_rcp_f32_e32 v227, v227
	v_rcp_f32_e32 v224, v224
	v_rcp_f32_e32 v225, v225
	v_pk_add_f32 v[136:137], v[136:137], v[16:17]
	v_pk_mul_f32 v[134:135], v[134:135], s[14:15] op_sel_hi:[1,0]
	v_pk_add_f32 v[202:203], v[202:203], 1.0 op_sel_hi:[1,0]
	v_exp_f32_e32 v134, v134
	v_exp_f32_e32 v135, v135
	v_pk_mul_f32 v[136:137], v[136:137], s[14:15] op_sel_hi:[1,0]
	v_rcp_f32_e32 v202, v202
	v_rcp_f32_e32 v203, v203
	v_pk_add_f32 v[204:205], v[204:205], 1.0 op_sel_hi:[1,0]
	v_exp_f32_e32 v136, v136
	v_exp_f32_e32 v137, v137
	s_waitcnt vmcnt(31)
	v_pk_add_f32 v[130:131], v[130:131], v[6:7]
	v_lshlrev_b32_e32 v222, 16, v216
	v_and_b32_e32 v223, 0xffff0000, v216
	v_lshlrev_b32_e32 v216, 16, v217
	v_and_b32_e32 v217, 0xffff0000, v217
	v_rcp_f32_e32 v204, v204
	v_rcp_f32_e32 v205, v205
	v_pk_add_f32 v[132:133], v[132:133], v[8:9]
	v_pk_mul_f32 v[130:131], v[130:131], s[14:15] op_sel_hi:[1,0]
	v_pk_mul_f32 v[222:223], v[226:227], v[222:223]
	v_pk_mul_f32 v[216:217], v[224:225], v[216:217]
	v_exp_f32_e32 v130, v130
	v_exp_f32_e32 v131, v131
	v_pk_mul_f32 v[132:133], v[132:133], s[14:15] op_sel_hi:[1,0]
	v_cvt_pk_bf16_f32 v222, v222, v223
	v_cvt_pk_bf16_f32 v223, v216, v217
	s_waitcnt vmcnt(30)
	v_lshlrev_b32_e32 v216, 16, v218
	v_and_b32_e32 v217, 0xffff0000, v218
	v_pk_add_f32 v[134:135], v[134:135], 1.0 op_sel_hi:[1,0]
	v_exp_f32_e32 v132, v132
	v_exp_f32_e32 v133, v133
	v_pk_mul_f32 v[202:203], v[202:203], v[216:217]
	v_lshlrev_b32_e32 v216, 16, v219
	v_and_b32_e32 v217, 0xffff0000, v219
	v_rcp_f32_e32 v134, v134
	v_rcp_f32_e32 v135, v135
	v_pk_add_f32 v[136:137], v[136:137], 1.0 op_sel_hi:[1,0]
	v_pk_add_f32 v[126:127], v[126:127], v[30:31]
	v_pk_mul_f32 v[204:205], v[204:205], v[216:217]
	v_rcp_f32_e32 v136, v136
	v_rcp_f32_e32 v137, v137
	v_pk_add_f32 v[128:129], v[128:129], v[32:33]
	v_pk_mul_f32 v[126:127], v[126:127], s[14:15] op_sel_hi:[1,0]
	v_cvt_pk_bf16_f32 v202, v202, v203
	v_cvt_pk_bf16_f32 v203, v204, v205
	v_pk_add_f32 v[130:131], v[130:131], 1.0 op_sel_hi:[1,0]
	v_exp_f32_e32 v126, v126
	v_exp_f32_e32 v127, v127
	v_pk_mul_f32 v[128:129], v[128:129], s[14:15] op_sel_hi:[1,0]
	ds_write2_b64 v215, v[222:223], v[202:203] offset1:4
	s_waitcnt vmcnt(29)
	v_lshlrev_b32_e32 v202, 16, v220
	v_and_b32_e32 v203, 0xffff0000, v220
	v_rcp_f32_e32 v130, v130
	v_rcp_f32_e32 v131, v131
	v_pk_add_f32 v[132:133], v[132:133], 1.0 op_sel_hi:[1,0]
	v_exp_f32_e32 v128, v128
	v_exp_f32_e32 v129, v129
	v_pk_add_f32 v[122:123], v[122:123], v[22:23]
	v_pk_mul_f32 v[134:135], v[134:135], v[202:203]
	v_lshlrev_b32_e32 v202, 16, v221
	v_and_b32_e32 v203, 0xffff0000, v221
	v_rcp_f32_e32 v132, v132
	v_rcp_f32_e32 v133, v133
	v_pk_add_f32 v[124:125], v[124:125], v[24:25]
	v_pk_mul_f32 v[122:123], v[122:123], s[14:15] op_sel_hi:[1,0]
	v_pk_mul_f32 v[136:137], v[136:137], v[202:203]
	v_exp_f32_e32 v122, v122
	v_exp_f32_e32 v123, v123
	v_pk_mul_f32 v[124:125], v[124:125], s[14:15] op_sel_hi:[1,0]
	v_cvt_pk_bf16_f32 v134, v134, v135
	v_cvt_pk_bf16_f32 v135, v136, v137
	s_waitcnt vmcnt(28)
	v_lshlrev_b32_e32 v136, 16, v200
	v_and_b32_e32 v137, 0xffff0000, v200
	v_pk_add_f32 v[126:127], v[126:127], 1.0 op_sel_hi:[1,0]
	v_exp_f32_e32 v124, v124
	v_exp_f32_e32 v125, v125
	v_pk_mul_f32 v[130:131], v[130:131], v[136:137]
	v_lshlrev_b32_e32 v136, 16, v201
	v_and_b32_e32 v137, 0xffff0000, v201
	v_rcp_f32_e32 v126, v126
	v_rcp_f32_e32 v127, v127
	v_pk_add_f32 v[128:129], v[128:129], 1.0 op_sel_hi:[1,0]
	v_pk_add_f32 v[118:119], v[118:119], v[14:15]
	v_pk_mul_f32 v[132:133], v[132:133], v[136:137]
	v_rcp_f32_e32 v128, v128
	v_rcp_f32_e32 v129, v129
	v_pk_add_f32 v[120:121], v[120:121], v[16:17]
	v_pk_mul_f32 v[118:119], v[118:119], s[14:15] op_sel_hi:[1,0]
	v_cvt_pk_bf16_f32 v130, v130, v131
	v_cvt_pk_bf16_f32 v131, v132, v133
	v_pk_add_f32 v[122:123], v[122:123], 1.0 op_sel_hi:[1,0]
	v_exp_f32_e32 v118, v118
	v_exp_f32_e32 v119, v119
	v_pk_mul_f32 v[120:121], v[120:121], s[14:15] op_sel_hi:[1,0]
	ds_write2_b64 v215, v[134:135], v[130:131] offset0:8 offset1:12
	s_waitcnt vmcnt(27)
	v_lshlrev_b32_e32 v130, 16, v198
	v_and_b32_e32 v131, 0xffff0000, v198
	v_rcp_f32_e32 v122, v122
	v_rcp_f32_e32 v123, v123
	v_pk_add_f32 v[124:125], v[124:125], 1.0 op_sel_hi:[1,0]
	v_exp_f32_e32 v120, v120
	v_exp_f32_e32 v121, v121
	v_pk_add_f32 v[114:115], v[114:115], v[6:7]
	v_pk_mul_f32 v[126:127], v[126:127], v[130:131]
	v_lshlrev_b32_e32 v130, 16, v199
	v_and_b32_e32 v131, 0xffff0000, v199
	v_rcp_f32_e32 v124, v124
	v_rcp_f32_e32 v125, v125
	v_pk_add_f32 v[116:117], v[116:117], v[8:9]
	v_pk_mul_f32 v[114:115], v[114:115], s[14:15] op_sel_hi:[1,0]
	v_pk_mul_f32 v[128:129], v[128:129], v[130:131]
	v_exp_f32_e32 v114, v114
	v_exp_f32_e32 v115, v115
	v_pk_mul_f32 v[116:117], v[116:117], s[14:15] op_sel_hi:[1,0]
	v_cvt_pk_bf16_f32 v126, v126, v127
	v_cvt_pk_bf16_f32 v127, v128, v129
	s_waitcnt vmcnt(26)
	v_lshlrev_b32_e32 v128, 16, v196
	v_and_b32_e32 v129, 0xffff0000, v196
	v_pk_add_f32 v[118:119], v[118:119], 1.0 op_sel_hi:[1,0]
	v_exp_f32_e32 v116, v116
	v_exp_f32_e32 v117, v117
	v_pk_mul_f32 v[122:123], v[122:123], v[128:129]
	v_lshlrev_b32_e32 v128, 16, v197
	v_and_b32_e32 v129, 0xffff0000, v197
	v_rcp_f32_e32 v118, v118
	v_rcp_f32_e32 v119, v119
	v_pk_add_f32 v[120:121], v[120:121], 1.0 op_sel_hi:[1,0]
	v_pk_add_f32 v[110:111], v[110:111], v[30:31]
	v_pk_mul_f32 v[124:125], v[124:125], v[128:129]
	v_rcp_f32_e32 v120, v120
	v_rcp_f32_e32 v121, v121
	v_pk_add_f32 v[112:113], v[112:113], v[32:33]
	v_pk_mul_f32 v[110:111], v[110:111], s[14:15] op_sel_hi:[1,0]
	v_cvt_pk_bf16_f32 v122, v122, v123
	v_cvt_pk_bf16_f32 v123, v124, v125
	v_add_u32_e32 v124, 0x2000, v215
	v_pk_add_f32 v[114:115], v[114:115], 1.0 op_sel_hi:[1,0]
	v_exp_f32_e32 v110, v110
	v_exp_f32_e32 v111, v111
	v_pk_mul_f32 v[112:113], v[112:113], s[14:15] op_sel_hi:[1,0]
	ds_write2_b64 v124, v[126:127], v[122:123] offset0:32 offset1:36
	s_waitcnt vmcnt(25)
	v_lshlrev_b32_e32 v122, 16, v194
	v_and_b32_e32 v123, 0xffff0000, v194
	v_rcp_f32_e32 v114, v114
	v_rcp_f32_e32 v115, v115
	v_pk_add_f32 v[116:117], v[116:117], 1.0 op_sel_hi:[1,0]
	v_exp_f32_e32 v112, v112
	v_exp_f32_e32 v113, v113
	v_pk_add_f32 v[106:107], v[106:107], v[22:23]
	v_pk_mul_f32 v[118:119], v[118:119], v[122:123]
	v_lshlrev_b32_e32 v122, 16, v195
	v_and_b32_e32 v123, 0xffff0000, v195
	v_rcp_f32_e32 v116, v116
	v_rcp_f32_e32 v117, v117
	v_pk_add_f32 v[108:109], v[108:109], v[24:25]
	v_pk_mul_f32 v[106:107], v[106:107], s[14:15] op_sel_hi:[1,0]
	v_pk_mul_f32 v[120:121], v[120:121], v[122:123]
	v_exp_f32_e32 v106, v106
	v_exp_f32_e32 v107, v107
	v_pk_mul_f32 v[108:109], v[108:109], s[14:15] op_sel_hi:[1,0]
	v_cvt_pk_bf16_f32 v118, v118, v119
	v_cvt_pk_bf16_f32 v119, v120, v121
	s_waitcnt vmcnt(24)
	v_lshlrev_b32_e32 v120, 16, v192
	v_and_b32_e32 v121, 0xffff0000, v192
	v_pk_add_f32 v[110:111], v[110:111], 1.0 op_sel_hi:[1,0]
	v_exp_f32_e32 v108, v108
	v_exp_f32_e32 v109, v109
	v_pk_mul_f32 v[114:115], v[114:115], v[120:121]
	v_lshlrev_b32_e32 v120, 16, v193
	v_and_b32_e32 v121, 0xffff0000, v193
	v_rcp_f32_e32 v110, v110
	v_rcp_f32_e32 v111, v111
	v_pk_add_f32 v[112:113], v[112:113], 1.0 op_sel_hi:[1,0]
	v_pk_add_f32 v[102:103], v[102:103], v[14:15]
	v_pk_mul_f32 v[116:117], v[116:117], v[120:121]
	v_rcp_f32_e32 v112, v112
	v_rcp_f32_e32 v113, v113
	v_pk_add_f32 v[104:105], v[104:105], v[16:17]
	v_pk_mul_f32 v[102:103], v[102:103], s[14:15] op_sel_hi:[1,0]
	v_cvt_pk_bf16_f32 v114, v114, v115
	v_cvt_pk_bf16_f32 v115, v116, v117
	v_pk_add_f32 v[106:107], v[106:107], 1.0 op_sel_hi:[1,0]
	v_exp_f32_e32 v102, v102
	v_exp_f32_e32 v103, v103
	v_pk_mul_f32 v[104:105], v[104:105], s[14:15] op_sel_hi:[1,0]
	ds_write2_b64 v124, v[118:119], v[114:115] offset0:40 offset1:44
	s_waitcnt vmcnt(23)
	v_lshlrev_b32_e32 v114, 16, v190
	v_and_b32_e32 v115, 0xffff0000, v190
	v_rcp_f32_e32 v106, v106
	v_rcp_f32_e32 v107, v107
	v_pk_add_f32 v[108:109], v[108:109], 1.0 op_sel_hi:[1,0]
	v_exp_f32_e32 v104, v104
	v_exp_f32_e32 v105, v105
	v_pk_add_f32 v[98:99], v[98:99], v[6:7]
	v_pk_mul_f32 v[110:111], v[110:111], v[114:115]
	v_lshlrev_b32_e32 v114, 16, v191
	v_and_b32_e32 v115, 0xffff0000, v191
	v_rcp_f32_e32 v108, v108
	v_rcp_f32_e32 v109, v109
	v_pk_add_f32 v[100:101], v[100:101], v[8:9]
	v_pk_mul_f32 v[98:99], v[98:99], s[14:15] op_sel_hi:[1,0]
	v_pk_mul_f32 v[112:113], v[112:113], v[114:115]
	v_exp_f32_e32 v98, v98
	v_exp_f32_e32 v99, v99
	v_pk_mul_f32 v[100:101], v[100:101], s[14:15] op_sel_hi:[1,0]
	v_cvt_pk_bf16_f32 v110, v110, v111
	v_cvt_pk_bf16_f32 v111, v112, v113
	s_waitcnt vmcnt(22)
	v_lshlrev_b32_e32 v112, 16, v188
	v_and_b32_e32 v113, 0xffff0000, v188
	v_pk_add_f32 v[102:103], v[102:103], 1.0 op_sel_hi:[1,0]
	v_exp_f32_e32 v100, v100
	v_exp_f32_e32 v101, v101
	v_pk_mul_f32 v[106:107], v[106:107], v[112:113]
	v_lshlrev_b32_e32 v112, 16, v189
	v_and_b32_e32 v113, 0xffff0000, v189
	v_rcp_f32_e32 v102, v102
	v_rcp_f32_e32 v103, v103
	v_pk_add_f32 v[104:105], v[104:105], 1.0 op_sel_hi:[1,0]
	v_pk_add_f32 v[94:95], v[94:95], v[30:31]
	v_pk_mul_f32 v[108:109], v[108:109], v[112:113]
	v_rcp_f32_e32 v104, v104
	v_rcp_f32_e32 v105, v105
	v_pk_add_f32 v[96:97], v[96:97], v[32:33]
	v_pk_mul_f32 v[94:95], v[94:95], s[14:15] op_sel_hi:[1,0]
	v_cvt_pk_bf16_f32 v106, v106, v107
	v_cvt_pk_bf16_f32 v107, v108, v109
	v_add_u32_e32 v108, 0x4000, v215
	v_pk_add_f32 v[98:99], v[98:99], 1.0 op_sel_hi:[1,0]
	v_exp_f32_e32 v94, v94
	v_exp_f32_e32 v95, v95
	v_pk_mul_f32 v[96:97], v[96:97], s[14:15] op_sel_hi:[1,0]
	ds_write2_b64 v108, v[110:111], v[106:107] offset0:64 offset1:68
	s_waitcnt vmcnt(21)
	v_lshlrev_b32_e32 v106, 16, v186
	v_and_b32_e32 v107, 0xffff0000, v186
	v_rcp_f32_e32 v98, v98
	v_rcp_f32_e32 v99, v99
	v_pk_add_f32 v[100:101], v[100:101], 1.0 op_sel_hi:[1,0]
	v_exp_f32_e32 v96, v96
	v_exp_f32_e32 v97, v97
	v_pk_add_f32 v[90:91], v[90:91], v[22:23]
	v_pk_mul_f32 v[102:103], v[102:103], v[106:107]
	v_lshlrev_b32_e32 v106, 16, v187
	v_and_b32_e32 v107, 0xffff0000, v187
	v_rcp_f32_e32 v100, v100
	v_rcp_f32_e32 v101, v101
	v_pk_add_f32 v[92:93], v[92:93], v[24:25]
	v_pk_mul_f32 v[90:91], v[90:91], s[14:15] op_sel_hi:[1,0]
	v_pk_mul_f32 v[104:105], v[104:105], v[106:107]
	v_exp_f32_e32 v90, v90
	v_exp_f32_e32 v91, v91
	v_pk_mul_f32 v[92:93], v[92:93], s[14:15] op_sel_hi:[1,0]
	v_cvt_pk_bf16_f32 v102, v102, v103
	v_cvt_pk_bf16_f32 v103, v104, v105
	s_waitcnt vmcnt(20)
	v_lshlrev_b32_e32 v104, 16, v184
	v_and_b32_e32 v105, 0xffff0000, v184
	v_pk_add_f32 v[94:95], v[94:95], 1.0 op_sel_hi:[1,0]
	v_exp_f32_e32 v92, v92
	v_exp_f32_e32 v93, v93
	v_pk_mul_f32 v[98:99], v[98:99], v[104:105]
	v_lshlrev_b32_e32 v104, 16, v185
	v_and_b32_e32 v105, 0xffff0000, v185
	v_rcp_f32_e32 v94, v94
	v_rcp_f32_e32 v95, v95
	v_pk_add_f32 v[96:97], v[96:97], 1.0 op_sel_hi:[1,0]
	v_pk_add_f32 v[86:87], v[86:87], v[14:15]
	v_pk_mul_f32 v[100:101], v[100:101], v[104:105]
	v_rcp_f32_e32 v96, v96
	v_rcp_f32_e32 v97, v97
	v_pk_add_f32 v[88:89], v[88:89], v[16:17]
	v_pk_mul_f32 v[86:87], v[86:87], s[14:15] op_sel_hi:[1,0]
	v_cvt_pk_bf16_f32 v98, v98, v99
	v_cvt_pk_bf16_f32 v99, v100, v101
	v_pk_add_f32 v[90:91], v[90:91], 1.0 op_sel_hi:[1,0]
	v_exp_f32_e32 v86, v86
	v_exp_f32_e32 v87, v87
	v_pk_mul_f32 v[88:89], v[88:89], s[14:15] op_sel_hi:[1,0]
	ds_write2_b64 v108, v[102:103], v[98:99] offset0:72 offset1:76
	s_waitcnt vmcnt(19)
	v_lshlrev_b32_e32 v98, 16, v182
	v_and_b32_e32 v99, 0xffff0000, v182
	v_rcp_f32_e32 v90, v90
	v_rcp_f32_e32 v91, v91
	v_pk_add_f32 v[92:93], v[92:93], 1.0 op_sel_hi:[1,0]
	v_exp_f32_e32 v88, v88
	v_exp_f32_e32 v89, v89
	v_pk_add_f32 v[82:83], v[82:83], v[6:7]
	v_pk_mul_f32 v[94:95], v[94:95], v[98:99]
	v_lshlrev_b32_e32 v98, 16, v183
	v_and_b32_e32 v99, 0xffff0000, v183
	v_rcp_f32_e32 v92, v92
	v_rcp_f32_e32 v93, v93
	v_pk_add_f32 v[84:85], v[84:85], v[8:9]
	v_pk_mul_f32 v[82:83], v[82:83], s[14:15] op_sel_hi:[1,0]
	v_pk_mul_f32 v[96:97], v[96:97], v[98:99]
	v_exp_f32_e32 v82, v82
	v_exp_f32_e32 v83, v83
	v_pk_mul_f32 v[84:85], v[84:85], s[14:15] op_sel_hi:[1,0]
	v_cvt_pk_bf16_f32 v94, v94, v95
	v_cvt_pk_bf16_f32 v95, v96, v97
	s_waitcnt vmcnt(18)
	v_lshlrev_b32_e32 v96, 16, v180
	v_and_b32_e32 v97, 0xffff0000, v180
	v_pk_add_f32 v[86:87], v[86:87], 1.0 op_sel_hi:[1,0]
	v_exp_f32_e32 v84, v84
	v_exp_f32_e32 v85, v85
	v_pk_mul_f32 v[90:91], v[90:91], v[96:97]
	v_lshlrev_b32_e32 v96, 16, v181
	v_and_b32_e32 v97, 0xffff0000, v181
	v_rcp_f32_e32 v86, v86
	v_rcp_f32_e32 v87, v87
	v_pk_add_f32 v[88:89], v[88:89], 1.0 op_sel_hi:[1,0]
	v_pk_add_f32 v[78:79], v[78:79], v[30:31]
	v_pk_mul_f32 v[92:93], v[92:93], v[96:97]
	v_rcp_f32_e32 v88, v88
	v_rcp_f32_e32 v89, v89
	v_pk_add_f32 v[80:81], v[80:81], v[32:33]
	v_pk_mul_f32 v[78:79], v[78:79], s[14:15] op_sel_hi:[1,0]
	v_cvt_pk_bf16_f32 v90, v90, v91
	v_cvt_pk_bf16_f32 v91, v92, v93
	v_add_u32_e32 v92, 0x6000, v215
	v_pk_add_f32 v[82:83], v[82:83], 1.0 op_sel_hi:[1,0]
	v_exp_f32_e32 v78, v78
	v_exp_f32_e32 v79, v79
	v_pk_mul_f32 v[80:81], v[80:81], s[14:15] op_sel_hi:[1,0]
	ds_write2_b64 v92, v[94:95], v[90:91] offset0:96 offset1:100
	s_waitcnt vmcnt(17)
	v_lshlrev_b32_e32 v90, 16, v178
	v_and_b32_e32 v91, 0xffff0000, v178
	v_rcp_f32_e32 v82, v82
	v_rcp_f32_e32 v83, v83
	v_pk_add_f32 v[84:85], v[84:85], 1.0 op_sel_hi:[1,0]
	v_exp_f32_e32 v80, v80
	v_exp_f32_e32 v81, v81
	v_pk_add_f32 v[74:75], v[74:75], v[22:23]
	v_pk_mul_f32 v[86:87], v[86:87], v[90:91]
	v_lshlrev_b32_e32 v90, 16, v179
	v_and_b32_e32 v91, 0xffff0000, v179
	v_rcp_f32_e32 v84, v84
	v_rcp_f32_e32 v85, v85
	v_pk_add_f32 v[76:77], v[76:77], v[24:25]
	v_pk_mul_f32 v[74:75], v[74:75], s[14:15] op_sel_hi:[1,0]
	v_pk_mul_f32 v[88:89], v[88:89], v[90:91]
	v_exp_f32_e32 v74, v74
	v_exp_f32_e32 v75, v75
	v_pk_mul_f32 v[76:77], v[76:77], s[14:15] op_sel_hi:[1,0]
	v_cvt_pk_bf16_f32 v86, v86, v87
	v_cvt_pk_bf16_f32 v87, v88, v89
	s_waitcnt vmcnt(16)
	v_lshlrev_b32_e32 v88, 16, v176
	v_and_b32_e32 v89, 0xffff0000, v176
	v_pk_add_f32 v[78:79], v[78:79], 1.0 op_sel_hi:[1,0]
	v_exp_f32_e32 v76, v76
	v_exp_f32_e32 v77, v77
	v_pk_mul_f32 v[82:83], v[82:83], v[88:89]
	v_lshlrev_b32_e32 v88, 16, v177
	v_and_b32_e32 v89, 0xffff0000, v177
	v_rcp_f32_e32 v78, v78
	v_rcp_f32_e32 v79, v79
	v_pk_add_f32 v[80:81], v[80:81], 1.0 op_sel_hi:[1,0]
	v_pk_add_f32 v[70:71], v[70:71], v[14:15]
	v_pk_mul_f32 v[84:85], v[84:85], v[88:89]
	v_rcp_f32_e32 v80, v80
	v_rcp_f32_e32 v81, v81
	v_pk_add_f32 v[72:73], v[72:73], v[16:17]
	v_pk_mul_f32 v[70:71], v[70:71], s[14:15] op_sel_hi:[1,0]
	v_cvt_pk_bf16_f32 v82, v82, v83
	v_cvt_pk_bf16_f32 v83, v84, v85
	v_pk_add_f32 v[74:75], v[74:75], 1.0 op_sel_hi:[1,0]
	v_exp_f32_e32 v70, v70
	v_exp_f32_e32 v71, v71
	v_pk_mul_f32 v[72:73], v[72:73], s[14:15] op_sel_hi:[1,0]
	ds_write2_b64 v92, v[86:87], v[82:83] offset0:104 offset1:108
	s_waitcnt vmcnt(15)
	v_lshlrev_b32_e32 v82, 16, v174
	v_and_b32_e32 v83, 0xffff0000, v174
	v_rcp_f32_e32 v74, v74
	v_rcp_f32_e32 v75, v75
	v_pk_add_f32 v[76:77], v[76:77], 1.0 op_sel_hi:[1,0]
	v_exp_f32_e32 v72, v72
	v_exp_f32_e32 v73, v73
	v_pk_add_f32 v[66:67], v[66:67], v[6:7]
	v_pk_mul_f32 v[78:79], v[78:79], v[82:83]
	v_lshlrev_b32_e32 v82, 16, v175
	v_and_b32_e32 v83, 0xffff0000, v175
	v_rcp_f32_e32 v76, v76
	v_rcp_f32_e32 v77, v77
	v_pk_add_f32 v[68:69], v[68:69], v[8:9]
	v_pk_mul_f32 v[66:67], v[66:67], s[14:15] op_sel_hi:[1,0]
	v_pk_mul_f32 v[80:81], v[80:81], v[82:83]
	v_exp_f32_e32 v66, v66
	v_exp_f32_e32 v67, v67
	v_pk_mul_f32 v[68:69], v[68:69], s[14:15] op_sel_hi:[1,0]
	v_cvt_pk_bf16_f32 v78, v78, v79
	v_cvt_pk_bf16_f32 v79, v80, v81
	s_waitcnt vmcnt(14)
	v_lshlrev_b32_e32 v80, 16, v172
	v_and_b32_e32 v81, 0xffff0000, v172
	v_pk_add_f32 v[70:71], v[70:71], 1.0 op_sel_hi:[1,0]
	v_exp_f32_e32 v68, v68
	v_exp_f32_e32 v69, v69
	v_pk_mul_f32 v[74:75], v[74:75], v[80:81]
	v_lshlrev_b32_e32 v80, 16, v173
	v_and_b32_e32 v81, 0xffff0000, v173
	v_rcp_f32_e32 v70, v70
	v_rcp_f32_e32 v71, v71
	v_pk_add_f32 v[72:73], v[72:73], 1.0 op_sel_hi:[1,0]
	v_pk_add_f32 v[62:63], v[62:63], v[30:31]
	v_pk_mul_f32 v[76:77], v[76:77], v[80:81]
	v_rcp_f32_e32 v72, v72
	v_rcp_f32_e32 v73, v73
	v_pk_add_f32 v[64:65], v[64:65], v[32:33]
	v_pk_mul_f32 v[62:63], v[62:63], s[14:15] op_sel_hi:[1,0]
	v_cvt_pk_bf16_f32 v74, v74, v75
	v_cvt_pk_bf16_f32 v75, v76, v77
	v_add_u32_e32 v76, 0x8000, v215
	v_pk_add_f32 v[66:67], v[66:67], 1.0 op_sel_hi:[1,0]
	v_exp_f32_e32 v62, v62
	v_exp_f32_e32 v63, v63
	v_pk_mul_f32 v[64:65], v[64:65], s[14:15] op_sel_hi:[1,0]
	ds_write2_b64 v76, v[78:79], v[74:75] offset0:128 offset1:132
	s_waitcnt vmcnt(13)
	v_lshlrev_b32_e32 v74, 16, v168
	v_and_b32_e32 v75, 0xffff0000, v168
	v_rcp_f32_e32 v66, v66
	v_rcp_f32_e32 v67, v67
	v_pk_add_f32 v[68:69], v[68:69], 1.0 op_sel_hi:[1,0]
	v_exp_f32_e32 v64, v64
	v_exp_f32_e32 v65, v65
	v_pk_add_f32 v[58:59], v[58:59], v[22:23]
	v_pk_mul_f32 v[70:71], v[70:71], v[74:75]
	v_lshlrev_b32_e32 v74, 16, v169
	v_and_b32_e32 v75, 0xffff0000, v169
	v_rcp_f32_e32 v68, v68
	v_rcp_f32_e32 v69, v69
	v_pk_add_f32 v[60:61], v[60:61], v[24:25]
	v_pk_mul_f32 v[58:59], v[58:59], s[14:15] op_sel_hi:[1,0]
	v_pk_mul_f32 v[72:73], v[72:73], v[74:75]
	v_exp_f32_e32 v58, v58
	v_exp_f32_e32 v59, v59
	v_pk_mul_f32 v[60:61], v[60:61], s[14:15] op_sel_hi:[1,0]
	v_cvt_pk_bf16_f32 v70, v70, v71
	v_cvt_pk_bf16_f32 v71, v72, v73
	s_waitcnt vmcnt(12)
	v_lshlrev_b32_e32 v72, 16, v166
	v_and_b32_e32 v73, 0xffff0000, v166
	v_pk_add_f32 v[62:63], v[62:63], 1.0 op_sel_hi:[1,0]
	v_exp_f32_e32 v60, v60
	v_exp_f32_e32 v61, v61
	v_pk_mul_f32 v[66:67], v[66:67], v[72:73]
	v_lshlrev_b32_e32 v72, 16, v167
	v_and_b32_e32 v73, 0xffff0000, v167
	v_rcp_f32_e32 v62, v62
	v_rcp_f32_e32 v63, v63
	v_pk_add_f32 v[64:65], v[64:65], 1.0 op_sel_hi:[1,0]
	v_pk_add_f32 v[54:55], v[54:55], v[14:15]
	v_pk_mul_f32 v[68:69], v[68:69], v[72:73]
	v_rcp_f32_e32 v64, v64
	v_rcp_f32_e32 v65, v65
	v_pk_add_f32 v[56:57], v[56:57], v[16:17]
	v_pk_mul_f32 v[54:55], v[54:55], s[14:15] op_sel_hi:[1,0]
	v_cvt_pk_bf16_f32 v66, v66, v67
	v_cvt_pk_bf16_f32 v67, v68, v69
	v_pk_add_f32 v[58:59], v[58:59], 1.0 op_sel_hi:[1,0]
	v_exp_f32_e32 v54, v54
	v_exp_f32_e32 v55, v55
	v_pk_mul_f32 v[56:57], v[56:57], s[14:15] op_sel_hi:[1,0]
	ds_write2_b64 v76, v[70:71], v[66:67] offset0:136 offset1:140
	s_waitcnt vmcnt(11)
	v_lshlrev_b32_e32 v66, 16, v164
	v_and_b32_e32 v67, 0xffff0000, v164
	v_rcp_f32_e32 v58, v58
	v_rcp_f32_e32 v59, v59
	v_pk_add_f32 v[60:61], v[60:61], 1.0 op_sel_hi:[1,0]
	v_exp_f32_e32 v56, v56
	v_exp_f32_e32 v57, v57
	v_pk_add_f32 v[50:51], v[50:51], v[6:7]
	v_pk_mul_f32 v[62:63], v[62:63], v[66:67]
	v_lshlrev_b32_e32 v66, 16, v165
	v_and_b32_e32 v67, 0xffff0000, v165
	v_rcp_f32_e32 v60, v60
	v_rcp_f32_e32 v61, v61
	v_pk_add_f32 v[52:53], v[52:53], v[8:9]
	v_pk_mul_f32 v[50:51], v[50:51], s[14:15] op_sel_hi:[1,0]
	v_pk_mul_f32 v[64:65], v[64:65], v[66:67]
	v_exp_f32_e32 v50, v50
	v_exp_f32_e32 v51, v51
	v_pk_mul_f32 v[52:53], v[52:53], s[14:15] op_sel_hi:[1,0]
	v_cvt_pk_bf16_f32 v62, v62, v63
	v_cvt_pk_bf16_f32 v63, v64, v65
	s_waitcnt vmcnt(10)
	v_lshlrev_b32_e32 v64, 16, v162
	v_and_b32_e32 v65, 0xffff0000, v162
	v_pk_add_f32 v[54:55], v[54:55], 1.0 op_sel_hi:[1,0]
	v_exp_f32_e32 v52, v52
	v_exp_f32_e32 v53, v53
	v_pk_mul_f32 v[58:59], v[58:59], v[64:65]
	v_lshlrev_b32_e32 v64, 16, v163
	v_and_b32_e32 v65, 0xffff0000, v163
	v_rcp_f32_e32 v54, v54
	v_rcp_f32_e32 v55, v55
	v_pk_add_f32 v[56:57], v[56:57], 1.0 op_sel_hi:[1,0]
	v_pk_add_f32 v[46:47], v[46:47], v[30:31]
	v_pk_mul_f32 v[60:61], v[60:61], v[64:65]
	v_rcp_f32_e32 v56, v56
	v_rcp_f32_e32 v57, v57
	v_pk_add_f32 v[48:49], v[48:49], v[32:33]
	v_pk_mul_f32 v[46:47], v[46:47], s[14:15] op_sel_hi:[1,0]
	v_cvt_pk_bf16_f32 v58, v58, v59
	v_cvt_pk_bf16_f32 v59, v60, v61
	v_add_u32_e32 v60, 0xa000, v215
	v_pk_add_f32 v[50:51], v[50:51], 1.0 op_sel_hi:[1,0]
	v_exp_f32_e32 v46, v46
	v_exp_f32_e32 v47, v47
	v_pk_mul_f32 v[48:49], v[48:49], s[14:15] op_sel_hi:[1,0]
	ds_write2_b64 v60, v[62:63], v[58:59] offset0:160 offset1:164
	s_waitcnt vmcnt(9)
	v_lshlrev_b32_e32 v58, 16, v160
	v_and_b32_e32 v59, 0xffff0000, v160
	v_rcp_f32_e32 v50, v50
	v_rcp_f32_e32 v51, v51
	v_pk_add_f32 v[52:53], v[52:53], 1.0 op_sel_hi:[1,0]
	v_exp_f32_e32 v48, v48
	v_exp_f32_e32 v49, v49
	v_pk_add_f32 v[42:43], v[42:43], v[22:23]
	v_pk_mul_f32 v[54:55], v[54:55], v[58:59]
	v_lshlrev_b32_e32 v58, 16, v161
	v_and_b32_e32 v59, 0xffff0000, v161
	v_rcp_f32_e32 v52, v52
	v_rcp_f32_e32 v53, v53
	v_pk_add_f32 v[44:45], v[44:45], v[24:25]
	v_pk_mul_f32 v[42:43], v[42:43], s[14:15] op_sel_hi:[1,0]
	v_pk_mul_f32 v[56:57], v[56:57], v[58:59]
	v_exp_f32_e32 v42, v42
	v_exp_f32_e32 v43, v43
	v_pk_mul_f32 v[44:45], v[44:45], s[14:15] op_sel_hi:[1,0]
	v_cvt_pk_bf16_f32 v54, v54, v55
	v_cvt_pk_bf16_f32 v55, v56, v57
	s_waitcnt vmcnt(8)
	v_lshlrev_b32_e32 v56, 16, v156
	v_and_b32_e32 v57, 0xffff0000, v156
	v_pk_add_f32 v[46:47], v[46:47], 1.0 op_sel_hi:[1,0]
	v_exp_f32_e32 v44, v44
	v_exp_f32_e32 v45, v45
	v_pk_mul_f32 v[50:51], v[50:51], v[56:57]
	v_lshlrev_b32_e32 v56, 16, v157
	v_and_b32_e32 v57, 0xffff0000, v157
	v_rcp_f32_e32 v46, v46
	v_rcp_f32_e32 v47, v47
	v_pk_add_f32 v[48:49], v[48:49], 1.0 op_sel_hi:[1,0]
	v_pk_add_f32 v[38:39], v[38:39], v[14:15]
	v_pk_mul_f32 v[52:53], v[52:53], v[56:57]
	v_rcp_f32_e32 v48, v48
	v_rcp_f32_e32 v49, v49
	v_pk_add_f32 v[40:41], v[40:41], v[16:17]
	v_pk_mul_f32 v[38:39], v[38:39], s[14:15] op_sel_hi:[1,0]
	v_cvt_pk_bf16_f32 v50, v50, v51
	v_cvt_pk_bf16_f32 v51, v52, v53
	v_pk_add_f32 v[42:43], v[42:43], 1.0 op_sel_hi:[1,0]
	v_exp_f32_e32 v38, v38
	v_exp_f32_e32 v39, v39
	v_pk_mul_f32 v[40:41], v[40:41], s[14:15] op_sel_hi:[1,0]
	ds_write2_b64 v60, v[54:55], v[50:51] offset0:168 offset1:172
	s_waitcnt vmcnt(7)
	v_lshlrev_b32_e32 v50, 16, v154
	v_and_b32_e32 v51, 0xffff0000, v154
	v_rcp_f32_e32 v42, v42
	v_rcp_f32_e32 v43, v43
	v_pk_add_f32 v[44:45], v[44:45], 1.0 op_sel_hi:[1,0]
	v_exp_f32_e32 v40, v40
	v_exp_f32_e32 v41, v41
	v_pk_add_f32 v[34:35], v[34:35], v[6:7]
	v_pk_mul_f32 v[46:47], v[46:47], v[50:51]
	v_lshlrev_b32_e32 v50, 16, v155
	v_and_b32_e32 v51, 0xffff0000, v155
	v_rcp_f32_e32 v44, v44
	v_rcp_f32_e32 v45, v45
	v_pk_add_f32 v[36:37], v[36:37], v[8:9]
	v_pk_mul_f32 v[34:35], v[34:35], s[14:15] op_sel_hi:[1,0]
	v_pk_mul_f32 v[48:49], v[48:49], v[50:51]
	v_exp_f32_e32 v34, v34
	v_exp_f32_e32 v35, v35
	v_pk_mul_f32 v[36:37], v[36:37], s[14:15] op_sel_hi:[1,0]
	v_cvt_pk_bf16_f32 v46, v46, v47
	v_cvt_pk_bf16_f32 v47, v48, v49
	s_waitcnt vmcnt(6)
	v_lshlrev_b32_e32 v48, 16, v152
	v_and_b32_e32 v49, 0xffff0000, v152
	v_pk_add_f32 v[38:39], v[38:39], 1.0 op_sel_hi:[1,0]
	v_exp_f32_e32 v36, v36
	v_exp_f32_e32 v37, v37
	v_pk_mul_f32 v[42:43], v[42:43], v[48:49]
	v_lshlrev_b32_e32 v48, 16, v153
	v_and_b32_e32 v49, 0xffff0000, v153
	v_rcp_f32_e32 v38, v38
	v_rcp_f32_e32 v39, v39
	v_pk_add_f32 v[40:41], v[40:41], 1.0 op_sel_hi:[1,0]
	v_pk_add_f32 v[28:29], v[28:29], v[32:33]
	v_pk_add_f32 v[26:27], v[26:27], v[30:31]
	v_pk_mul_f32 v[44:45], v[44:45], v[48:49]
	v_rcp_f32_e32 v40, v40
	v_rcp_f32_e32 v41, v41
	v_pk_mul_f32 v[26:27], v[26:27], s[14:15] op_sel_hi:[1,0]
	v_pk_mul_f32 v[28:29], v[28:29], s[14:15] op_sel_hi:[1,0]
	v_cvt_pk_bf16_f32 v42, v42, v43
	v_cvt_pk_bf16_f32 v43, v44, v45
	v_add_u32_e32 v44, 0xc000, v215
	v_pk_add_f32 v[34:35], v[34:35], 1.0 op_sel_hi:[1,0]
	v_exp_f32_e32 v26, v26
	v_exp_f32_e32 v27, v27
	v_exp_f32_e32 v28, v28
	v_exp_f32_e32 v29, v29
	v_pk_add_f32 v[20:21], v[20:21], v[24:25]
	v_pk_add_f32 v[18:19], v[18:19], v[22:23]
	ds_write2_b64 v44, v[46:47], v[42:43] offset0:192 offset1:196
	s_waitcnt vmcnt(5)
	v_lshlrev_b32_e32 v42, 16, v150
	v_and_b32_e32 v43, 0xffff0000, v150
	v_rcp_f32_e32 v34, v34
	v_rcp_f32_e32 v35, v35
	v_pk_add_f32 v[36:37], v[36:37], 1.0 op_sel_hi:[1,0]
	v_pk_mul_f32 v[18:19], v[18:19], s[14:15] op_sel_hi:[1,0]
	v_pk_mul_f32 v[20:21], v[20:21], s[14:15] op_sel_hi:[1,0]
	v_pk_mul_f32 v[38:39], v[38:39], v[42:43]
	v_lshlrev_b32_e32 v42, 16, v151
	v_and_b32_e32 v43, 0xffff0000, v151
	v_rcp_f32_e32 v36, v36
	v_rcp_f32_e32 v37, v37
	v_exp_f32_e32 v18, v18
	v_exp_f32_e32 v19, v19
	v_exp_f32_e32 v20, v20
	v_exp_f32_e32 v21, v21
	v_pk_mul_f32 v[40:41], v[40:41], v[42:43]
	v_pk_add_f32 v[12:13], v[12:13], v[16:17]
	v_pk_add_f32 v[10:11], v[10:11], v[14:15]
	v_cvt_pk_bf16_f32 v38, v38, v39
	v_cvt_pk_bf16_f32 v39, v40, v41
	s_waitcnt vmcnt(4)
	v_lshlrev_b32_e32 v40, 16, v148
	v_and_b32_e32 v41, 0xffff0000, v148
	v_pk_add_f32 v[26:27], v[26:27], 1.0 op_sel_hi:[1,0]
	v_pk_add_f32 v[28:29], v[28:29], 1.0 op_sel_hi:[1,0]
	v_pk_mul_f32 v[10:11], v[10:11], s[14:15] op_sel_hi:[1,0]
	v_pk_mul_f32 v[12:13], v[12:13], s[14:15] op_sel_hi:[1,0]
	v_pk_mul_f32 v[34:35], v[34:35], v[40:41]
	v_lshlrev_b32_e32 v40, 16, v149
	v_and_b32_e32 v41, 0xffff0000, v149
	v_rcp_f32_e32 v26, v26
	v_rcp_f32_e32 v27, v27
	v_rcp_f32_e32 v28, v28
	v_rcp_f32_e32 v29, v29
	v_exp_f32_e32 v10, v10
	v_exp_f32_e32 v11, v11
	v_exp_f32_e32 v12, v12
	v_exp_f32_e32 v13, v13
	v_pk_add_f32 v[4:5], v[4:5], v[8:9]
	v_pk_add_f32 v[2:3], v[2:3], v[6:7]
	v_pk_mul_f32 v[36:37], v[36:37], v[40:41]
	v_pk_add_f32 v[18:19], v[18:19], 1.0 op_sel_hi:[1,0]
	v_pk_add_f32 v[20:21], v[20:21], 1.0 op_sel_hi:[1,0]
	v_pk_mul_f32 v[2:3], v[2:3], s[14:15] op_sel_hi:[1,0]
	v_pk_mul_f32 v[4:5], v[4:5], s[14:15] op_sel_hi:[1,0]
	v_cvt_pk_bf16_f32 v34, v34, v35
	v_cvt_pk_bf16_f32 v35, v36, v37
	v_rcp_f32_e32 v18, v18
	v_rcp_f32_e32 v19, v19
	v_rcp_f32_e32 v20, v20
	v_rcp_f32_e32 v21, v21
	v_exp_f32_e32 v2, v2
	v_exp_f32_e32 v3, v3
	v_exp_f32_e32 v4, v4
	v_exp_f32_e32 v5, v5
	ds_write2_b64 v44, v[38:39], v[34:35] offset0:200 offset1:204
	s_waitcnt vmcnt(3)
	v_lshlrev_b32_e32 v34, 16, v144
	v_and_b32_e32 v35, 0xffff0000, v144
	v_lshlrev_b32_e32 v30, 16, v145
	v_and_b32_e32 v31, 0xffff0000, v145
	v_pk_mul_f32 v[26:27], v[26:27], v[34:35]
	v_pk_mul_f32 v[28:29], v[28:29], v[30:31]
	v_pk_add_f32 v[10:11], v[10:11], 1.0 op_sel_hi:[1,0]
	v_pk_add_f32 v[12:13], v[12:13], 1.0 op_sel_hi:[1,0]
	v_cvt_pk_bf16_f32 v26, v26, v27
	v_cvt_pk_bf16_f32 v27, v28, v29
	s_waitcnt vmcnt(2)
	v_lshlrev_b32_e32 v28, 16, v142
	v_and_b32_e32 v29, 0xffff0000, v142
	v_lshlrev_b32_e32 v22, 16, v143
	v_and_b32_e32 v23, 0xffff0000, v143
	v_rcp_f32_e32 v10, v10
	v_rcp_f32_e32 v11, v11
	v_rcp_f32_e32 v12, v12
	v_rcp_f32_e32 v13, v13
	v_pk_mul_f32 v[18:19], v[18:19], v[28:29]
	v_pk_mul_f32 v[20:21], v[20:21], v[22:23]
	v_pk_add_f32 v[2:3], v[2:3], 1.0 op_sel_hi:[1,0]
	v_pk_add_f32 v[4:5], v[4:5], 1.0 op_sel_hi:[1,0]
	v_cvt_pk_bf16_f32 v18, v18, v19
	v_cvt_pk_bf16_f32 v19, v20, v21
	v_add_u32_e32 v20, 0xe000, v215
	v_rcp_f32_e32 v2, v2
	v_rcp_f32_e32 v3, v3
	v_rcp_f32_e32 v4, v4
	v_rcp_f32_e32 v5, v5
	ds_write2_b64 v20, v[26:27], v[18:19] offset0:224 offset1:228
	s_waitcnt vmcnt(1)
	v_lshlrev_b32_e32 v18, 16, v140
	v_and_b32_e32 v19, 0xffff0000, v140
	v_lshlrev_b32_e32 v14, 16, v141
	v_and_b32_e32 v15, 0xffff0000, v141
	v_pk_mul_f32 v[10:11], v[10:11], v[18:19]
	v_pk_mul_f32 v[12:13], v[12:13], v[14:15]
	v_cvt_pk_bf16_f32 v10, v10, v11
	v_cvt_pk_bf16_f32 v11, v12, v13
	s_waitcnt vmcnt(0)
	v_lshlrev_b32_e32 v12, 16, v138
	v_and_b32_e32 v13, 0xffff0000, v138
	v_lshlrev_b32_e32 v6, 16, v139
	v_and_b32_e32 v7, 0xffff0000, v139
	v_pk_mul_f32 v[2:3], v[2:3], v[12:13]
	v_pk_mul_f32 v[4:5], v[4:5], v[6:7]
	v_cvt_pk_bf16_f32 v2, v2, v3
	v_cvt_pk_bf16_f32 v3, v4, v5
	v_lshl_or_b32 v4, s23, 5, v253
	ds_write2_b64 v20, v[10:11], v[2:3] offset0:232 offset1:236
	v_mul_lo_u32 v2, v4, s18
	s_waitcnt lgkmcnt(0)
	s_barrier
	v_add_u32_e32 v5, v211, v2
	ds_read_b128 v[14:17], v5
	s_waitcnt lgkmcnt(0)
	v_and_b32_e32 v3, 0xffff0000, v14
	v_lshlrev_b32_e32 v2, 16, v14
	v_mul_f32_e32 v3, v3, v3
	v_fmac_f32_e32 v3, v2, v2
	v_lshlrev_b32_e32 v2, 16, v15
	v_fmac_f32_e32 v3, v2, v2
	v_and_b32_e32 v2, 0xffff0000, v15
	v_fmac_f32_e32 v3, v2, v2
	v_lshlrev_b32_e32 v2, 16, v16
	v_fmac_f32_e32 v3, v2, v2
	v_and_b32_e32 v2, 0xffff0000, v16
	v_fmac_f32_e32 v3, v2, v2
	v_lshlrev_b32_e32 v2, 16, v17
	v_fmac_f32_e32 v3, v2, v2
	v_and_b32_e32 v2, 0xffff0000, v17
	v_fmac_f32_e32 v3, v2, v2
	v_and_b32_e32 v2, 64, v214
	v_add_u32_e32 v12, 64, v2
	v_xor_b32_e32 v2, 1, v214
	v_cmp_lt_i32_e64 s[0:1], v2, v12
	s_nop 1
	v_cndmask_b32_e64 v2, v214, v2, s[0:1]
	v_lshlrev_b32_e32 v6, 2, v2
	ds_bpermute_b32 v2, v6, v3
	s_waitcnt lgkmcnt(0)
	v_add_f32_e32 v2, v3, v2
	v_xor_b32_e32 v3, 2, v214
	v_cmp_lt_i32_e64 s[0:1], v3, v12
	s_nop 1
	v_cndmask_b32_e64 v3, v214, v3, s[0:1]
	v_lshlrev_b32_e32 v7, 2, v3
	ds_bpermute_b32 v3, v7, v2
	s_waitcnt lgkmcnt(0)
	v_add_f32_e32 v9, v2, v3
	v_xor_b32_e32 v2, 4, v214
	v_cmp_lt_i32_e64 s[0:1], v2, v12
	s_nop 1
	v_cndmask_b32_e64 v2, v214, v2, s[0:1]
	v_lshlrev_b32_e32 v8, 2, v2
	ds_bpermute_b32 v13, v8, v9
	v_add_u32_e32 v2, s21, v4
	v_ashrrev_i32_e32 v3, 31, v2
	v_lshlrev_b64 v[10:11], 12, v[2:3]
	v_lshl_add_u64 v[10:11], s[8:9], 0, v[10:11]
	s_waitcnt lgkmcnt(0)
	v_add_f32_e32 v13, v9, v13
	v_xor_b32_e32 v9, 8, v214
	v_cmp_lt_i32_e64 s[0:1], v9, v12
	v_lshl_add_u64 v[10:11], v[10:11], 0, s[2:3]
	v_lshl_add_u64 v[18:19], v[10:11], 0, v[146:147]
	v_cndmask_b32_e64 v9, v214, v9, s[0:1]
	v_lshlrev_b32_e32 v9, 2, v9
	ds_bpermute_b32 v20, v9, v13
	v_xor_b32_e32 v10, 16, v214
	v_cmp_lt_i32_e64 s[0:1], v10, v12
	global_store_dwordx4 v[18:19], v[14:17], off sc1
	s_nop 1
	s_waitcnt lgkmcnt(0)
	v_add_f32_e32 v11, v13, v20
	v_cndmask_b32_e64 v10, v214, v10, s[0:1]
	v_lshlrev_b32_e32 v10, 2, v10
	ds_bpermute_b32 v12, v10, v11
	s_and_saveexec_b64 s[0:1], vcc
	s_cbranch_execz .LBB0_1042
	v_lshl_add_u64 v[2:3], v[2:3], 4, s[10:11]
	s_lshl_b32 s22, s20, 2
	s_mov_b32 s23, s3
	s_waitcnt lgkmcnt(0)
	v_add_f32_e32 v11, v11, v12
	v_lshl_add_u64 v[2:3], v[2:3], 0, s[22:23]
	global_store_dword v[2:3], v11, off

.Lrot_o1:
	v_mfma_f32_16x16x32_bf16 v[114:117], v[214:217], v[198:201], v[114:117]
	v_mfma_f32_16x16x32_bf16 v[118:121], v[218:221], v[198:201], v[118:121]
	v_mfma_f32_16x16x32_bf16 v[122:125], v[222:225], v[198:201], v[122:125]
	v_mfma_f32_16x16x32_bf16 v[126:129], v[190:193], v[198:201], v[126:129]
	v_mfma_f32_16x16x32_bf16 v[130:133], v[214:217], v[186:189], v[130:133]
	v_mfma_f32_16x16x32_bf16 v[134:137], v[218:221], v[186:189], v[134:137]
	v_mfma_f32_16x16x32_bf16 v[138:141], v[222:225], v[186:189], v[138:141]
	v_mfma_f32_16x16x32_bf16 v[142:145], v[190:193], v[186:189], v[142:145]
	v_add_u32_e32 v218, s49, v161
	v_add_u32_e32 v224, s50, v155
.Ldef_o1_body:
	ds_read_b64_tr_b16 v[186:187], v154
	ds_read_b64_tr_b16 v[188:189], v154 offset:2048
	ds_read_b64_tr_b16 v[190:191], v185
	ds_read_b64_tr_b16 v[192:193], v185 offset:2048
	ds_read_b128 v[194:197], v218
	ds_read_b128 v[198:201], v218 offset:2048
	ds_read_b64_tr_b16 v[202:203], v224
	ds_read_b64_tr_b16 v[204:205], v224 offset:2048
	v_add_u32_e32 v226, s50, v153
	ds_read_b64_tr_b16 v[206:207], v226
	ds_read_b64_tr_b16 v[208:209], v226 offset:2048
	ds_read_b128 v[210:213], v218 offset:4096
	s_waitcnt lgkmcnt(6)
	v_mfma_f32_16x16x32_bf16 v[18:21], v[186:189], v[194:197], v[18:21]
	s_add_i32 s50, s48, 0
	v_add_u32_e32 v214, 0xfff40000, v152
	s_add_i32 s51, s50, s44
	v_mfma_f32_16x16x32_bf16 v[22:25], v[190:193], v[194:197], v[22:25]
	s_mov_b32 s52, m0
	s_mov_b32 m0, s51
	s_nop 0
	global_load_lds_dwordx4 v214, s[10:11]
	s_mov_b32 m0, s52
	s_waitcnt lgkmcnt(3)
	v_mfma_f32_16x16x32_bf16 v[26:29], v[202:205], v[194:197], v[26:29]
	s_waitcnt lgkmcnt(1)
	v_mfma_f32_16x16x32_bf16 v[30:33], v[206:209], v[194:197], v[30:33]
	v_mfma_f32_16x16x32_bf16 v[34:37], v[186:189], v[198:201], v[34:37]
	ds_read_b128 v[194:197], v218 offset:6144
	v_add_u32_e32 v214, 0xfff80000, v152
	s_add_i32 s51, s50, s45
	v_mfma_f32_16x16x32_bf16 v[38:41], v[190:193], v[198:201], v[38:41]
	s_mov_b32 s52, m0
	s_mov_b32 m0, s51
	s_nop 0
	global_load_lds_dwordx4 v214, s[10:11]
	s_mov_b32 m0, s52
	v_mfma_f32_16x16x32_bf16 v[42:45], v[202:205], v[198:201], v[42:45]
	v_mfma_f32_16x16x32_bf16 v[46:49], v[206:209], v[198:201], v[46:49]
	s_waitcnt lgkmcnt(1)
	v_mfma_f32_16x16x32_bf16 v[50:53], v[186:189], v[210:213], v[50:53]
	ds_read_b128 v[198:201], v218 offset:8192
	v_add_u32_e32 v214, 0xfffc0000, v152
	s_add_i32 s51, s50, s46
	v_mfma_f32_16x16x32_bf16 v[54:57], v[190:193], v[210:213], v[54:57]
	s_mov_b32 s52, m0
	s_mov_b32 m0, s51
	s_nop 0
	global_load_lds_dwordx4 v214, s[10:11]
	s_mov_b32 m0, s52
	v_mfma_f32_16x16x32_bf16 v[58:61], v[202:205], v[210:213], v[58:61]
	v_mfma_f32_16x16x32_bf16 v[62:65], v[206:209], v[210:213], v[62:65]
	s_waitcnt lgkmcnt(1)
	v_mfma_f32_16x16x32_bf16 v[66:69], v[186:189], v[194:197], v[66:69]
	ds_read_b128 v[210:213], v218 offset:10240
	s_add_i32 s50, s50, s47
	s_mov_b32 s51, m0
	s_mov_b32 m0, s50
	s_nop 0
	global_load_lds_dwordx4 v152, s[10:11]
	s_mov_b32 m0, s51
	v_mfma_f32_16x16x32_bf16 v[70:73], v[190:193], v[194:197], v[70:73]
	v_mfma_f32_16x16x32_bf16 v[74:77], v[202:205], v[194:197], v[74:77]
	v_mfma_f32_16x16x32_bf16 v[78:81], v[206:209], v[194:197], v[78:81]
	ds_read_b128 v[194:197], v218 offset:12288
	ds_read_b64_tr_b16 v[214:215], v154 offset:16384
	ds_read_b64_tr_b16 v[216:217], v154 offset:18432
	s_waitcnt lgkmcnt(4)
	v_mfma_f32_16x16x32_bf16 v[82:85], v[186:189], v[198:201], v[82:85]
	v_mfma_f32_16x16x32_bf16 v[86:89], v[190:193], v[198:201], v[86:89]
	v_mfma_f32_16x16x32_bf16 v[90:93], v[202:205], v[198:201], v[90:93]
	v_mfma_f32_16x16x32_bf16 v[94:97], v[206:209], v[198:201], v[94:97]
	ds_read_b128 v[198:201], v218 offset:14336
	ds_read_b64_tr_b16 v[218:219], v185 offset:16384
	ds_read_b64_tr_b16 v[220:221], v185 offset:18432
	s_waitcnt lgkmcnt(6)
	v_mfma_f32_16x16x32_bf16 v[98:101], v[186:189], v[210:213], v[98:101]
	v_mfma_f32_16x16x32_bf16 v[102:105], v[190:193], v[210:213], v[102:105]
	v_mfma_f32_16x16x32_bf16 v[106:109], v[202:205], v[210:213], v[106:109]
	v_mfma_f32_16x16x32_bf16 v[110:113], v[206:209], v[210:213], v[110:113]
	v_add_u32_e32 v154, s49, v162
	ds_read_b128 v[210:213], v154
	ds_read_b64_tr_b16 v[222:223], v224 offset:16384
	ds_read_b64_tr_b16 v[224:225], v224 offset:18432
	s_waitcnt lgkmcnt(8)
	v_mfma_f32_16x16x32_bf16 v[114:117], v[186:189], v[194:197], v[114:117]
	v_mfma_f32_16x16x32_bf16 v[118:121], v[190:193], v[194:197], v[118:121]
	v_mfma_f32_16x16x32_bf16 v[122:125], v[202:205], v[194:197], v[122:125]
	v_mfma_f32_16x16x32_bf16 v[126:129], v[206:209], v[194:197], v[126:129]
	s_waitcnt lgkmcnt(5)
	v_mfma_f32_16x16x32_bf16 v[130:133], v[186:189], v[198:201], v[130:133]
	ds_read_b128 v[186:189], v154 offset:2048
	s_and_b32 s49, s26, 0x8000
	v_mfma_f32_16x16x32_bf16 v[134:137], v[190:193], v[198:201], v[134:137]
	ds_read_b64_tr_b16 v[190:191], v226 offset:16384
	ds_read_b64_tr_b16 v[192:193], v226 offset:18432
	v_mfma_f32_16x16x32_bf16 v[138:141], v[202:205], v[198:201], v[138:141]
	v_mfma_f32_16x16x32_bf16 v[142:145], v[206:209], v[198:201], v[142:145]
	s_waitcnt lgkmcnt(5)
	v_mfma_f32_16x16x32_bf16 v[18:21], v[214:217], v[210:213], v[18:21]
	ds_read_b128 v[194:197], v154 offset:4096
	v_add_u32_e32 v185, s49, v163
	s_add_u32 s49, s6, s4
	v_mfma_f32_16x16x32_bf16 v[22:25], v[218:221], v[210:213], v[22:25]
	s_addc_u32 s52, s7, s5
	s_waitcnt vmcnt(7)
	s_add_u32 s50, s49, 0x80000
	s_waitcnt lgkmcnt(4)
	v_mfma_f32_16x16x32_bf16 v[26:29], v[222:225], v[210:213], v[26:29]
	ds_write_b128 v185, v[14:17]
	s_addc_u32 s51, s52, 0
	global_load_dwordx4 v[14:17], v173, s[50:51]
	s_waitcnt lgkmcnt(2)
	v_mfma_f32_16x16x32_bf16 v[30:33], v[190:193], v[210:213], v[30:33]
	v_mfma_f32_16x16x32_bf16 v[34:37], v[214:217], v[186:189], v[34:37]
	ds_read_b128 v[198:201], v154 offset:6144
	s_waitcnt vmcnt(7)
	s_add_u32 s50, s49, 0x90000
	v_mfma_f32_16x16x32_bf16 v[38:41], v[218:221], v[186:189], v[38:41]
	ds_write_b128 v185, v[10:13] offset:8192
	s_addc_u32 s51, s52, 0
	global_load_dwordx4 v[10:13], v173, s[50:51]
	v_mfma_f32_16x16x32_bf16 v[42:45], v[222:225], v[186:189], v[42:45]
	v_mfma_f32_16x16x32_bf16 v[46:49], v[190:193], v[186:189], v[46:49]
	s_waitcnt lgkmcnt(3)
	v_mfma_f32_16x16x32_bf16 v[50:53], v[214:217], v[194:197], v[50:53]
	ds_read_b128 v[186:189], v154 offset:8192
	s_waitcnt vmcnt(7)
	s_add_u32 s50, s49, 0xa0000
	v_mfma_f32_16x16x32_bf16 v[54:57], v[218:221], v[194:197], v[54:57]
	ds_write_b128 v185, v[6:9] offset:16384
	s_addc_u32 s51, s52, 0
	global_load_dwordx4 v[6:9], v173, s[50:51]
	v_mfma_f32_16x16x32_bf16 v[58:61], v[222:225], v[194:197], v[58:61]
	v_mfma_f32_16x16x32_bf16 v[62:65], v[190:193], v[194:197], v[62:65]
	s_waitcnt lgkmcnt(3)
	v_mfma_f32_16x16x32_bf16 v[66:69], v[214:217], v[198:201], v[66:69]
	ds_read_b128 v[194:197], v154 offset:10240
	s_waitcnt vmcnt(7)
	s_add_u32 s50, s49, 0xb0000
	v_mfma_f32_16x16x32_bf16 v[70:73], v[218:221], v[198:201], v[70:73]
	ds_write_b128 v185, v[2:5] offset:24576
	s_addc_u32 s51, s52, 0
	global_load_dwordx4 v[2:5], v173, s[50:51]
	v_mfma_f32_16x16x32_bf16 v[74:77], v[222:225], v[198:201], v[74:77]
	v_mfma_f32_16x16x32_bf16 v[78:81], v[190:193], v[198:201], v[78:81]
	s_waitcnt lgkmcnt(3)
	v_mfma_f32_16x16x32_bf16 v[82:85], v[214:217], v[186:189], v[82:85]
	ds_read_b128 v[198:201], v154 offset:12288
	v_mfma_f32_16x16x32_bf16 v[86:89], v[218:221], v[186:189], v[86:89]
	v_mfma_f32_16x16x32_bf16 v[90:93], v[222:225], v[186:189], v[90:93]
	v_mfma_f32_16x16x32_bf16 v[94:97], v[190:193], v[186:189], v[94:97]
	s_waitcnt lgkmcnt(2)
	v_mfma_f32_16x16x32_bf16 v[98:101], v[214:217], v[194:197], v[98:101]
	ds_read_b128 v[186:189], v154 offset:14336
	v_mfma_f32_16x16x32_bf16 v[102:105], v[218:221], v[194:197], v[102:105]
	v_mfma_f32_16x16x32_bf16 v[106:109], v[222:225], v[194:197], v[106:109]
	v_mfma_f32_16x16x32_bf16 v[110:113], v[190:193], v[194:197], v[110:113]
	s_waitcnt lgkmcnt(1)
	s_waitcnt lgkmcnt(0)
	s_add_i32 s49, s8, 0x8000
	s_cmp_lg_u32 s8, 0x10000
	s_cselect_b32 s8, s49, 0
	s_add_i32 s49, s48, 0x8000
	s_cmp_lg_u32 s48, 0x10000
	s_cselect_b32 s48, s49, 0
	s_add_u32 s4, s4, 0x40000
	s_addc_u32 s5, s5, 0
	s_add_i32 s26, s26, 0x8000
	v_add_u32_e32 v152, 0x80, v152
	s_add_i32 s50, s26, 0xffff8000
	s_and_b32 s50, s50, 0x8000
	s_add_i32 s50, s50, 0
	s_add_i32 s49, s8, 0
	s_add_i32 s50, s50, 0x18000
	v_add_u32_e32 v154, s50, v157
	v_add_u32_e32 v185, s50, v156
	s_waitcnt lgkmcnt(0)
	s_barrier
	s_cmp_eq_u32 s4, 0x400000
	s_cbranch_scc0 .Lrot_o1
	v_mfma_f32_16x16x32_bf16 v[114:117], v[214:217], v[198:201], v[114:117]
	v_mfma_f32_16x16x32_bf16 v[118:121], v[218:221], v[198:201], v[118:121]
	v_mfma_f32_16x16x32_bf16 v[122:125], v[222:225], v[198:201], v[122:125]
	v_mfma_f32_16x16x32_bf16 v[126:129], v[190:193], v[198:201], v[126:129]
	v_mfma_f32_16x16x32_bf16 v[130:133], v[214:217], v[186:189], v[130:133]
	v_mfma_f32_16x16x32_bf16 v[134:137], v[218:221], v[186:189], v[134:137]
	v_mfma_f32_16x16x32_bf16 v[138:141], v[222:225], v[186:189], v[138:141]
	v_mfma_f32_16x16x32_bf16 v[142:145], v[190:193], v[186:189], v[142:145]
	v_or_b32_e32 v152, v181, v1
	v_lshlrev_b32_e32 v185, 2, v152
	ds_bpermute_b32 v152, v185, v165
	ds_bpermute_b32 v154, v185, v165 offset:64
	ds_bpermute_b32 v186, v185, v165 offset:128
	ds_bpermute_b32 v188, v185, v184 offset:192
	ds_bpermute_b32 v190, v185, v165 offset:192
	ds_bpermute_b32 v192, v185, v184
	ds_bpermute_b32 v194, v185, v184 offset:64
	ds_bpermute_b32 v184, v185, v184 offset:128
	s_mov_b32 s8, 0
	s_waitcnt lgkmcnt(4)
	v_pk_mul_f32 v[144:145], v[144:145], v[188:189] op_sel_hi:[1,0]
	v_pk_mul_f32 v[142:143], v[142:143], v[188:189] op_sel_hi:[1,0]
	v_pk_mul_f32 v[140:141], v[140:141], v[188:189] op_sel_hi:[1,0]
	v_pk_mul_f32 v[138:139], v[138:139], v[188:189] op_sel_hi:[1,0]
	v_pk_mul_f32 v[136:137], v[136:137], v[188:189] op_sel_hi:[1,0]
	v_pk_mul_f32 v[134:135], v[134:135], v[188:189] op_sel_hi:[1,0]
	v_pk_mul_f32 v[132:133], v[132:133], v[188:189] op_sel_hi:[1,0]
	v_pk_mul_f32 v[130:131], v[130:131], v[188:189] op_sel_hi:[1,0]
	s_waitcnt lgkmcnt(0)
	v_pk_mul_f32 v[128:129], v[128:129], v[184:185] op_sel_hi:[1,0]
	v_pk_mul_f32 v[126:127], v[126:127], v[184:185] op_sel_hi:[1,0]
	v_pk_mul_f32 v[124:125], v[124:125], v[184:185] op_sel_hi:[1,0]
	v_pk_mul_f32 v[122:123], v[122:123], v[184:185] op_sel_hi:[1,0]
	v_pk_mul_f32 v[120:121], v[120:121], v[184:185] op_sel_hi:[1,0]
	v_pk_mul_f32 v[118:119], v[118:119], v[184:185] op_sel_hi:[1,0]
	v_pk_mul_f32 v[116:117], v[116:117], v[184:185] op_sel_hi:[1,0]
	v_pk_mul_f32 v[114:115], v[114:115], v[184:185] op_sel_hi:[1,0]
	v_pk_mul_f32 v[112:113], v[112:113], v[194:195] op_sel_hi:[1,0]
	v_pk_mul_f32 v[110:111], v[110:111], v[194:195] op_sel_hi:[1,0]
	v_pk_mul_f32 v[108:109], v[108:109], v[194:195] op_sel_hi:[1,0]
	v_pk_mul_f32 v[106:107], v[106:107], v[194:195] op_sel_hi:[1,0]
	v_pk_mul_f32 v[104:105], v[104:105], v[194:195] op_sel_hi:[1,0]
	v_pk_mul_f32 v[102:103], v[102:103], v[194:195] op_sel_hi:[1,0]
	v_pk_mul_f32 v[100:101], v[100:101], v[194:195] op_sel_hi:[1,0]
	v_pk_mul_f32 v[98:99], v[98:99], v[194:195] op_sel_hi:[1,0]
	v_pk_mul_f32 v[96:97], v[96:97], v[192:193] op_sel_hi:[1,0]
	v_pk_mul_f32 v[94:95], v[94:95], v[192:193] op_sel_hi:[1,0]
	v_pk_mul_f32 v[92:93], v[92:93], v[192:193] op_sel_hi:[1,0]
	v_pk_mul_f32 v[90:91], v[90:91], v[192:193] op_sel_hi:[1,0]
	v_pk_mul_f32 v[88:89], v[88:89], v[192:193] op_sel_hi:[1,0]
	v_pk_mul_f32 v[86:87], v[86:87], v[192:193] op_sel_hi:[1,0]
	v_pk_mul_f32 v[84:85], v[84:85], v[192:193] op_sel_hi:[1,0]
	v_pk_mul_f32 v[82:83], v[82:83], v[192:193] op_sel_hi:[1,0]
	v_pk_mul_f32 v[80:81], v[80:81], v[190:191] op_sel_hi:[1,0]
	v_pk_mul_f32 v[78:79], v[78:79], v[190:191] op_sel_hi:[1,0]
	v_pk_mul_f32 v[76:77], v[76:77], v[190:191] op_sel_hi:[1,0]
	v_pk_mul_f32 v[74:75], v[74:75], v[190:191] op_sel_hi:[1,0]
	v_pk_mul_f32 v[72:73], v[72:73], v[190:191] op_sel_hi:[1,0]
	v_pk_mul_f32 v[70:71], v[70:71], v[190:191] op_sel_hi:[1,0]
	v_pk_mul_f32 v[68:69], v[68:69], v[190:191] op_sel_hi:[1,0]
	v_pk_mul_f32 v[66:67], v[66:67], v[190:191] op_sel_hi:[1,0]
	v_pk_mul_f32 v[64:65], v[64:65], v[186:187] op_sel_hi:[1,0]
	v_pk_mul_f32 v[62:63], v[62:63], v[186:187] op_sel_hi:[1,0]
	v_pk_mul_f32 v[60:61], v[60:61], v[186:187] op_sel_hi:[1,0]
	v_pk_mul_f32 v[58:59], v[58:59], v[186:187] op_sel_hi:[1,0]
	v_pk_mul_f32 v[56:57], v[56:57], v[186:187] op_sel_hi:[1,0]
	v_pk_mul_f32 v[54:55], v[54:55], v[186:187] op_sel_hi:[1,0]
	v_pk_mul_f32 v[52:53], v[52:53], v[186:187] op_sel_hi:[1,0]
	v_pk_mul_f32 v[50:51], v[50:51], v[186:187] op_sel_hi:[1,0]
	v_pk_mul_f32 v[48:49], v[48:49], v[154:155] op_sel_hi:[1,0]
	v_pk_mul_f32 v[46:47], v[46:47], v[154:155] op_sel_hi:[1,0]
	v_pk_mul_f32 v[44:45], v[44:45], v[154:155] op_sel_hi:[1,0]
	v_pk_mul_f32 v[42:43], v[42:43], v[154:155] op_sel_hi:[1,0]
	v_pk_mul_f32 v[40:41], v[40:41], v[154:155] op_sel_hi:[1,0]
	v_pk_mul_f32 v[38:39], v[38:39], v[154:155] op_sel_hi:[1,0]
	v_pk_mul_f32 v[36:37], v[36:37], v[154:155] op_sel_hi:[1,0]
	v_pk_mul_f32 v[34:35], v[34:35], v[154:155] op_sel_hi:[1,0]
	v_pk_mul_f32 v[32:33], v[32:33], v[152:153] op_sel_hi:[1,0]
	v_pk_mul_f32 v[30:31], v[30:31], v[152:153] op_sel_hi:[1,0]
	v_pk_mul_f32 v[28:29], v[28:29], v[152:153] op_sel_hi:[1,0]
	v_pk_mul_f32 v[26:27], v[26:27], v[152:153] op_sel_hi:[1,0]
	v_pk_mul_f32 v[24:25], v[24:25], v[152:153] op_sel_hi:[1,0]
	v_pk_mul_f32 v[22:23], v[22:23], v[152:153] op_sel_hi:[1,0]
	v_pk_mul_f32 v[20:21], v[20:21], v[152:153] op_sel_hi:[1,0]
	v_pk_mul_f32 v[18:19], v[18:19], v[152:153] op_sel_hi:[1,0]
	v_add_u32_e32 v152, v178, v164
	s_mov_b32 s26, 0x8000
	s_mov_b64 s[4:5], 0
	s_mov_b32 s48, 0x88000

.Lrot_o2:
	v_mfma_f32_16x16x32_bf16 v[114:117], v[212:215], v[196:199], v[114:117]
	v_mfma_f32_16x16x32_bf16 v[118:121], v[216:219], v[196:199], v[118:121]
	v_mfma_f32_16x16x32_bf16 v[122:125], v[220:223], v[196:199], v[122:125]
	v_mfma_f32_16x16x32_bf16 v[126:129], v[188:191], v[196:199], v[126:129]
	v_mfma_f32_16x16x32_bf16 v[130:133], v[212:215], v[184:187], v[130:133]
	v_mfma_f32_16x16x32_bf16 v[134:137], v[216:219], v[184:187], v[134:137]
	v_mfma_f32_16x16x32_bf16 v[138:141], v[220:223], v[184:187], v[138:141]
	v_mfma_f32_16x16x32_bf16 v[142:145], v[188:191], v[184:187], v[142:145]
	v_add_u32_e32 v222, s50, v155
.Ldef_o2_body:
	ds_read_b64_tr_b16 v[184:185], v154
	ds_read_b64_tr_b16 v[186:187], v154 offset:2048
	ds_read_b64_tr_b16 v[188:189], v164
	ds_read_b64_tr_b16 v[190:191], v164 offset:2048
	ds_read_b128 v[192:195], v165
	ds_read_b128 v[196:199], v165 offset:2048
	ds_read_b64_tr_b16 v[200:201], v222
	ds_read_b64_tr_b16 v[202:203], v222 offset:2048
	v_add_u32_e32 v224, s50, v153
	ds_read_b64_tr_b16 v[204:205], v224
	ds_read_b64_tr_b16 v[206:207], v224 offset:2048
	ds_read_b128 v[208:211], v165 offset:4096
	s_waitcnt lgkmcnt(6)
	v_mfma_f32_16x16x32_bf16 v[18:21], v[184:187], v[192:195], v[18:21]
	s_add_i32 s50, s8, 0
	v_add_u32_e32 v212, 0xfff40000, v152
	s_add_i32 s51, s50, s44
	v_mfma_f32_16x16x32_bf16 v[22:25], v[188:191], v[192:195], v[22:25]
	s_mov_b32 s52, m0
	s_mov_b32 m0, s51
	s_nop 0
	global_load_lds_dwordx4 v212, s[10:11]
	s_mov_b32 m0, s52
	s_waitcnt lgkmcnt(3)
	v_mfma_f32_16x16x32_bf16 v[26:29], v[200:203], v[192:195], v[26:29]
	s_waitcnt lgkmcnt(1)
	v_mfma_f32_16x16x32_bf16 v[30:33], v[204:207], v[192:195], v[30:33]
	v_mfma_f32_16x16x32_bf16 v[34:37], v[184:187], v[196:199], v[34:37]
	ds_read_b128 v[192:195], v165 offset:6144
	v_add_u32_e32 v212, 0xfff80000, v152
	s_add_i32 s51, s50, s45
	v_mfma_f32_16x16x32_bf16 v[38:41], v[188:191], v[196:199], v[38:41]
	s_mov_b32 s52, m0
	s_mov_b32 m0, s51
	s_nop 0
	global_load_lds_dwordx4 v212, s[10:11]
	s_mov_b32 m0, s52
	v_mfma_f32_16x16x32_bf16 v[42:45], v[200:203], v[196:199], v[42:45]
	v_mfma_f32_16x16x32_bf16 v[46:49], v[204:207], v[196:199], v[46:49]
	s_waitcnt lgkmcnt(1)
	v_mfma_f32_16x16x32_bf16 v[50:53], v[184:187], v[208:211], v[50:53]
	ds_read_b128 v[196:199], v165 offset:8192
	v_add_u32_e32 v212, 0xfffc0000, v152
	s_add_i32 s51, s50, s46
	v_mfma_f32_16x16x32_bf16 v[54:57], v[188:191], v[208:211], v[54:57]
	s_mov_b32 s52, m0
	s_mov_b32 m0, s51
	s_nop 0
	global_load_lds_dwordx4 v212, s[10:11]
	s_mov_b32 m0, s52
	v_mfma_f32_16x16x32_bf16 v[58:61], v[200:203], v[208:211], v[58:61]
	v_mfma_f32_16x16x32_bf16 v[62:65], v[204:207], v[208:211], v[62:65]
	s_waitcnt lgkmcnt(1)
	v_mfma_f32_16x16x32_bf16 v[66:69], v[184:187], v[192:195], v[66:69]
	ds_read_b128 v[208:211], v165 offset:10240
	s_add_i32 s50, s50, s47
	s_mov_b32 s51, m0
	s_mov_b32 m0, s50
	s_nop 0
	global_load_lds_dwordx4 v152, s[10:11]
	s_mov_b32 m0, s51
	v_mfma_f32_16x16x32_bf16 v[70:73], v[188:191], v[192:195], v[70:73]
	v_mfma_f32_16x16x32_bf16 v[74:77], v[200:203], v[192:195], v[74:77]
	v_mfma_f32_16x16x32_bf16 v[78:81], v[204:207], v[192:195], v[78:81]
	ds_read_b128 v[192:195], v165 offset:12288
	ds_read_b64_tr_b16 v[212:213], v154 offset:16384
	ds_read_b64_tr_b16 v[214:215], v154 offset:18432
	s_waitcnt lgkmcnt(4)
	v_mfma_f32_16x16x32_bf16 v[82:85], v[184:187], v[196:199], v[82:85]
	v_mfma_f32_16x16x32_bf16 v[86:89], v[188:191], v[196:199], v[86:89]
	v_mfma_f32_16x16x32_bf16 v[90:93], v[200:203], v[196:199], v[90:93]
	v_mfma_f32_16x16x32_bf16 v[94:97], v[204:207], v[196:199], v[94:97]
	ds_read_b128 v[196:199], v165 offset:14336
	ds_read_b64_tr_b16 v[216:217], v164 offset:16384
	ds_read_b64_tr_b16 v[218:219], v164 offset:18432
	s_waitcnt lgkmcnt(6)
	v_mfma_f32_16x16x32_bf16 v[98:101], v[184:187], v[208:211], v[98:101]
	v_mfma_f32_16x16x32_bf16 v[102:105], v[188:191], v[208:211], v[102:105]
	v_mfma_f32_16x16x32_bf16 v[106:109], v[200:203], v[208:211], v[106:109]
	v_mfma_f32_16x16x32_bf16 v[110:113], v[204:207], v[208:211], v[110:113]
	v_add_u32_e32 v154, s49, v162
	ds_read_b128 v[208:211], v154
	ds_read_b64_tr_b16 v[220:221], v222 offset:16384
	ds_read_b64_tr_b16 v[222:223], v222 offset:18432
	s_waitcnt lgkmcnt(8)
	v_mfma_f32_16x16x32_bf16 v[114:117], v[184:187], v[192:195], v[114:117]
	v_mfma_f32_16x16x32_bf16 v[118:121], v[188:191], v[192:195], v[118:121]
	v_mfma_f32_16x16x32_bf16 v[122:125], v[200:203], v[192:195], v[122:125]
	v_mfma_f32_16x16x32_bf16 v[126:129], v[204:207], v[192:195], v[126:129]
	s_waitcnt lgkmcnt(5)
	v_mfma_f32_16x16x32_bf16 v[130:133], v[184:187], v[196:199], v[130:133]
	ds_read_b128 v[184:187], v154 offset:2048
	s_and_b32 s49, s48, 0x8000
	v_mfma_f32_16x16x32_bf16 v[134:137], v[188:191], v[196:199], v[134:137]
	ds_read_b64_tr_b16 v[188:189], v224 offset:16384
	ds_read_b64_tr_b16 v[190:191], v224 offset:18432
	v_mfma_f32_16x16x32_bf16 v[138:141], v[200:203], v[196:199], v[138:141]
	v_mfma_f32_16x16x32_bf16 v[142:145], v[204:207], v[196:199], v[142:145]
	s_waitcnt lgkmcnt(5)
	v_mfma_f32_16x16x32_bf16 v[18:21], v[212:215], v[208:211], v[18:21]
	ds_read_b128 v[192:195], v154 offset:4096
	v_add_u32_e32 v164, s49, v163
	s_add_u32 s49, s6, s4
	v_mfma_f32_16x16x32_bf16 v[22:25], v[216:219], v[208:211], v[22:25]
	s_addc_u32 s52, s7, s5
	s_waitcnt vmcnt(7)
	s_add_u32 s50, s49, 0x480000
	s_waitcnt lgkmcnt(4)
	v_mfma_f32_16x16x32_bf16 v[26:29], v[220:223], v[208:211], v[26:29]
	ds_write_b128 v164, v[14:17]
	s_addc_u32 s51, s52, 0
	global_load_dwordx4 v[14:17], v173, s[50:51]
	s_waitcnt lgkmcnt(2)
	v_mfma_f32_16x16x32_bf16 v[30:33], v[188:191], v[208:211], v[30:33]
	v_mfma_f32_16x16x32_bf16 v[34:37], v[212:215], v[184:187], v[34:37]
	ds_read_b128 v[196:199], v154 offset:6144
	s_waitcnt vmcnt(7)
	s_add_u32 s50, s49, 0x490000
	v_mfma_f32_16x16x32_bf16 v[38:41], v[216:219], v[184:187], v[38:41]
	ds_write_b128 v164, v[10:13] offset:8192
	s_addc_u32 s51, s52, 0
	global_load_dwordx4 v[10:13], v173, s[50:51]
	v_mfma_f32_16x16x32_bf16 v[42:45], v[220:223], v[184:187], v[42:45]
	v_mfma_f32_16x16x32_bf16 v[46:49], v[188:191], v[184:187], v[46:49]
	s_waitcnt lgkmcnt(3)
	v_mfma_f32_16x16x32_bf16 v[50:53], v[212:215], v[192:195], v[50:53]
	ds_read_b128 v[184:187], v154 offset:8192
	s_waitcnt vmcnt(7)
	s_add_u32 s50, s49, 0x4a0000
	v_mfma_f32_16x16x32_bf16 v[54:57], v[216:219], v[192:195], v[54:57]
	ds_write_b128 v164, v[6:9] offset:16384
	s_addc_u32 s51, s52, 0
	global_load_dwordx4 v[6:9], v173, s[50:51]
	v_mfma_f32_16x16x32_bf16 v[58:61], v[220:223], v[192:195], v[58:61]
	v_mfma_f32_16x16x32_bf16 v[62:65], v[188:191], v[192:195], v[62:65]
	s_waitcnt lgkmcnt(3)
	v_mfma_f32_16x16x32_bf16 v[66:69], v[212:215], v[196:199], v[66:69]
	ds_read_b128 v[192:195], v154 offset:10240
	s_waitcnt vmcnt(7)
	s_add_u32 s50, s49, 0x4b0000
	v_mfma_f32_16x16x32_bf16 v[70:73], v[216:219], v[196:199], v[70:73]
	ds_write_b128 v164, v[2:5] offset:24576
	s_addc_u32 s51, s52, 0
	global_load_dwordx4 v[2:5], v173, s[50:51]
	v_mfma_f32_16x16x32_bf16 v[74:77], v[220:223], v[196:199], v[74:77]
	v_mfma_f32_16x16x32_bf16 v[78:81], v[188:191], v[196:199], v[78:81]
	s_waitcnt lgkmcnt(3)
	v_mfma_f32_16x16x32_bf16 v[82:85], v[212:215], v[184:187], v[82:85]
	ds_read_b128 v[196:199], v154 offset:12288
	v_mfma_f32_16x16x32_bf16 v[86:89], v[216:219], v[184:187], v[86:89]
	v_mfma_f32_16x16x32_bf16 v[90:93], v[220:223], v[184:187], v[90:93]
	v_mfma_f32_16x16x32_bf16 v[94:97], v[188:191], v[184:187], v[94:97]
	s_waitcnt lgkmcnt(2)
	v_mfma_f32_16x16x32_bf16 v[98:101], v[212:215], v[192:195], v[98:101]
	ds_read_b128 v[184:187], v154 offset:14336
	v_mfma_f32_16x16x32_bf16 v[102:105], v[216:219], v[192:195], v[102:105]
	v_mfma_f32_16x16x32_bf16 v[106:109], v[220:223], v[192:195], v[106:109]
	v_mfma_f32_16x16x32_bf16 v[110:113], v[188:191], v[192:195], v[110:113]
	s_waitcnt lgkmcnt(1)
	s_waitcnt lgkmcnt(0)
	s_add_i32 s49, s26, 0x8000
	s_cmp_lg_u32 s26, 0x10000
	s_cselect_b32 s26, s49, 0
	s_add_i32 s49, s8, 0x8000
	s_cmp_lg_u32 s8, 0x10000
	s_cselect_b32 s8, s49, 0
	s_add_u32 s4, s4, 0x40000
	s_addc_u32 s5, s5, 0
	s_add_i32 s48, s48, 0x8000
	v_add_u32_e32 v152, 0x80, v152
	s_add_i32 s50, s48, 0xffff8000
	s_and_b32 s50, s50, 0x8000
	s_add_i32 s50, s50, 0
	s_add_i32 s49, s26, 0
	s_add_i32 s50, s50, 0x18000
	v_add_u32_e32 v154, s50, v157
	v_add_u32_e32 v165, s49, v161
	v_add_u32_e32 v164, s50, v156
	s_waitcnt lgkmcnt(0)
	s_barrier
	s_cmp_lg_u32 s4, 0x380000
	s_cbranch_scc1 .Lrot_o2
	v_mfma_f32_16x16x32_bf16 v[114:117], v[212:215], v[196:199], v[114:117]
	v_mfma_f32_16x16x32_bf16 v[118:121], v[216:219], v[196:199], v[118:121]
	v_mfma_f32_16x16x32_bf16 v[122:125], v[220:223], v[196:199], v[122:125]
	v_mfma_f32_16x16x32_bf16 v[126:129], v[188:191], v[196:199], v[126:129]
	v_mfma_f32_16x16x32_bf16 v[130:133], v[212:215], v[184:187], v[130:133]
	v_mfma_f32_16x16x32_bf16 v[134:137], v[216:219], v[184:187], v[134:137]
	v_mfma_f32_16x16x32_bf16 v[138:141], v[220:223], v[184:187], v[138:141]
	v_mfma_f32_16x16x32_bf16 v[142:145], v[188:191], v[184:187], v[142:145]
	s_add_i32 s4, 0, 0x18000
	v_add_u32_e32 v152, s4, v157
	v_add_u32_e32 v220, 0, v161
	v_add_u32_e32 v161, s4, v155
	v_add_u32_e32 v221, s4, v153
	ds_read_b64_tr_b16 v[184:185], v152
	ds_read_b64_tr_b16 v[186:187], v152 offset:2048
	v_add_u32_e32 v154, s4, v156
	ds_read_b128 v[188:191], v220
	ds_read_b64_tr_b16 v[192:193], v154
	ds_read_b64_tr_b16 v[194:195], v154 offset:2048
	ds_read_b128 v[196:199], v220 offset:2048
	ds_read_b64_tr_b16 v[200:201], v161
	ds_read_b64_tr_b16 v[202:203], v161 offset:2048
	ds_read_b64_tr_b16 v[204:205], v221
	ds_read_b64_tr_b16 v[206:207], v221 offset:2048
	ds_read_b128 v[208:211], v220 offset:4096
	s_waitcnt lgkmcnt(8)
	v_mfma_f32_16x16x32_bf16 v[18:21], v[184:187], v[188:191], v[18:21]
	s_waitcnt lgkmcnt(6)
	v_mfma_f32_16x16x32_bf16 v[22:25], v[192:195], v[188:191], v[22:25]
	s_waitcnt lgkmcnt(3)
	v_mfma_f32_16x16x32_bf16 v[26:29], v[200:203], v[188:191], v[26:29]
	s_waitcnt lgkmcnt(1)
	v_mfma_f32_16x16x32_bf16 v[30:33], v[204:207], v[188:191], v[30:33]
	ds_read_b128 v[188:191], v220 offset:6144
	v_mfma_f32_16x16x32_bf16 v[34:37], v[184:187], v[196:199], v[34:37]
	v_mfma_f32_16x16x32_bf16 v[38:41], v[192:195], v[196:199], v[38:41]
	v_mfma_f32_16x16x32_bf16 v[42:45], v[200:203], v[196:199], v[42:45]
	v_mfma_f32_16x16x32_bf16 v[46:49], v[204:207], v[196:199], v[46:49]
	ds_read_b128 v[196:199], v220 offset:8192
	s_waitcnt lgkmcnt(2)
	v_mfma_f32_16x16x32_bf16 v[50:53], v[184:187], v[208:211], v[50:53]
	v_mfma_f32_16x16x32_bf16 v[54:57], v[192:195], v[208:211], v[54:57]
	v_mfma_f32_16x16x32_bf16 v[58:61], v[200:203], v[208:211], v[58:61]
	v_mfma_f32_16x16x32_bf16 v[62:65], v[204:207], v[208:211], v[62:65]
	ds_read_b128 v[208:211], v220 offset:10240
	s_waitcnt lgkmcnt(2)
	v_mfma_f32_16x16x32_bf16 v[66:69], v[184:187], v[188:191], v[66:69]
	v_mfma_f32_16x16x32_bf16 v[70:73], v[192:195], v[188:191], v[70:73]
	v_mfma_f32_16x16x32_bf16 v[74:77], v[200:203], v[188:191], v[74:77]
	v_mfma_f32_16x16x32_bf16 v[78:81], v[204:207], v[188:191], v[78:81]
	ds_read_b128 v[188:191], v220 offset:12288
	ds_read_b64_tr_b16 v[212:213], v152 offset:16384
	ds_read_b64_tr_b16 v[214:215], v152 offset:18432
	s_waitcnt lgkmcnt(4)
	v_mfma_f32_16x16x32_bf16 v[82:85], v[184:187], v[196:199], v[82:85]
	v_mfma_f32_16x16x32_bf16 v[86:89], v[192:195], v[196:199], v[86:89]
	v_mfma_f32_16x16x32_bf16 v[90:93], v[200:203], v[196:199], v[90:93]
	v_mfma_f32_16x16x32_bf16 v[94:97], v[204:207], v[196:199], v[94:97]
	ds_read_b128 v[196:199], v220 offset:14336
	ds_read_b64_tr_b16 v[216:217], v154 offset:16384
	ds_read_b64_tr_b16 v[218:219], v154 offset:18432
	s_waitcnt lgkmcnt(6)
	v_mfma_f32_16x16x32_bf16 v[98:101], v[184:187], v[208:211], v[98:101]
	v_mfma_f32_16x16x32_bf16 v[102:105], v[192:195], v[208:211], v[102:105]
	v_mfma_f32_16x16x32_bf16 v[106:109], v[200:203], v[208:211], v[106:109]
	v_mfma_f32_16x16x32_bf16 v[110:113], v[204:207], v[208:211], v[110:113]
	v_add_u32_e32 v236, 0, v162
	ds_read_b128 v[162:165], v236
	ds_read_b64_tr_b16 v[208:209], v161 offset:16384
	ds_read_b64_tr_b16 v[210:211], v161 offset:18432
	s_waitcnt lgkmcnt(8)
	v_mfma_f32_16x16x32_bf16 v[114:117], v[184:187], v[188:191], v[114:117]
	v_mfma_f32_16x16x32_bf16 v[118:121], v[192:195], v[188:191], v[118:121]
	v_mfma_f32_16x16x32_bf16 v[122:125], v[200:203], v[188:191], v[122:125]
	v_mfma_f32_16x16x32_bf16 v[126:129], v[204:207], v[188:191], v[126:129]
	s_waitcnt lgkmcnt(5)
	v_mfma_f32_16x16x32_bf16 v[130:133], v[184:187], v[196:199], v[130:133]
	ds_read_b128 v[184:187], v236 offset:2048
	ds_read_b64_tr_b16 v[188:189], v221 offset:16384
	ds_read_b64_tr_b16 v[190:191], v221 offset:18432
	v_mfma_f32_16x16x32_bf16 v[134:137], v[192:195], v[196:199], v[134:137]
	v_mfma_f32_16x16x32_bf16 v[138:141], v[200:203], v[196:199], v[138:141]
	v_mfma_f32_16x16x32_bf16 v[142:145], v[204:207], v[196:199], v[142:145]
	ds_read_b128 v[192:195], v236 offset:4096
	s_waitcnt vmcnt(3)
	v_add_u32_e32 v152, s34, v160
	s_waitcnt lgkmcnt(6)
	v_mfma_f32_16x16x32_bf16 v[18:21], v[212:215], v[162:165], v[18:21]
	ds_write_b128 v152, v[14:17]
	v_mfma_f32_16x16x32_bf16 v[22:25], v[216:219], v[162:165], v[22:25]
	s_waitcnt lgkmcnt(5)
	v_mfma_f32_16x16x32_bf16 v[26:29], v[208:211], v[162:165], v[26:29]
	s_waitcnt lgkmcnt(2)
	v_mfma_f32_16x16x32_bf16 v[14:17], v[188:191], v[162:165], v[30:33]
	v_mfma_f32_16x16x32_bf16 v[30:33], v[212:215], v[184:187], v[34:37]
	v_mfma_f32_16x16x32_bf16 v[34:37], v[216:219], v[184:187], v[38:41]
	v_mfma_f32_16x16x32_bf16 v[38:41], v[208:211], v[184:187], v[42:45]
	s_nop 2
	ds_read_b128 v[42:45], v236 offset:6144
	s_waitcnt vmcnt(2)
	ds_write_b128 v152, v[10:13] offset:8192
	v_mfma_f32_16x16x32_bf16 v[10:13], v[188:191], v[184:187], v[46:49]
	s_waitcnt lgkmcnt(3)
	v_mfma_f32_16x16x32_bf16 v[46:49], v[212:215], v[192:195], v[50:53]
	v_mfma_f32_16x16x32_bf16 v[50:53], v[216:219], v[192:195], v[54:57]
	v_mfma_f32_16x16x32_bf16 v[54:57], v[208:211], v[192:195], v[58:61]
	s_nop 2
	ds_read_b128 v[58:61], v236 offset:8192
	s_waitcnt vmcnt(1)
	ds_write_b128 v152, v[6:9] offset:16384
	v_mfma_f32_16x16x32_bf16 v[6:9], v[188:191], v[192:195], v[62:65]
	s_waitcnt lgkmcnt(3)
	v_mfma_f32_16x16x32_bf16 v[62:65], v[212:215], v[42:45], v[66:69]
	v_mfma_f32_16x16x32_bf16 v[66:69], v[216:219], v[42:45], v[70:73]
	v_mfma_f32_16x16x32_bf16 v[70:73], v[208:211], v[42:45], v[74:77]
	s_nop 2
	ds_read_b128 v[74:77], v236 offset:10240
	s_waitcnt vmcnt(0)
	ds_write_b128 v152, v[2:5] offset:24576
	v_mfma_f32_16x16x32_bf16 v[2:5], v[188:191], v[42:45], v[78:81]
	s_waitcnt lgkmcnt(3)
	v_mfma_f32_16x16x32_bf16 v[78:81], v[216:219], v[58:61], v[86:89]
	s_nop 2
	ds_read_b128 v[86:89], v236 offset:12288
	v_mfma_f32_16x16x32_bf16 v[42:45], v[212:215], v[58:61], v[82:85]
	v_mfma_f32_16x16x32_bf16 v[82:85], v[208:211], v[58:61], v[90:93]
	v_mfma_f32_16x16x32_bf16 v[58:61], v[188:191], v[58:61], v[94:97]
	s_waitcnt lgkmcnt(2)
	v_mfma_f32_16x16x32_bf16 v[94:97], v[216:219], v[74:77], v[102:105]
	s_nop 2
	ds_read_b128 v[102:105], v236 offset:14336
	v_mfma_f32_16x16x32_bf16 v[90:93], v[212:215], v[74:77], v[98:101]
	v_mfma_f32_16x16x32_bf16 v[98:101], v[208:211], v[74:77], v[106:109]
	v_mfma_f32_16x16x32_bf16 v[74:77], v[188:191], v[74:77], v[110:113]
	s_waitcnt lgkmcnt(1)
	v_mfma_f32_16x16x32_bf16 v[106:109], v[212:215], v[86:89], v[114:117]
	v_mfma_f32_16x16x32_bf16 v[110:113], v[216:219], v[86:89], v[118:121]
	v_mfma_f32_16x16x32_bf16 v[114:117], v[208:211], v[86:89], v[122:125]
	v_mfma_f32_16x16x32_bf16 v[86:89], v[188:191], v[86:89], v[126:129]
	s_waitcnt lgkmcnt(0)
	v_mfma_f32_16x16x32_bf16 v[118:121], v[212:215], v[102:105], v[130:133]
	v_mfma_f32_16x16x32_bf16 v[122:125], v[216:219], v[102:105], v[134:137]
	v_mfma_f32_16x16x32_bf16 v[126:129], v[208:211], v[102:105], v[138:141]
	v_mfma_f32_16x16x32_bf16 v[102:105], v[188:191], v[102:105], v[142:145]
	s_waitcnt lgkmcnt(0)
	s_barrier
	v_add_u32_e32 v164, s34, v157
	v_add_u32_e32 v165, s34, v156
	v_add_u32_e32 v198, s34, v155
	ds_read_b64_tr_b16 v[130:131], v164
	ds_read_b64_tr_b16 v[132:133], v164 offset:2048
	ds_read_b64_tr_b16 v[134:135], v165
	ds_read_b64_tr_b16 v[136:137], v165 offset:2048
	ds_read_b128 v[138:141], v220 offset:32768
	ds_read_b64_tr_b16 v[142:143], v198
	ds_read_b128 v[154:157], v220 offset:34816
	ds_read_b128 v[160:163], v220 offset:36864
	ds_read_b64_tr_b16 v[144:145], v198 offset:2048
	v_add_u32_e32 v200, s34, v153
	ds_read_b64_tr_b16 v[184:185], v200
	ds_read_b64_tr_b16 v[186:187], v200 offset:2048
	s_waitcnt lgkmcnt(6)
	v_mfma_f32_16x16x32_bf16 v[18:21], v[130:133], v[138:141], v[18:21]
	v_mfma_f32_16x16x32_bf16 v[22:25], v[134:137], v[138:141], v[22:25]
	s_waitcnt lgkmcnt(2)
	v_mfma_f32_16x16x32_bf16 v[26:29], v[142:145], v[138:141], v[26:29]
	s_waitcnt lgkmcnt(0)
	v_mfma_f32_16x16x32_bf16 v[14:17], v[184:187], v[138:141], v[14:17]
	ds_read_b128 v[138:141], v220 offset:38912
	v_mfma_f32_16x16x32_bf16 v[30:33], v[130:133], v[154:157], v[30:33]
	v_mfma_f32_16x16x32_bf16 v[34:37], v[134:137], v[154:157], v[34:37]
	v_mfma_f32_16x16x32_bf16 v[38:41], v[142:145], v[154:157], v[38:41]
	v_mfma_f32_16x16x32_bf16 v[10:13], v[184:187], v[154:157], v[10:13]
	ds_read_b128 v[152:155], v220 offset:40960
	v_mfma_f32_16x16x32_bf16 v[46:49], v[130:133], v[160:163], v[46:49]
	v_mfma_f32_16x16x32_bf16 v[50:53], v[134:137], v[160:163], v[50:53]
	v_mfma_f32_16x16x32_bf16 v[54:57], v[142:145], v[160:163], v[54:57]
	v_mfma_f32_16x16x32_bf16 v[6:9], v[184:187], v[160:163], v[6:9]
	ds_read_b128 v[160:163], v220 offset:43008
	s_waitcnt lgkmcnt(2)
	v_mfma_f32_16x16x32_bf16 v[62:65], v[130:133], v[138:141], v[62:65]
	v_mfma_f32_16x16x32_bf16 v[66:69], v[134:137], v[138:141], v[66:69]
	v_mfma_f32_16x16x32_bf16 v[70:73], v[142:145], v[138:141], v[70:73]
	v_mfma_f32_16x16x32_bf16 v[2:5], v[184:187], v[138:141], v[2:5]
	s_waitcnt lgkmcnt(1)
	v_mfma_f32_16x16x32_bf16 v[138:141], v[134:137], v[152:155], v[78:81]
	s_nop 2
	ds_read_b128 v[78:81], v220 offset:45056
	ds_read_b64_tr_b16 v[188:189], v164 offset:16384
	ds_read_b64_tr_b16 v[190:191], v164 offset:18432
	v_mfma_f32_16x16x32_bf16 v[42:45], v[130:133], v[152:155], v[42:45]
	v_mfma_f32_16x16x32_bf16 v[82:85], v[142:145], v[152:155], v[82:85]
	v_mfma_f32_16x16x32_bf16 v[152:155], v[184:187], v[152:155], v[58:61]
	s_nop 2
	ds_read_b128 v[58:61], v220 offset:47104
	ds_read_b64_tr_b16 v[192:193], v165 offset:16384
	ds_read_b64_tr_b16 v[194:195], v165 offset:18432
	s_waitcnt lgkmcnt(6)
	v_mfma_f32_16x16x32_bf16 v[90:93], v[130:133], v[160:163], v[90:93]
	v_mfma_f32_16x16x32_bf16 v[94:97], v[134:137], v[160:163], v[94:97]
	v_mfma_f32_16x16x32_bf16 v[98:101], v[142:145], v[160:163], v[98:101]
	v_mfma_f32_16x16x32_bf16 v[160:163], v[184:187], v[160:163], v[74:77]
	s_nop 2
	ds_read_b128 v[74:77], v236 offset:32768
	ds_read_b64_tr_b16 v[196:197], v198 offset:16384
	ds_read_b64_tr_b16 v[198:199], v198 offset:18432
	s_waitcnt lgkmcnt(8)
	v_mfma_f32_16x16x32_bf16 v[106:109], v[130:133], v[78:81], v[106:109]
	v_mfma_f32_16x16x32_bf16 v[110:113], v[134:137], v[78:81], v[110:113]
	v_mfma_f32_16x16x32_bf16 v[114:117], v[142:145], v[78:81], v[114:117]
	v_mfma_f32_16x16x32_bf16 v[86:89], v[184:187], v[78:81], v[86:89]
	s_waitcnt lgkmcnt(5)
	v_mfma_f32_16x16x32_bf16 v[118:121], v[130:133], v[58:61], v[118:121]
	ds_read_b128 v[78:81], v236 offset:34816
	ds_read_b64_tr_b16 v[130:131], v200 offset:16384
	ds_read_b64_tr_b16 v[132:133], v200 offset:18432
	v_mfma_f32_16x16x32_bf16 v[122:125], v[134:137], v[58:61], v[122:125]
	v_mfma_f32_16x16x32_bf16 v[126:129], v[142:145], v[58:61], v[126:129]
	v_mfma_f32_16x16x32_bf16 v[102:105], v[184:187], v[58:61], v[102:105]
	s_waitcnt lgkmcnt(5)
	v_mfma_f32_16x16x32_bf16 v[134:137], v[188:191], v[74:77], v[18:21]
	s_nop 2
	ds_read_b128 v[18:21], v236 offset:36864
	v_mfma_f32_16x16x32_bf16 v[142:145], v[192:195], v[74:77], v[22:25]
	s_waitcnt lgkmcnt(4)
	v_mfma_f32_16x16x32_bf16 v[184:187], v[196:199], v[74:77], v[26:29]
	s_waitcnt lgkmcnt(1)
	v_mfma_f32_16x16x32_bf16 v[14:17], v[130:133], v[74:77], v[14:17]
	ds_read_b128 v[22:25], v236 offset:38912
	v_mfma_f32_16x16x32_bf16 v[200:203], v[188:191], v[78:81], v[30:33]
	v_mfma_f32_16x16x32_bf16 v[204:207], v[192:195], v[78:81], v[34:37]
	v_mfma_f32_16x16x32_bf16 v[208:211], v[196:199], v[78:81], v[38:41]
	v_mfma_f32_16x16x32_bf16 v[10:13], v[130:133], v[78:81], v[10:13]
	ds_read_b128 v[26:29], v236 offset:40960
	s_waitcnt lgkmcnt(2)
	v_mfma_f32_16x16x32_bf16 v[212:215], v[188:191], v[18:21], v[46:49]
	v_mfma_f32_16x16x32_bf16 v[216:219], v[192:195], v[18:21], v[50:53]
	v_mfma_f32_16x16x32_bf16 v[220:223], v[196:199], v[18:21], v[54:57]
	v_mfma_f32_16x16x32_bf16 v[6:9], v[130:133], v[18:21], v[6:9]
	ds_read_b128 v[18:21], v236 offset:43008
	s_waitcnt lgkmcnt(2)
	v_mfma_f32_16x16x32_bf16 v[224:227], v[188:191], v[22:25], v[62:65]
	v_mfma_f32_16x16x32_bf16 v[228:231], v[192:195], v[22:25], v[66:69]
	v_mfma_f32_16x16x32_bf16 v[232:235], v[196:199], v[22:25], v[70:73]
	v_mfma_f32_16x16x32_bf16 v[2:5], v[130:133], v[22:25], v[2:5]
	ds_read_b128 v[22:25], v236 offset:45056
	s_waitcnt lgkmcnt(2)
	v_mfma_f32_16x16x32_bf16 v[78:81], v[188:191], v[26:29], v[42:45]
	v_mfma_f32_16x16x32_bf16 v[74:77], v[192:195], v[26:29], v[138:141]
	v_mfma_f32_16x16x32_bf16 v[58:61], v[196:199], v[26:29], v[82:85]
	v_mfma_f32_16x16x32_bf16 v[62:65], v[130:133], v[26:29], v[152:155]
	s_nop 1
	ds_read_b128 v[82:85], v236 offset:47104
	s_waitcnt lgkmcnt(2)
	v_mfma_f32_16x16x32_bf16 v[70:73], v[188:191], v[18:21], v[90:93]
	v_mfma_f32_16x16x32_bf16 v[66:69], v[192:195], v[18:21], v[94:97]
	v_mfma_f32_16x16x32_bf16 v[50:53], v[196:199], v[18:21], v[98:101]
	v_mfma_f32_16x16x32_bf16 v[54:57], v[130:133], v[18:21], v[160:163]
	s_waitcnt lgkmcnt(1)
	v_mfma_f32_16x16x32_bf16 v[46:49], v[188:191], v[22:25], v[106:109]
	v_mfma_f32_16x16x32_bf16 v[42:45], v[192:195], v[22:25], v[110:113]
	v_mfma_f32_16x16x32_bf16 v[38:41], v[196:199], v[22:25], v[114:117]
	v_mfma_f32_16x16x32_bf16 v[30:33], v[130:133], v[22:25], v[86:89]
	s_waitcnt lgkmcnt(0)
	v_mfma_f32_16x16x32_bf16 v[34:37], v[188:191], v[82:85], v[118:121]
	v_mfma_f32_16x16x32_bf16 v[26:29], v[192:195], v[82:85], v[122:125]
	v_mfma_f32_16x16x32_bf16 v[22:25], v[196:199], v[82:85], v[126:129]
	v_mfma_f32_16x16x32_bf16 v[18:21], v[130:133], v[82:85], v[102:105]
	v_mov_b32_e32 v236, v1
	v_mov_b32_e32 v237, v166
	s_waitcnt lgkmcnt(0)
	s_barrier
	s_lshl_b32 s4, s42, 6
	v_and_or_b32 v82, v236, 63, v181
	v_lshlrev_b32_e32 v122, 2, v82
	ds_bpermute_b32 v82, v122, v183
	v_xor_b32_e32 v239, 0x80, v122
	s_or_b32 s4, s4, s24
	v_lshlrev_b32_e32 v240, 3, v237
	s_waitcnt lgkmcnt(0)
	v_pk_mul_f32 v[162:163], v[136:137], v[82:83] op_sel_hi:[1,0]
	v_pk_mul_f32 v[164:165], v[134:135], v[82:83] op_sel_hi:[1,0]
	v_pk_mul_f32 v[152:153], v[144:145], v[82:83] op_sel_hi:[1,0]
	v_pk_mul_f32 v[154:155], v[142:143], v[82:83] op_sel_hi:[1,0]
	v_add_u32_e32 v83, 16, v236
	v_and_or_b32 v83, v83, 63, v181
	v_lshlrev_b32_e32 v238, 2, v83
	ds_bpermute_b32 v84, v238, v183
	v_pk_mul_f32 v[138:139], v[14:15], v[82:83] op_sel_hi:[1,0]
	ds_bpermute_b32 v14, v239, v183
	v_add_u32_e32 v144, s43, v236
	v_ashrrev_i32_e32 v145, 31, v144
	s_waitcnt lgkmcnt(1)
	v_pk_mul_f32 v[116:117], v[10:11], v[84:85] op_sel_hi:[1,0]
	v_add_u32_e32 v10, 48, v236
	v_and_or_b32 v10, v10, 63, v181
	s_waitcnt lgkmcnt(0)
	v_pk_mul_f32 v[112:113], v[212:213], v[14:15] op_sel_hi:[1,0]
	v_lshlrev_b32_e32 v213, 2, v10
	ds_bpermute_b32 v10, v213, v183
	v_pk_mul_f32 v[98:99], v[8:9], v[14:15] op_sel_hi:[1,0]
	v_lshlrev_b64 v[8:9], 13, v[144:145]
	v_pk_mul_f32 v[118:119], v[208:209], v[84:85] op_sel_hi:[1,0]
	v_pk_mul_f32 v[100:101], v[6:7], v[14:15] op_sel_hi:[1,0]
	s_waitcnt lgkmcnt(0)
	v_pk_mul_f32 v[86:87], v[2:3], v[10:11] op_sel_hi:[1,0]
	v_lshl_add_u32 v2, v237, 2, s4
	s_mul_i32 s4, s41, 0x3000
	s_ashr_i32 s5, s4, 31
	s_lshl_b64 s[4:5], s[4:5], 2
	s_add_u32 s4, s70, s4
	s_addc_u32 s5, s71, s5
	s_add_u32 s4, s4, 0xc000
	v_ashrrev_i32_e32 v3, 31, v2
	ds_bpermute_b32 v208, v122, v182
	s_addc_u32 s5, s5, 0
	v_lshlrev_b64 v[122:123], 2, v[2:3]
	v_add_u32_e32 v6, 16, v2
	v_lshl_add_u64 v[8:9], s[12:13], 0, v[8:9]
	v_pk_mul_f32 v[128:129], v[202:203], v[84:85] op_sel_hi:[1,0]
	v_pk_mul_f32 v[130:131], v[200:201], v[84:85] op_sel_hi:[1,0]
	v_pk_mul_f32 v[124:125], v[206:207], v[84:85] op_sel_hi:[1,0]
	v_pk_mul_f32 v[126:127], v[204:205], v[84:85] op_sel_hi:[1,0]
	v_pk_mul_f32 v[120:121], v[210:211], v[84:85] op_sel_hi:[1,0]
	v_pk_mul_f32 v[114:115], v[12:13], v[84:85] op_sel_hi:[1,0]
	v_pk_mul_f32 v[84:85], v[4:5], v[10:11] op_sel_hi:[1,0]
	v_lshl_add_u64 v[4:5], s[4:5], 0, v[122:123]
	v_ashrrev_i32_e32 v7, 31, v6
	v_lshl_add_u64 v[132:133], v[8:9], 0, v[122:123]
	v_pk_mul_f32 v[156:157], v[186:187], v[82:83] op_sel_hi:[1,0]
	v_pk_mul_f32 v[160:161], v[184:185], v[82:83] op_sel_hi:[1,0]
	v_pk_mul_f32 v[136:137], v[16:17], v[82:83] op_sel_hi:[1,0]
	v_pk_mul_f32 v[110:111], v[214:215], v[14:15] op_sel_hi:[1,0]
	v_pk_mul_f32 v[106:107], v[218:219], v[14:15] op_sel_hi:[1,0]
	v_pk_mul_f32 v[108:109], v[216:217], v[14:15] op_sel_hi:[1,0]
	v_pk_mul_f32 v[102:103], v[222:223], v[14:15] op_sel_hi:[1,0]
	v_pk_mul_f32 v[104:105], v[220:221], v[14:15] op_sel_hi:[1,0]
	v_pk_mul_f32 v[94:95], v[226:227], v[10:11] op_sel_hi:[1,0]
	v_pk_mul_f32 v[96:97], v[224:225], v[10:11] op_sel_hi:[1,0]
	v_pk_mul_f32 v[90:91], v[230:231], v[10:11] op_sel_hi:[1,0]
	v_pk_mul_f32 v[92:93], v[228:229], v[10:11] op_sel_hi:[1,0]
	v_pk_mul_f32 v[88:89], v[234:235], v[10:11] op_sel_hi:[1,0]
	v_pk_mul_f32 v[82:83], v[232:233], v[10:11] op_sel_hi:[1,0]
	v_lshl_add_u64 v[6:7], v[6:7], 2, s[4:5]
	global_load_dwordx4 v[184:187], v[132:133], off nt
	global_load_dwordx4 v[14:17], v[4:5], off
	global_load_dwordx4 v[10:13], v[6:7], off
	v_add_u32_e32 v4, 32, v2
	v_add_u32_e32 v2, 48, v2
	v_ashrrev_i32_e32 v5, 31, v4
	v_ashrrev_i32_e32 v3, 31, v2
	v_lshl_add_u64 v[4:5], v[4:5], 2, s[4:5]
	v_lshl_add_u64 v[2:3], v[2:3], 2, s[4:5]
	global_load_dwordx4 v[188:191], v[132:133], off offset:64 nt
	global_load_dwordx4 v[192:195], v[132:133], off offset:128 nt
	global_load_dwordx4 v[6:9], v[4:5], off
	s_nop 0
	global_load_dwordx4 v[2:5], v[2:3], off
	s_nop 0
	global_load_dwordx4 v[196:199], v[132:133], off offset:192 nt
	v_add_u32_e32 v132, 16, v144
	ds_bpermute_b32 v212, v238, v182
	ds_bpermute_b32 v216, v239, v182
	v_ashrrev_i32_e32 v133, 31, v132
	v_lshlrev_b64 v[132:133], 13, v[132:133]
	v_lshl_add_u64 v[132:133], s[12:13], 0, v[132:133]
	v_lshl_add_u64 v[210:211], v[132:133], 0, v[122:123]
	global_load_dwordx4 v[200:203], v[210:211], off nt
	global_load_dwordx4 v[204:207], v[210:211], off offset:64 nt
	s_waitcnt lgkmcnt(2)
	v_pk_mul_f32 v[142:143], v[78:79], v[208:209] op_sel_hi:[1,0]
	v_pk_mul_f32 v[78:79], v[60:61], v[208:209] op_sel_hi:[1,0]
	s_waitcnt lgkmcnt(1)
	v_pk_mul_f32 v[60:61], v[50:51], v[212:213] op_sel_hi:[1,0]
	s_waitcnt lgkmcnt(0)
	v_pk_mul_f32 v[50:51], v[48:49], v[216:217] op_sel_hi:[1,0]
	v_pk_mul_f32 v[48:49], v[42:43], v[216:217] op_sel_hi:[1,0]
	v_add_u32_e32 v42, 32, v144
	ds_bpermute_b32 v182, v213, v182
	v_ashrrev_i32_e32 v43, 31, v42
	v_pk_mul_f32 v[132:133], v[76:77], v[208:209] op_sel_hi:[1,0]
	v_pk_mul_f32 v[134:135], v[74:75], v[208:209] op_sel_hi:[1,0]
	v_pk_mul_f32 v[74:75], v[64:65], v[208:209] op_sel_hi:[1,0]
	v_pk_mul_f32 v[76:77], v[62:63], v[208:209] op_sel_hi:[1,0]
	v_pk_mul_f32 v[62:63], v[68:69], v[212:213] op_sel_hi:[1,0]
	v_pk_mul_f32 v[64:65], v[66:67], v[212:213] op_sel_hi:[1,0]
	global_load_dwordx4 v[66:69], v[210:211], off offset:128 nt
	v_lshlrev_b64 v[42:43], 13, v[42:43]
	v_lshl_add_u64 v[42:43], s[12:13], 0, v[42:43]
	v_lshl_add_u64 v[220:221], v[42:43], 0, v[122:123]
	v_pk_mul_f32 v[140:141], v[80:81], v[208:209] op_sel_hi:[1,0]
	v_pk_mul_f32 v[80:81], v[58:59], v[208:209] op_sel_hi:[1,0]
	v_pk_mul_f32 v[72:73], v[72:73], v[212:213] op_sel_hi:[1,0]
	v_pk_mul_f32 v[70:71], v[70:71], v[212:213] op_sel_hi:[1,0]
	v_pk_mul_f32 v[58:59], v[52:53], v[212:213] op_sel_hi:[1,0]
	v_pk_mul_f32 v[56:57], v[56:57], v[212:213] op_sel_hi:[1,0]
	v_pk_mul_f32 v[54:55], v[54:55], v[212:213] op_sel_hi:[1,0]
	global_load_dwordx4 v[212:215], v[220:221], off nt
	v_pk_mul_f32 v[52:53], v[46:47], v[216:217] op_sel_hi:[1,0]
	global_load_dwordx4 v[208:211], v[210:211], off offset:192 nt
	v_pk_mul_f32 v[46:47], v[44:45], v[216:217] op_sel_hi:[1,0]
	v_pk_mul_f32 v[42:43], v[32:33], v[216:217] op_sel_hi:[1,0]
	v_pk_mul_f32 v[44:45], v[30:31], v[216:217] op_sel_hi:[1,0]
	s_waitcnt lgkmcnt(0)
	v_pk_mul_f32 v[30:31], v[36:37], v[182:183] op_sel_hi:[1,0]
	v_pk_mul_f32 v[32:33], v[34:35], v[182:183] op_sel_hi:[1,0]
	global_load_dwordx4 v[34:37], v[220:221], off offset:64 nt
	v_pk_mul_f32 v[40:41], v[40:41], v[216:217] op_sel_hi:[1,0]
	v_pk_mul_f32 v[38:39], v[38:39], v[216:217] op_sel_hi:[1,0]
	global_load_dwordx4 v[216:219], v[220:221], off offset:128 nt
	s_nop 0
	global_load_dwordx4 v[220:223], v[220:221], off offset:192 nt
	v_pk_mul_f32 v[28:29], v[28:29], v[182:183] op_sel_hi:[1,0]
	v_pk_mul_f32 v[26:27], v[26:27], v[182:183] op_sel_hi:[1,0]
	v_pk_mul_f32 v[24:25], v[24:25], v[182:183] op_sel_hi:[1,0]
	v_pk_mul_f32 v[22:23], v[22:23], v[182:183] op_sel_hi:[1,0]
	v_pk_mul_f32 v[20:21], v[20:21], v[182:183] op_sel_hi:[1,0]
	v_pk_mul_f32 v[18:19], v[18:19], v[182:183] op_sel_hi:[1,0]
	v_add_u32_e32 v182, 48, v144
	v_ashrrev_i32_e32 v183, 31, v182
	v_lshlrev_b64 v[182:183], 13, v[182:183]
	v_lshl_add_u64 v[182:183], s[12:13], 0, v[182:183]
	v_lshl_add_u64 v[182:183], v[182:183], 0, v[122:123]
	v_add_u32_e32 v145, s39, v236
	global_load_dwordx4 v[224:227], v[182:183], off nt
	global_load_dwordx4 v[228:231], v[182:183], off offset:64 nt
	global_load_dwordx4 v[232:235], v[182:183], off offset:128 nt
	global_load_dwordx4 v[236:239], v[182:183], off offset:192 nt
	s_add_i32 s40, s40, 0
	v_mul_lo_u32 v145, v145, s35
	v_add3_u32 v240, s40, v240, v145
	v_add_u32_e32 v145, 0x2000, v240
	s_andn2_b64 vcc, exec, s[76:77]
	s_waitcnt vmcnt(18)
	v_pk_fma_f32 v[162:163], v[162:163], v[16:17], v[186:187]
	v_pk_fma_f32 v[164:165], v[164:165], v[14:15], v[184:185]
	s_waitcnt vmcnt(16)
	v_pk_fma_f32 v[152:153], v[152:153], v[12:13], v[190:191]
	v_pk_fma_f32 v[154:155], v[154:155], v[10:11], v[188:189]
	v_cvt_pk_bf16_f32 v164, v164, v165
	v_cvt_pk_bf16_f32 v165, v162, v163
	v_cvt_pk_bf16_f32 v154, v154, v155
	v_cvt_pk_bf16_f32 v155, v152, v153
	ds_write2_b64 v240, v[164:165], v[154:155] offset1:4
	s_waitcnt vmcnt(14)
	v_pk_fma_f32 v[152:153], v[156:157], v[8:9], v[194:195]
	v_pk_fma_f32 v[154:155], v[160:161], v[6:7], v[192:193]
	s_waitcnt vmcnt(12)
	v_pk_fma_f32 v[136:137], v[136:137], v[4:5], v[198:199]
	v_pk_fma_f32 v[138:139], v[138:139], v[2:3], v[196:197]
	s_waitcnt vmcnt(11)
	v_pk_fma_f32 v[128:129], v[128:129], v[16:17], v[202:203]
	v_pk_fma_f32 v[130:131], v[130:131], v[14:15], v[200:201]
	s_waitcnt vmcnt(10)
	v_pk_fma_f32 v[124:125], v[124:125], v[12:13], v[206:207]
	v_cvt_pk_bf16_f32 v130, v130, v131
	v_cvt_pk_bf16_f32 v131, v128, v129
	v_cvt_pk_bf16_f32 v129, v124, v125
	v_add_u32_e32 v124, 64, v144
	v_ashrrev_i32_e32 v125, 31, v124
	v_lshlrev_b64 v[124:125], 13, v[124:125]
	v_pk_fma_f32 v[126:127], v[126:127], v[10:11], v[204:205]
	v_lshl_add_u64 v[124:125], s[12:13], 0, v[124:125]
	v_cvt_pk_bf16_f32 v154, v154, v155
	v_cvt_pk_bf16_f32 v155, v152, v153
	v_cvt_pk_bf16_f32 v138, v138, v139
	v_cvt_pk_bf16_f32 v139, v136, v137
	v_cvt_pk_bf16_f32 v128, v126, v127
	s_waitcnt vmcnt(9)
	v_pk_fma_f32 v[66:67], v[118:119], v[6:7], v[66:67]
	v_add_u32_e32 v118, 0x50, v144
	v_ashrrev_i32_e32 v119, 31, v118
	v_lshlrev_b64 v[118:119], 13, v[118:119]
	v_lshl_add_u64 v[136:137], v[124:125], 0, v[122:123]
	v_pk_fma_f32 v[68:69], v[120:121], v[8:9], v[68:69]
	v_lshl_add_u64 v[118:119], s[12:13], 0, v[118:119]
	ds_write2_b64 v240, v[154:155], v[138:139] offset0:8 offset1:12
	global_load_dwordx4 v[124:127], v[136:137], off nt
	ds_write2_b64 v145, v[130:131], v[128:129] offset0:32 offset1:36
	global_load_dwordx4 v[128:131], v[136:137], off offset:64 nt
	v_cvt_pk_bf16_f32 v138, v66, v67
	v_cvt_pk_bf16_f32 v139, v68, v69
	s_waitcnt vmcnt(9)
	v_pk_fma_f32 v[114:115], v[114:115], v[4:5], v[210:211]
	v_pk_fma_f32 v[116:117], v[116:117], v[2:3], v[208:209]
	global_load_dwordx4 v[66:69], v[136:137], off offset:128 nt
	v_cvt_pk_bf16_f32 v152, v116, v117
	v_cvt_pk_bf16_f32 v153, v114, v115
	global_load_dwordx4 v[114:117], v[136:137], off offset:192 nt
	v_lshl_add_u64 v[136:137], v[118:119], 0, v[122:123]
	s_waitcnt vmcnt(10)
	v_pk_fma_f32 v[106:107], v[106:107], v[12:13], v[36:37]
	v_pk_fma_f32 v[34:35], v[108:109], v[10:11], v[34:35]
	global_load_dwordx4 v[118:121], v[136:137], off nt
	ds_write2_b64 v145, v[138:139], v[152:153] offset0:40 offset1:44
	v_pk_fma_f32 v[138:139], v[110:111], v[16:17], v[214:215]
	v_pk_fma_f32 v[152:153], v[112:113], v[14:15], v[212:213]
	global_load_dwordx4 v[110:113], v[136:137], off offset:64 nt
	v_cvt_pk_bf16_f32 v154, v34, v35
	global_load_dwordx4 v[34:37], v[136:137], off offset:128 nt
	v_cvt_pk_bf16_f32 v155, v106, v107
	global_load_dwordx4 v[106:109], v[136:137], off offset:192 nt
	v_add_u32_e32 v136, 0x60, v144
	v_cvt_pk_bf16_f32 v152, v152, v153
	v_cvt_pk_bf16_f32 v153, v138, v139
	v_add_u32_e32 v145, 0x4000, v240
	v_ashrrev_i32_e32 v137, 31, v136
	v_lshlrev_b64 v[136:137], 13, v[136:137]
	ds_write2_b64 v145, v[152:153], v[154:155] offset0:64 offset1:68
	s_waitcnt vmcnt(13)
	v_pk_fma_f32 v[152:153], v[102:103], v[8:9], v[218:219]
	v_pk_fma_f32 v[154:155], v[104:105], v[6:7], v[216:217]
	v_lshl_add_u64 v[136:137], s[12:13], 0, v[136:137]
	v_cvt_pk_bf16_f32 v154, v154, v155
	v_cvt_pk_bf16_f32 v155, v152, v153
	s_waitcnt vmcnt(12)
	v_pk_fma_f32 v[152:153], v[98:99], v[4:5], v[222:223]
	v_pk_fma_f32 v[98:99], v[100:101], v[2:3], v[220:221]
	v_lshl_add_u64 v[156:157], v[136:137], 0, v[122:123]
	v_cvt_pk_bf16_f32 v160, v98, v99
	v_cvt_pk_bf16_f32 v161, v152, v153
	v_add_u32_e32 v144, 0x70, v144
	global_load_dwordx4 v[136:139], v[156:157], off nt
	global_load_dwordx4 v[102:105], v[156:157], off offset:64 nt
	ds_write2_b64 v145, v[154:155], v[160:161] offset0:72 offset1:76
	v_ashrrev_i32_e32 v145, 31, v144
	v_lshlrev_b64 v[144:145], 13, v[144:145]
	v_lshl_add_u64 v[144:145], s[12:13], 0, v[144:145]
	global_load_dwordx4 v[98:101], v[156:157], off offset:128 nt
	global_load_dwordx4 v[152:155], v[156:157], off offset:192 nt
	v_lshl_add_u64 v[122:123], v[144:145], 0, v[122:123]
	s_waitcnt vmcnt(15)
	v_pk_fma_f32 v[144:145], v[94:95], v[16:17], v[226:227]
	v_pk_fma_f32 v[94:95], v[96:97], v[14:15], v[224:225]
	s_waitcnt vmcnt(14)
	v_pk_fma_f32 v[90:91], v[90:91], v[12:13], v[230:231]
	v_pk_fma_f32 v[92:93], v[92:93], v[10:11], v[228:229]
	global_load_dwordx4 v[160:163], v[122:123], off nt
	v_cvt_pk_bf16_f32 v156, v94, v95
	global_load_dwordx4 v[94:97], v[122:123], off offset:64 nt
	v_cvt_pk_bf16_f32 v157, v144, v145
	v_cvt_pk_bf16_f32 v144, v92, v93
	v_cvt_pk_bf16_f32 v145, v90, v91
	global_load_dwordx4 v[90:93], v[122:123], off offset:128 nt
	global_load_dwordx4 v[182:185], v[122:123], off offset:192 nt
	s_waitcnt vmcnt(17)
	v_pk_fma_f32 v[88:89], v[88:89], v[8:9], v[234:235]
	v_pk_fma_f32 v[82:83], v[82:83], v[6:7], v[232:233]
	s_waitcnt vmcnt(16)
	v_pk_fma_f32 v[84:85], v[84:85], v[4:5], v[238:239]
	v_pk_fma_f32 v[86:87], v[86:87], v[2:3], v[236:237]
	v_add_u32_e32 v164, 0x6000, v240
	v_cvt_pk_bf16_f32 v82, v82, v83
	v_cvt_pk_bf16_f32 v83, v88, v89
	v_cvt_pk_bf16_f32 v86, v86, v87
	v_cvt_pk_bf16_f32 v87, v84, v85
	ds_write2_b64 v164, v[82:83], v[86:87] offset0:104 offset1:108
	ds_write2_b64 v164, v[156:157], v[144:145] offset0:96 offset1:100
	s_waitcnt vmcnt(15)
	v_pk_fma_f32 v[82:83], v[140:141], v[16:17], v[126:127]
	v_pk_fma_f32 v[84:85], v[142:143], v[14:15], v[124:125]
	s_waitcnt vmcnt(14)
	v_pk_fma_f32 v[86:87], v[134:135], v[10:11], v[128:129]
	v_cvt_pk_bf16_f32 v84, v84, v85
	v_cvt_pk_bf16_f32 v85, v82, v83
	v_pk_fma_f32 v[82:83], v[132:133], v[12:13], v[130:131]
	v_cvt_pk_bf16_f32 v86, v86, v87
	s_waitcnt vmcnt(13)
	v_pk_fma_f32 v[68:69], v[78:79], v[8:9], v[68:69]
	v_pk_fma_f32 v[66:67], v[80:81], v[6:7], v[66:67]
	v_cvt_pk_bf16_f32 v87, v82, v83
	v_cvt_pk_bf16_f32 v66, v66, v67
	v_cvt_pk_bf16_f32 v67, v68, v69
	s_waitcnt vmcnt(12)
	v_pk_fma_f32 v[68:69], v[74:75], v[4:5], v[116:117]
	v_pk_fma_f32 v[74:75], v[76:77], v[2:3], v[114:115]
	v_add_u32_e32 v82, 0x8000, v240
	v_cvt_pk_bf16_f32 v74, v74, v75
	v_cvt_pk_bf16_f32 v75, v68, v69
	ds_write2_b64 v82, v[66:67], v[74:75] offset0:136 offset1:140
	s_waitcnt vmcnt(10)
	v_pk_fma_f32 v[62:63], v[62:63], v[12:13], v[112:113]
	v_pk_fma_f32 v[64:65], v[64:65], v[10:11], v[110:111]
	s_waitcnt vmcnt(9)
	v_pk_fma_f32 v[36:37], v[58:59], v[8:9], v[36:37]
	v_pk_fma_f32 v[34:35], v[60:61], v[6:7], v[34:35]
	s_waitcnt vmcnt(8)
	v_pk_fma_f32 v[54:55], v[54:55], v[2:3], v[106:107]
	v_cvt_pk_bf16_f32 v34, v34, v35
	v_cvt_pk_bf16_f32 v35, v36, v37
	v_pk_fma_f32 v[36:37], v[56:57], v[4:5], v[108:109]
	v_cvt_pk_bf16_f32 v64, v64, v65
	v_cvt_pk_bf16_f32 v65, v62, v63
	v_add_u32_e32 v62, 0xa000, v240
	v_cvt_pk_bf16_f32 v54, v54, v55
	v_cvt_pk_bf16_f32 v55, v36, v37
	ds_write2_b64 v62, v[34:35], v[54:55] offset0:168 offset1:172
	v_pk_fma_f32 v[66:67], v[16:17], v[72:73], v[120:121]
	v_pk_fma_f32 v[68:69], v[14:15], v[70:71], v[118:119]
	ds_write2_b64 v82, v[84:85], v[86:87] offset0:128 offset1:132
	v_cvt_pk_bf16_f32 v68, v68, v69
	v_cvt_pk_bf16_f32 v69, v66, v67
	ds_write2_b64 v62, v[68:69], v[64:65] offset0:160 offset1:164
	s_waitcnt vmcnt(7)
	v_pk_fma_f32 v[34:35], v[16:17], v[50:51], v[138:139]
	v_pk_fma_f32 v[36:37], v[14:15], v[52:53], v[136:137]
	s_waitcnt vmcnt(3)
	v_pk_fma_f32 v[16:17], v[16:17], v[30:31], v[162:163]
	v_cvt_pk_bf16_f32 v36, v36, v37
	v_cvt_pk_bf16_f32 v37, v34, v35
	v_pk_fma_f32 v[34:35], v[12:13], v[46:47], v[104:105]
	v_pk_fma_f32 v[46:47], v[10:11], v[48:49], v[102:103]
	v_add_u32_e32 v48, 0xc000, v240
	v_cvt_pk_bf16_f32 v46, v46, v47
	v_cvt_pk_bf16_f32 v47, v34, v35
	ds_write2_b64 v48, v[36:37], v[46:47] offset0:192 offset1:196
	v_pk_fma_f32 v[34:35], v[40:41], v[8:9], v[100:101]
	v_pk_fma_f32 v[36:37], v[38:39], v[6:7], v[98:99]
	v_pk_fma_f32 v[38:39], v[44:45], v[2:3], v[152:153]
	v_cvt_pk_bf16_f32 v36, v36, v37
	v_cvt_pk_bf16_f32 v37, v34, v35
	v_pk_fma_f32 v[34:35], v[42:43], v[4:5], v[154:155]
	s_waitcnt vmcnt(2)
	v_pk_fma_f32 v[12:13], v[12:13], v[28:29], v[96:97]
	v_pk_fma_f32 v[10:11], v[10:11], v[26:27], v[94:95]
	s_waitcnt vmcnt(1)
	v_pk_fma_f32 v[8:9], v[8:9], v[24:25], v[92:93]
	v_pk_fma_f32 v[6:7], v[6:7], v[22:23], v[90:91]
	s_waitcnt vmcnt(0)
	v_pk_fma_f32 v[4:5], v[20:21], v[4:5], v[184:185]
	v_pk_fma_f32 v[2:3], v[18:19], v[2:3], v[182:183]
	v_cvt_pk_bf16_f32 v10, v10, v11
	v_cvt_pk_bf16_f32 v11, v12, v13
	v_add_u32_e32 v12, 0xe000, v240
	v_cvt_pk_bf16_f32 v6, v6, v7
	v_cvt_pk_bf16_f32 v7, v8, v9
	v_cvt_pk_bf16_f32 v2, v2, v3
	v_cvt_pk_bf16_f32 v3, v4, v5
	v_lshl_or_b32 v8, s38, 5, v167
	v_pk_fma_f32 v[14:15], v[14:15], v[32:33], v[160:161]
	ds_write2_b64 v12, v[6:7], v[2:3] offset0:232 offset1:236
	v_mad_u64_u32 v[6:7], s[4:5], v8, s35, v[148:149]
	v_add_u32_e32 v8, s25, v8
	v_cvt_pk_bf16_f32 v14, v14, v15
	v_cvt_pk_bf16_f32 v15, v16, v17
	v_ashrrev_i32_e32 v9, 31, v8
	ds_write2_b64 v12, v[14:15], v[10:11] offset0:224 offset1:228
	v_lshlrev_b64 v[10:11], 12, v[8:9]
	v_cvt_pk_bf16_f32 v38, v38, v39
	v_cvt_pk_bf16_f32 v39, v34, v35
	v_lshl_add_u64 v[10:11], s[18:19], 0, v[10:11]
	ds_write2_b64 v48, v[36:37], v[38:39] offset0:200 offset1:204
	v_lshl_add_u64 v[10:11], v[10:11], 0, s[22:23]
	s_waitcnt lgkmcnt(0)
	s_barrier
	v_lshl_add_u64 v[10:11], v[10:11], 0, v[146:147]
	ds_read_b128 v[2:5], v6
	s_waitcnt lgkmcnt(0)
	global_store_dwordx4 v[10:11], v[2:5], off sc1
	s_nop 1
	v_add_u32_e32 v10, 2, v8
	v_ashrrev_i32_e32 v11, 31, v10
	v_lshlrev_b64 v[10:11], 12, v[10:11]
	v_lshl_add_u64 v[10:11], s[18:19], 0, v[10:11]
	v_lshl_add_u64 v[10:11], v[10:11], 0, s[22:23]
	v_lshl_add_u64 v[10:11], v[10:11], 0, v[146:147]
	ds_read_b128 v[2:5], v6 offset:1056
	s_waitcnt lgkmcnt(0)
	global_store_dwordx4 v[10:11], v[2:5], off sc1
	s_nop 1
	v_add_u32_e32 v10, 4, v8
	v_ashrrev_i32_e32 v11, 31, v10
	v_lshlrev_b64 v[10:11], 12, v[10:11]
	v_lshl_add_u64 v[10:11], s[18:19], 0, v[10:11]
	v_lshl_add_u64 v[10:11], v[10:11], 0, s[22:23]
	v_lshl_add_u64 v[10:11], v[10:11], 0, v[146:147]
	ds_read_b128 v[2:5], v6 offset:2112
	s_waitcnt lgkmcnt(0)
	global_store_dwordx4 v[10:11], v[2:5], off sc1
	s_nop 1
	v_add_u32_e32 v10, 6, v8
	v_ashrrev_i32_e32 v11, 31, v10
	v_lshlrev_b64 v[10:11], 12, v[10:11]
	v_lshl_add_u64 v[10:11], s[18:19], 0, v[10:11]
	v_lshl_add_u64 v[10:11], v[10:11], 0, s[22:23]
	v_lshl_add_u64 v[10:11], v[10:11], 0, v[146:147]
	ds_read_b128 v[2:5], v6 offset:3168
	s_waitcnt lgkmcnt(0)
	global_store_dwordx4 v[10:11], v[2:5], off sc1
	s_nop 1
	v_add_u32_e32 v10, 8, v8
	v_ashrrev_i32_e32 v11, 31, v10
	v_lshlrev_b64 v[10:11], 12, v[10:11]
	v_lshl_add_u64 v[10:11], s[18:19], 0, v[10:11]
	v_lshl_add_u64 v[10:11], v[10:11], 0, s[22:23]
	v_lshl_add_u64 v[10:11], v[10:11], 0, v[146:147]
	ds_read_b128 v[2:5], v6 offset:4224
	s_waitcnt lgkmcnt(0)
	global_store_dwordx4 v[10:11], v[2:5], off sc1
	s_nop 1
	v_add_u32_e32 v10, 10, v8
	v_ashrrev_i32_e32 v11, 31, v10
	v_lshlrev_b64 v[10:11], 12, v[10:11]
	v_lshl_add_u64 v[10:11], s[18:19], 0, v[10:11]
	v_lshl_add_u64 v[10:11], v[10:11], 0, s[22:23]
	v_lshl_add_u64 v[10:11], v[10:11], 0, v[146:147]
	ds_read_b128 v[2:5], v6 offset:5280
	s_waitcnt lgkmcnt(0)
	global_store_dwordx4 v[10:11], v[2:5], off sc1
	s_nop 1
	v_add_u32_e32 v10, 12, v8
	v_ashrrev_i32_e32 v11, 31, v10
	v_lshlrev_b64 v[10:11], 12, v[10:11]
	v_lshl_add_u64 v[10:11], s[18:19], 0, v[10:11]
	v_lshl_add_u64 v[10:11], v[10:11], 0, s[22:23]
	v_lshl_add_u64 v[10:11], v[10:11], 0, v[146:147]
	ds_read_b128 v[2:5], v6 offset:6336
	s_waitcnt lgkmcnt(0)
	global_store_dwordx4 v[10:11], v[2:5], off sc1
	s_nop 1
	v_add_u32_e32 v10, 14, v8
	v_ashrrev_i32_e32 v11, 31, v10
	v_lshlrev_b64 v[10:11], 12, v[10:11]
	v_lshl_add_u64 v[10:11], s[18:19], 0, v[10:11]
	v_lshl_add_u64 v[10:11], v[10:11], 0, s[22:23]
	v_lshl_add_u64 v[10:11], v[10:11], 0, v[146:147]
	ds_read_b128 v[2:5], v6 offset:7392
	s_waitcnt lgkmcnt(0)
	global_store_dwordx4 v[10:11], v[2:5], off sc1
	s_nop 1
	v_add_u32_e32 v10, 16, v8
	v_ashrrev_i32_e32 v11, 31, v10
	v_lshlrev_b64 v[10:11], 12, v[10:11]
	v_lshl_add_u64 v[10:11], s[18:19], 0, v[10:11]
	v_lshl_add_u64 v[10:11], v[10:11], 0, s[22:23]
	v_lshl_add_u64 v[10:11], v[10:11], 0, v[146:147]
	ds_read_b128 v[2:5], v6 offset:8448
	s_waitcnt lgkmcnt(0)
	global_store_dwordx4 v[10:11], v[2:5], off sc1
	s_nop 1
	v_add_u32_e32 v10, 18, v8
	v_ashrrev_i32_e32 v11, 31, v10
	v_lshlrev_b64 v[10:11], 12, v[10:11]
	v_lshl_add_u64 v[10:11], s[18:19], 0, v[10:11]
	v_lshl_add_u64 v[10:11], v[10:11], 0, s[22:23]
	v_lshl_add_u64 v[10:11], v[10:11], 0, v[146:147]
	ds_read_b128 v[2:5], v6 offset:9504
	s_waitcnt lgkmcnt(0)
	global_store_dwordx4 v[10:11], v[2:5], off sc1
	s_nop 1
	v_add_u32_e32 v10, 20, v8
	v_ashrrev_i32_e32 v11, 31, v10
	v_lshlrev_b64 v[10:11], 12, v[10:11]
	v_lshl_add_u64 v[10:11], s[18:19], 0, v[10:11]
	v_lshl_add_u64 v[10:11], v[10:11], 0, s[22:23]
	v_lshl_add_u64 v[10:11], v[10:11], 0, v[146:147]
	ds_read_b128 v[2:5], v6 offset:10560
	s_waitcnt lgkmcnt(0)
	global_store_dwordx4 v[10:11], v[2:5], off sc1
	s_nop 1
	v_add_u32_e32 v10, 22, v8
	v_ashrrev_i32_e32 v11, 31, v10
	v_lshlrev_b64 v[10:11], 12, v[10:11]
	v_lshl_add_u64 v[10:11], s[18:19], 0, v[10:11]
	v_lshl_add_u64 v[10:11], v[10:11], 0, s[22:23]
	v_lshl_add_u64 v[10:11], v[10:11], 0, v[146:147]
	ds_read_b128 v[2:5], v6 offset:11616
	s_waitcnt lgkmcnt(0)
	global_store_dwordx4 v[10:11], v[2:5], off sc1
	s_nop 1
	v_add_u32_e32 v10, 24, v8
	v_ashrrev_i32_e32 v11, 31, v10
	v_lshlrev_b64 v[10:11], 12, v[10:11]
	v_lshl_add_u64 v[10:11], s[18:19], 0, v[10:11]
	v_lshl_add_u64 v[10:11], v[10:11], 0, s[22:23]
	v_lshl_add_u64 v[10:11], v[10:11], 0, v[146:147]
	ds_read_b128 v[2:5], v6 offset:12672
	s_waitcnt lgkmcnt(0)
	global_store_dwordx4 v[10:11], v[2:5], off sc1
	s_nop 1
	v_add_u32_e32 v10, 26, v8
	v_ashrrev_i32_e32 v11, 31, v10
	v_lshlrev_b64 v[10:11], 12, v[10:11]
	v_lshl_add_u64 v[10:11], s[18:19], 0, v[10:11]
	v_lshl_add_u64 v[10:11], v[10:11], 0, s[22:23]
	v_lshl_add_u64 v[10:11], v[10:11], 0, v[146:147]
	ds_read_b128 v[2:5], v6 offset:13728
	s_waitcnt lgkmcnt(0)
	global_store_dwordx4 v[10:11], v[2:5], off sc1
	s_nop 1
	v_add_u32_e32 v10, 28, v8
	v_ashrrev_i32_e32 v11, 31, v10
	v_lshlrev_b64 v[10:11], 12, v[10:11]
	v_lshl_add_u64 v[10:11], s[18:19], 0, v[10:11]
	v_lshl_add_u64 v[10:11], v[10:11], 0, s[22:23]
	ds_read_b128 v[2:5], v6 offset:14784
	v_lshl_add_u64 v[10:11], v[10:11], 0, v[146:147]
	s_waitcnt lgkmcnt(0)
	global_store_dwordx4 v[10:11], v[2:5], off sc1
	s_nop 1
	ds_read_b128 v[2:5], v6 offset:15840
	v_add_u32_e32 v6, 30, v8
	v_ashrrev_i32_e32 v7, 31, v6
	v_lshlrev_b64 v[6:7], 12, v[6:7]
	v_lshl_add_u64 v[6:7], s[18:19], 0, v[6:7]
	v_lshl_add_u64 v[6:7], v[6:7], 0, s[22:23]
	v_lshl_add_u64 v[6:7], v[6:7], 0, v[146:147]
	s_waitcnt lgkmcnt(0)
	global_store_dwordx4 v[6:7], v[2:5], off sc1
	s_nop 1
	s_waitcnt lgkmcnt(0)
	s_barrier
	s_cbranch_vccnz .LBB0_1127
	s_waitcnt vmcnt(0)
	s_barrier
	s_and_saveexec_b64 s[4:5], s[0:1]
	s_cbranch_execz .LBB0_1126
	s_mov_b64 s[6:7], exec
	v_mbcnt_lo_u32_b32 v2, s6, 0
	v_mbcnt_hi_u32_b32 v2, s7, v2
	v_cmp_eq_u32_e32 vcc, 0, v2
	s_and_b64 s[22:23], exec, vcc
	s_mov_b64 exec, s[22:23]
	s_cbranch_execz .LBB0_1126
	s_lshl_b32 s22, s37, 4
	s_ashr_i32 s23, s22, 31
	s_lshl_b64 s[22:23], s[22:23], 2
	s_add_u32 s22, s29, s22
	s_addc_u32 s23, s30, s23
	s_bcnt1_i32_b64 s6, s[6:7]
	v_mov_b32_e32 v2, s6
	global_atomic_add v147, v2, s[22:23]
	s_branch .LBB0_1126
